# SGU unit: XOR swizzle of the transposed Vl LDS tile (column group ^= row>>3) removes the 16-way bank conflict of the ds_write_b16 scatter
# baseline (speedup 1.0000x reference)
;     __device__ __forceinline__ void init(const void* A_, const void* B_, int G_, int c_) { T.init(A_, B_, DM, DM, NLAT / 256, INP / 256, 1, 0, 0, G_, c_, 0); }
; __device__ __forceinline__ void sgu_unit(const Params& p, int l, int un, LAS unsigned char* lds) {
;     ...
;     const float* Wg = p.in[I_SGUW] + ((size_t)l * 4 + h) * 128 * 128;
;     f32x4 wq[8]; u32x4 vv[16];
; #pragma unroll
;     for (int i = 0; i < 8; ++i) wq[i] = *(const f32x4*)(Wg + (i * 512 + tid) * 4);
; #pragma unroll
;     for (int qi = 0; qi < 16; ++qi) vv[qi] = *(const u32x4*)(P + (size_t)(row0 + wave * 16 + qi) * INP + C_SGU_V + lane * 8);
; __global__ void __launch_bounds__(512, 2) fwd(Params p) {
;     ...
;             { pg8::TileSched S; S.init(ws + WS_UPK, (bf16_t*)(ws + WS_G2B) + (size_t)l * 32 * 256 * 512, 512, 512, 3, 1, 32, (size_t)768 * 512 * 2, (size_t)256 * 512 * 2, G, c, (l == 0 && G == 256) ? 32 : 0);
;               pg8::EpiS2 E{(bf16_t*)(ws + WS_GB)};
;               pg8::Unit u0; if (S.next(0, u0)) { carry_wait(p, l); pg8::gemm_phase(lds, pg8::Desc{512, 512, 512}, S, E); }
;               else if (G == 256) { const int un = c - (l == 0 ? 128 : 96); if (un >= 0) sgu_unit(p, l, un, lds); } }
.LBB0_1258:
	v_readlane_b32 s0, v251, 50
	v_readlane_b32 s2, v252, 20
	v_readlane_b32 s1, v251, 51
	v_readlane_b32 s3, v252, 21
	s_and_b64 s[0:1], s[0:1], s[2:3]
	s_and_b64 s[0:1], s[0:1], exec
	s_cselect_b32 s0, 32, 0
	v_readlane_b32 s2, v255, 11
	s_mul_hi_u32 s1, s0, s2
	v_readlane_b32 s3, v255, 12
	s_mul_i32 s1, s1, s3
	s_sub_i32 s0, s0, s1
	s_sub_i32 s1, s0, s3
	s_cmp_ge_u32 s0, s3
	s_cselect_b32 s0, s1, s0
	s_sub_i32 s1, s0, s3
	s_cmp_ge_u32 s0, s3
	s_cselect_b32 s0, s1, s0
	v_readlane_b32 s1, v255, 42
	s_sub_i32 s0, s1, s0
	s_ashr_i32 s1, s0, 31
	s_abs_i32 s0, s0
	s_mul_hi_u32 s2, s0, s2
	s_mul_i32 s2, s2, s3
	s_sub_i32 s0, s0, s2
	s_sub_i32 s2, s0, s3
	s_cmp_ge_u32 s0, s3
	s_cselect_b32 s0, s2, s0
	s_sub_i32 s2, s0, s3
	s_cmp_ge_u32 s0, s3
	s_cselect_b32 s0, s2, s0
	s_xor_b32 s0, s0, s1
	s_sub_i32 s26, s0, s1
	s_cmpk_gt_i32 s26, 0x5f
	s_mov_b64 s[0:1], -1
	s_barrier
	s_cbranch_scc0 .LBB0_1294
	v_readlane_b32 s0, v252, 20
	v_readlane_b32 s1, v252, 21
	s_and_b64 s[0:1], s[0:1], exec
	s_movk_i32 s0, 0xff80
	s_cselect_b32 s0, s0, 0xffffffa0
	s_add_i32 s0, s0, s92
	v_readlane_b32 s12, v251, 50
	s_cmp_lt_i32 s0, 0
	v_readlane_b32 s13, v251, 51
	s_cselect_b64 s[2:3], -1, 0
	s_xor_b64 s[12:13], s[12:13], -1
	s_or_b64 s[2:3], s[2:3], s[12:13]
	s_and_b64 vcc, exec, s[2:3]
	s_cbranch_vccnz .LBB0_1293
	v_readlane_b32 s2, v252, 5
	v_readlane_b32 s44, v251, 16
	s_lshl_b32 s1, s0, 5
	s_lshl_b32 s0, s2, 9
	v_readlane_b32 s2, v253, 39
	v_readlane_b32 s48, v251, 20
	v_readlane_b32 s49, v251, 21
	v_readlane_b32 s3, v252, 6
	s_or_b32 s40, s0, s2
	s_mov_b32 s41, s5
	v_readlane_b32 s50, v251, 22
	v_readlane_b32 s51, v251, 23
	v_readlane_b32 s52, v251, 24
	v_readlane_b32 s53, v251, 25
	v_readlane_b32 s54, v251, 26
	v_readlane_b32 s55, v251, 27
	s_mov_b64 s[12:13], s[48:49]
	s_lshl_b64 s[2:3], s[40:41], 9
	s_mov_b64 s[14:15], s[50:51]
	v_mov_b32_e32 v64, v0
	s_add_u32 s2, s14, s2
	s_addc_u32 s3, s15, s3
	v_lshlrev_b32_e32 v2, 2, v64
	v_ashrrev_i32_e32 v3, 31, v2
	v_add_u32_e32 v62, 0x800, v2
	s_mov_b64 s[14:15], 0
	v_lshl_add_u64 v[4:5], v[2:3], 2, s[2:3]
	v_ashrrev_i32_e32 v63, 31, v62
	v_lshl_add_u64 v[6:7], v[62:63], 2, s[2:3]
	global_load_dwordx4 v[66:69], v[4:5], off
	global_load_dwordx4 v[70:73], v[6:7], off
	v_add_u32_e32 v102, 0x1000, v2
	v_ashrrev_i32_e32 v103, 31, v102
	v_add_u32_e32 v104, 0x1800, v2
	v_lshl_add_u64 v[4:5], v[102:103], 2, s[2:3]
	v_ashrrev_i32_e32 v105, 31, v104
	s_and_b32 s12, s1, 0x7fffff80
	s_mov_b32 s1, s5
	v_lshl_add_u64 v[6:7], v[104:105], 2, s[2:3]
	global_load_dwordx4 v[74:77], v[4:5], off
	global_load_dwordx4 v[78:81], v[6:7], off
	s_lshl_b64 s[0:1], s[0:1], 2
	v_readlane_b32 s13, v253, 41
	v_add_u32_e32 v106, 0x2000, v2
	s_add_u32 s0, s13, s0
	v_readlane_b32 s13, v253, 42
	v_ashrrev_i32_e32 v107, 31, v106
	v_add_u32_e32 v108, 0x2800, v2
	s_addc_u32 s1, s13, s1
	v_lshl_add_u64 v[4:5], v[106:107], 2, s[2:3]
	v_ashrrev_i32_e32 v109, 31, v108
	s_add_u32 s36, s84, s14
	v_lshl_add_u64 v[6:7], v[108:109], 2, s[2:3]
	global_load_dwordx4 v[82:85], v[4:5], off
	global_load_dwordx4 v[86:89], v[6:7], off
	s_addc_u32 s37, s85, s15
	v_add_u32_e32 v110, 0x3000, v2
	v_add_u32_e32 v112, 0x3800, v2
	s_add_u32 s38, s36, 0x1f1b8000
	v_ashrrev_i32_e32 v111, 31, v110
	v_ashrrev_i32_e32 v113, 31, v112
	v_ashrrev_i32_e32 v103, 6, v64
	s_addc_u32 s39, s37, 0
	v_lshl_add_u64 v[4:5], v[110:111], 2, s[2:3]
	v_lshl_add_u64 v[2:3], v[112:113], 2, s[2:3]
	v_lshlrev_b32_e32 v65, 4, v103
	v_and_b32_e32 v8, 63, v64
	global_load_dwordx4 v[90:93], v[4:5], off
	global_load_dwordx4 v[94:97], v[2:3], off
	v_add_u32_e32 v9, s12, v65
	v_mov_b64_e32 v[2:3], s[38:39]
	s_movk_i32 s13, 0x1e00
	v_mad_i64_i32 v[4:5], s[2:3], v9, s13, v[2:3]
	v_lshlrev_b32_e32 v206, 4, v8
	v_or_b32_e32 v6, 1, v9
	v_lshl_add_u64 v[4:5], v[4:5], 0, v[206:207]
	v_mad_i64_i32 v[6:7], s[2:3], v6, s13, v[2:3]
	v_lshl_add_u64 v[6:7], v[6:7], 0, v[206:207]
	global_load_dwordx4 v[98:101], v[4:5], off offset:1024
	global_load_dwordx4 v[58:61], v[6:7], off offset:1024
	v_or_b32_e32 v4, 2, v9
	v_or_b32_e32 v6, 3, v9
	v_mad_i64_i32 v[4:5], s[2:3], v4, s13, v[2:3]
	v_mad_i64_i32 v[6:7], s[2:3], v6, s13, v[2:3]
	v_lshl_add_u64 v[4:5], v[4:5], 0, v[206:207]
	v_lshl_add_u64 v[6:7], v[6:7], 0, v[206:207]
	global_load_dwordx4 v[54:57], v[4:5], off offset:1024
	global_load_dwordx4 v[50:53], v[6:7], off offset:1024
	v_or_b32_e32 v4, 4, v9
	v_or_b32_e32 v6, 5, v9
	v_mad_i64_i32 v[4:5], s[2:3], v4, s13, v[2:3]
	v_mad_i64_i32 v[6:7], s[2:3], v6, s13, v[2:3]
	v_lshl_add_u64 v[4:5], v[4:5], 0, v[206:207]
	v_lshl_add_u64 v[6:7], v[6:7], 0, v[206:207]
	global_load_dwordx4 v[46:49], v[4:5], off offset:1024
	global_load_dwordx4 v[42:45], v[6:7], off offset:1024
	v_or_b32_e32 v4, 6, v9
	v_or_b32_e32 v6, 7, v9
	v_mad_i64_i32 v[4:5], s[2:3], v4, s13, v[2:3]
	v_mad_i64_i32 v[6:7], s[2:3], v6, s13, v[2:3]
	v_lshl_add_u64 v[4:5], v[4:5], 0, v[206:207]
	v_lshl_add_u64 v[6:7], v[6:7], 0, v[206:207]
	global_load_dwordx4 v[38:41], v[4:5], off offset:1024
	global_load_dwordx4 v[34:37], v[6:7], off offset:1024
	v_or_b32_e32 v4, 8, v9
	v_or_b32_e32 v6, 9, v9
	v_mad_i64_i32 v[4:5], s[2:3], v4, s13, v[2:3]
	v_mad_i64_i32 v[6:7], s[2:3], v6, s13, v[2:3]
	v_lshl_add_u64 v[4:5], v[4:5], 0, v[206:207]
	v_lshl_add_u64 v[6:7], v[6:7], 0, v[206:207]
	global_load_dwordx4 v[30:33], v[4:5], off offset:1024
	global_load_dwordx4 v[26:29], v[6:7], off offset:1024
	v_or_b32_e32 v4, 10, v9
	v_or_b32_e32 v6, 11, v9
	v_mad_i64_i32 v[4:5], s[2:3], v4, s13, v[2:3]
	v_mad_i64_i32 v[6:7], s[2:3], v6, s13, v[2:3]
	v_lshl_add_u64 v[4:5], v[4:5], 0, v[206:207]
	v_lshl_add_u64 v[6:7], v[6:7], 0, v[206:207]
	global_load_dwordx4 v[22:25], v[4:5], off offset:1024
	global_load_dwordx4 v[18:21], v[6:7], off offset:1024
	v_or_b32_e32 v4, 12, v9
	v_or_b32_e32 v6, 13, v9
	v_mad_i64_i32 v[4:5], s[2:3], v4, s13, v[2:3]
	v_mad_i64_i32 v[6:7], s[2:3], v6, s13, v[2:3]
	v_lshl_add_u64 v[4:5], v[4:5], 0, v[206:207]
	v_lshl_add_u64 v[6:7], v[6:7], 0, v[206:207]
	v_lshlrev_b32_e32 v105, 3, v64
	global_load_dwordx4 v[14:17], v[4:5], off offset:1024
	global_load_dwordx4 v[10:13], v[6:7], off offset:1024
	v_or_b32_e32 v4, 14, v9
	v_or_b32_e32 v6, 15, v9
	v_and_b32_e32 v63, 0xf8, v105
	v_mad_i64_i32 v[4:5], s[2:3], v4, s13, v[2:3]
	v_mad_i64_i32 v[2:3], s[2:3], v6, s13, v[2:3]
	v_add_u32_e32 v114, 0, v63
	v_bfe_i32 v63, v64, 5, 25
	s_movk_i32 s13, 0x110
	v_lshl_add_u64 v[4:5], v[4:5], 0, v[206:207]
	v_lshl_add_u64 v[2:3], v[2:3], 0, v[206:207]
	s_waitcnt vmcnt(21)
; #define LAS __attribute__((address_space(3)))
; __device__ __forceinline__ unsigned cvt_pk_bf16(float lo, float hi) { const f32x2 v = {lo, hi}; const bf16x2_t b = __builtin_convertvector(v, bf16x2_t); return __builtin_bit_cast(unsigned, b); }
; __device__ __forceinline__ float bflo(unsigned w) { return __uint_as_float(w << 16); }
; __device__ __forceinline__ float bfhi(unsigned w) { return __uint_as_float(w & 0xffff0000u); }
; __device__ __forceinline__ unsigned short f2bf(float f) { return (unsigned short)(cvt_pk_bf16(f, 0.f) & 0xffffu); }
; __device__ __forceinline__ void sgu_unit(const Params& p, int l, int un, LAS unsigned char* lds) {
;     ...
;     for (int i = 0; i < 8; ++i) { const int e4 = (i * 512 + tid) * 4, r = e4 >> 7, c = e4 & 127; const f32x4 v = wq[i];
;         u32x2 w; w.x = cvt_pk_bf16(v[0], v[1]); w.y = cvt_pk_bf16(v[2], v[3]); *(LAS u32x2*)(Wl + r * 136 + c) = w; }
; #pragma unroll
;     for (int qi = 0; qi < 16; ++qi) { const int q = wave * 16 + qi;
;         const u32x4 v = vv[qi]; float f[8] = {bflo(v.x), bfhi(v.x), bflo(v.y), bfhi(v.y), bflo(v.z), bfhi(v.z), bflo(v.w), bfhi(v.w)}; float ss = 0.f;
; #pragma unroll
;         for (int j = 0; j < 8; ++j) { f[j] = gelu_tanh(f[j]); ss += f[j] * f[j]; }
;         ss = wave_sum(ss); const float rinv = rsqrtf(ss * (1.0f / 512.0f) + EPS);
;     ...
;             for (int j = 0; j < 8; ++j) Vl[(c0 + j) * 136 + q] = f2bf(f[j] * rinv * g[j]); } }
	v_cvt_pk_bf16_f32 v66, v66, v67
	v_cvt_pk_bf16_f32 v67, v68, v69
	v_mad_u64_u32 v[68:69], s[2:3], v63, s13, v[114:115]
	global_load_dwordx4 v[6:9], v[4:5], off offset:1024
	s_nop 0
	global_load_dwordx4 v[2:5], v[2:3], off offset:1024
	ds_write_b64 v68, v[66:67]
	v_ashrrev_i32_e32 v66, 7, v62
	s_waitcnt vmcnt(22)
	v_cvt_pk_bf16_f32 v62, v70, v71
	v_cvt_pk_bf16_f32 v63, v72, v73
	v_mad_u64_u32 v[66:67], s[2:3], v66, s13, v[114:115]
	ds_write_b64 v66, v[62:63]
	v_ashrrev_i32_e32 v66, 7, v102
	s_waitcnt vmcnt(21)
	v_cvt_pk_bf16_f32 v62, v74, v75
	v_cvt_pk_bf16_f32 v63, v76, v77
	v_mad_u64_u32 v[66:67], s[2:3], v66, s13, v[114:115]
	ds_write_b64 v66, v[62:63]
	v_ashrrev_i32_e32 v66, 7, v104
	s_waitcnt vmcnt(20)
	v_cvt_pk_bf16_f32 v62, v78, v79
	v_cvt_pk_bf16_f32 v63, v80, v81
	v_mad_u64_u32 v[66:67], s[2:3], v66, s13, v[114:115]
	ds_write_b64 v66, v[62:63]
	v_ashrrev_i32_e32 v66, 7, v106
	s_waitcnt vmcnt(19)
	v_cvt_pk_bf16_f32 v62, v82, v83
	v_cvt_pk_bf16_f32 v63, v84, v85
	v_mad_u64_u32 v[66:67], s[2:3], v66, s13, v[114:115]
	ds_write_b64 v66, v[62:63]
	v_ashrrev_i32_e32 v66, 7, v108
	s_waitcnt vmcnt(18)
	v_cvt_pk_bf16_f32 v62, v86, v87
	v_cvt_pk_bf16_f32 v63, v88, v89
	v_mad_u64_u32 v[66:67], s[2:3], v66, s13, v[114:115]
	ds_write_b64 v66, v[62:63]
	v_ashrrev_i32_e32 v66, 7, v110
	s_waitcnt vmcnt(17)
	v_cvt_pk_bf16_f32 v62, v90, v91
	v_cvt_pk_bf16_f32 v63, v92, v93
	v_mad_u64_u32 v[66:67], s[2:3], v66, s13, v[114:115]
	ds_write_b64 v66, v[62:63]
	v_ashrrev_i32_e32 v66, 7, v112
	v_mad_u64_u32 v[66:67], s[2:3], v66, s13, v[114:115]
	s_waitcnt vmcnt(15)
	v_and_b32_e32 v67, 0xffff0000, v98
	v_mul_f32_e32 v73, 0x3dd2d3e8, v67
	v_fma_f32 v73, -v73, v67, s33
	v_mul_f32_e32 v73, v73, v67
	v_exp_f32_e32 v73, v73
	v_cvt_pk_bf16_f32 v62, v94, v95
	v_cvt_pk_bf16_f32 v63, v96, v97
	ds_write_b64 v66, v[62:63]
	v_lshlrev_b32_e32 v66, 16, v98
	v_add_f32_e32 v73, 1.0, v73
	v_mul_f32_e32 v72, 0x3dd2d3e8, v66
	v_rcp_f32_e32 v73, v73
	v_fma_f32 v72, -v72, v66, s33
	v_mul_f32_e32 v72, v72, v66
	v_lshlrev_b32_e32 v69, 16, v99
	v_exp_f32_e32 v72, v72
	v_mul_f32_e32 v79, v73, v67
	v_mul_f32_e32 v67, 0x3dd2d3e8, v69
	v_fma_f32 v67, -v67, v69, s33
	v_mul_f32_e32 v67, v67, v69
	v_add_f32_e32 v72, 1.0, v72
	v_exp_f32_e32 v67, v67
	v_rcp_f32_e32 v72, v72
	v_lshlrev_b32_e32 v71, 16, v100
	v_and_b32_e32 v70, 0xffff0000, v99
	v_add_f32_e32 v67, 1.0, v67
	v_mul_f32_e32 v73, 0x3dd2d3e8, v71
	v_mul_f32_e32 v81, v72, v66
	v_mul_f32_e32 v72, 0x3dd2d3e8, v70
	v_rcp_f32_e32 v67, v67
	v_fma_f32 v73, -v73, v71, s33
	v_fma_f32 v72, -v72, v70, s33
	v_mul_f32_e32 v73, v73, v71
	v_mul_f32_e32 v72, v72, v70
	v_exp_f32_e32 v73, v73
	v_and_b32_e32 v74, 0xffff0000, v100
	v_exp_f32_e32 v72, v72
	v_mul_f32_e32 v80, v67, v69
	v_mul_f32_e32 v69, 0x3dd2d3e8, v74
	v_fma_f32 v69, -v69, v74, s33
	v_add_f32_e32 v67, 1.0, v73
	v_mul_f32_e32 v69, v69, v74
	v_add_f32_e32 v72, 1.0, v72
	v_rcp_f32_e32 v67, v67
	v_exp_f32_e32 v69, v69
	v_rcp_f32_e32 v72, v72
	v_lshlrev_b32_e32 v75, 16, v101
	v_and_b32_e32 v82, 0xffff0000, v101
	v_mul_f32_e32 v76, v67, v71
	v_add_f32_e32 v67, 1.0, v69
	v_mul_f32_e32 v69, 0x3dd2d3e8, v75
	v_mul_f32_e32 v78, v72, v70
	v_fma_f32 v69, -v69, v75, s33
	v_mul_f32_e32 v70, 0x3dd2d3e8, v82
	v_mul_f32_e32 v69, v69, v75
	v_fma_f32 v70, -v70, v82, s33
	v_rcp_f32_e32 v67, v67
	v_exp_f32_e32 v69, v69
	v_mul_f32_e32 v70, v70, v82
	v_exp_f32_e32 v70, v70
	v_mul_f32_e32 v66, v79, v79
	v_mul_f32_e32 v77, v67, v74
	v_add_f32_e32 v67, 1.0, v69
	v_fmac_f32_e32 v66, v81, v81
	v_rcp_f32_e32 v67, v67
	v_add_f32_e32 v69, 1.0, v70
	v_fmac_f32_e32 v66, v80, v80
	v_rcp_f32_e32 v69, v69
	v_and_b32_e32 v62, 64, v249
	v_fmac_f32_e32 v66, v78, v78
	v_add_u32_e32 v62, 64, v62
	v_xor_b32_e32 v63, 32, v249
	v_fmac_f32_e32 v66, v76, v76
	v_cmp_lt_i32_e32 vcc, v63, v62
	v_fmac_f32_e32 v66, v77, v77
	v_mul_f32_e32 v75, v67, v75
	v_cndmask_b32_e32 v63, v249, v63, vcc
	v_fmac_f32_e32 v66, v75, v75
	v_mul_f32_e32 v74, v69, v82
	v_lshlrev_b32_e32 v68, 2, v63
	v_fmac_f32_e32 v66, v74, v74
	v_mov_b32_e32 v67, v66
	s_nop 1
	v_permlane32_swap_b32_e32 v67, v66
	v_xor_b32_e32 v63, 16, v249
	v_cmp_lt_i32_e32 vcc, v63, v62
	v_and_b32_e32 v84, 0x78, v105
	v_readlane_b32 s2, v253, 40
	v_cndmask_b32_e32 v63, v249, v63, vcc
	v_lshlrev_b32_e32 v69, 2, v63
	s_waitcnt lgkmcnt(0)
	v_add_f32_e32 v66, v66, v67
	v_mov_b32_e32 v67, v66
	s_nop 1
	v_permlane16_swap_b32_e32 v67, v66
	v_xor_b32_e32 v63, 8, v249
	v_cmp_lt_i32_e32 vcc, v63, v62
	v_lshlrev_b32_e32 v206, 2, v84
	v_readlane_b32 s45, v251, 17
	v_cndmask_b32_e32 v63, v249, v63, vcc
	v_lshlrev_b32_e32 v70, 2, v63
	s_waitcnt lgkmcnt(0)
	v_add_f32_e32 v66, v66, v67
	s_nop 1
	v_mov_b32_dpp v67, v66 row_ror:8 row_mask:0xf bank_mask:0xf
	v_xor_b32_e32 v63, 4, v249
	v_cmp_lt_i32_e32 vcc, v63, v62
	v_readlane_b32 s46, v251, 18
	v_readlane_b32 s47, v251, 19
	v_cndmask_b32_e32 v63, v249, v63, vcc
	v_lshlrev_b32_e32 v71, 2, v63
	s_waitcnt lgkmcnt(0)
	v_add_f32_e32 v66, v66, v67
	v_xor_b32_e32 v63, 2, v249
	s_nop 1
	v_mov_b32_dpp v67, v66 row_shl:4 row_mask:0xf bank_mask:0x5
	v_mov_b32_dpp v67, v66 row_shr:4 row_mask:0xf bank_mask:0xa
	v_cmp_lt_i32_e32 vcc, v63, v62
	v_readlane_b32 s56, v251, 28
	v_readlane_b32 s57, v251, 29
	v_cndmask_b32_e32 v63, v249, v63, vcc
	v_lshlrev_b32_e32 v72, 2, v63
	v_xor_b32_e32 v63, 1, v249
	v_cmp_lt_i32_e32 vcc, v63, v62
	v_readlane_b32 s58, v251, 30
	v_readlane_b32 s59, v251, 31
	v_cndmask_b32_e32 v62, v249, v63, vcc
	s_waitcnt lgkmcnt(0)
	v_add_f32_e32 v63, v66, v67
	s_nop 1
	v_mov_b32_dpp v67, v63 quad_perm:[2,3,0,1] row_mask:0xf bank_mask:0xf
	v_lshlrev_b32_e32 v73, 2, v62
	v_bfe_u32 v66, v64, 4, 2
	v_cmp_eq_u32_e32 vcc, s2, v66
	s_mov_b64 s[16:17], s[52:53]
	s_waitcnt lgkmcnt(0)
	v_add_f32_e32 v82, v63, v67
	s_nop 1
	v_mov_b32_dpp v83, v82 quad_perm:[1,0,3,2] row_mask:0xf bank_mask:0xf
	v_lshl_add_u32 v67, v103, 5, 0
	v_lshl_add_u64 v[62:63], s[0:1], 0, v[206:207]
	v_mad_u32_u24 v67, v84, s13, v67
	v_lshrrev_b32_e32 v170, 6, v0
	v_lshlrev_b32_e32 v170, 1, v170
	v_and_b32_e32 v171, 15, v0
	v_xor_b32_e32 v168, v170, v171
	v_sub_u32_e32 v168, v168, v170
	v_lshl_add_u32 v168, v168, 4, v67
	v_or_b32_e32 v170, 1, v170
	v_xor_b32_e32 v169, v170, v171
	v_sub_u32_e32 v169, v169, v170
	v_lshl_add_u32 v169, v169, 4, v67
	s_mov_b64 s[18:19], s[54:55]
	s_and_saveexec_b64 s[0:1], vcc
	s_cbranch_execz .LBB0_1262
; __device__ __forceinline__ float bflo(unsigned w) { return __uint_as_float(w << 16); }
; __device__ __forceinline__ float bfhi(unsigned w) { return __uint_as_float(w & 0xffff0000u); }
; __device__ __forceinline__ unsigned short f2bf(float f) { return (unsigned short)(cvt_pk_bf16(f, 0.f) & 0xffffu); }
; __device__ __forceinline__ void sgu_unit(const Params& p, int l, int un, LAS unsigned char* lds) {
;     ...
;     for (int qi = 0; qi < 16; ++qi) { const int q = wave * 16 + qi;
;         const u32x4 v = vv[qi]; float f[8] = {bflo(v.x), bfhi(v.x), bflo(v.y), bfhi(v.y), bflo(v.z), bfhi(v.z), bflo(v.w), bfhi(v.w)}; float ss = 0.f;
; #pragma unroll
;         for (int j = 0; j < 8; ++j) { f[j] = gelu_tanh(f[j]); ss += f[j] * f[j]; }
;         ss = wave_sum(ss); const float rinv = rsqrtf(ss * (1.0f / 512.0f) + EPS);
;         if ((lane >> 4) == h) { const int c0 = (lane & 15) * 8; const float* g = p.in[I_SGUNG] + l * 512 + h * 128 + c0;
; #pragma unroll
;             for (int j = 0; j < 8; ++j) Vl[(c0 + j) * 136 + q] = f2bf(f[j] * rinv * g[j]); } }
	s_waitcnt lgkmcnt(0)
	v_add_f32_e32 v82, v82, v83
	v_fmamk_f32 v82, v82, 0x3b000000, v246
	s_mov_b32 s2, 0x800000
	v_cmp_gt_f32_e64 s[2:3], s2, v82
	v_mul_f32_e32 v83, 0x4b800000, v82
	s_nop 0
	v_cndmask_b32_e64 v82, v82, v83, s[2:3]
	v_rsq_f32_e32 v82, v82
	s_nop 0
	v_mul_f32_e32 v83, 0x45800000, v82
	v_cndmask_b32_e64 v90, v82, v83, s[2:3]
	global_load_dwordx4 v[82:85], v[62:63], off offset:16
	global_load_dwordx4 v[86:89], v[62:63], off
	v_mul_f32_e32 v79, v79, v90
	v_mul_f32_e32 v76, v76, v90
	v_mul_f32_e32 v81, v81, v90
	v_mul_f32_e32 v78, v78, v90
	v_mul_f32_e32 v75, v75, v90
	v_mul_f32_e32 v74, v74, v90
	s_waitcnt vmcnt(1)
	v_mul_f32_e32 v76, v76, v82
	s_waitcnt vmcnt(0)
	v_mul_f32_e32 v79, v79, v87
	v_cvt_pk_bf16_f32 v79, v79, s0
	v_cvt_pk_bf16_f32 v76, v76, s0
	ds_write_b16 v168, v79 offset:35088
	v_mul_f32_e32 v79, v80, v90
	ds_write_b16 v168, v76 offset:35904
	v_mul_f32_e32 v76, v77, v90
	v_mul_f32_e32 v81, v81, v86
	v_mul_f32_e32 v79, v79, v88
	v_mul_f32_e32 v78, v78, v89
	v_mul_f32_e32 v76, v76, v83
	v_mul_f32_e32 v75, v75, v84
	v_mul_f32_e32 v74, v74, v85
	v_cvt_pk_bf16_f32 v81, v81, s0
	v_cvt_pk_bf16_f32 v79, v79, s0
	v_cvt_pk_bf16_f32 v78, v78, s0
	v_cvt_pk_bf16_f32 v76, v76, s0
	v_cvt_pk_bf16_f32 v75, v75, s0
	v_cvt_pk_bf16_f32 v74, v74, s0
	ds_write_b16 v168, v81 offset:34816
	ds_write_b16 v168, v79 offset:35360
	ds_write_b16 v168, v78 offset:35632
	ds_write_b16 v168, v76 offset:36176
	ds_write_b16 v168, v75 offset:36448
	ds_write_b16 v168, v74 offset:36720
.LBB0_1262:
	s_or_b64 exec, exec, s[0:1]
	s_waitcnt vmcnt(14)
	v_lshlrev_b32_e32 v74, 16, v58
	v_lshlrev_b32_e32 v75, 16, v59
	v_and_b32_e32 v77, 0xffff0000, v59
	v_mul_f32_e32 v59, 0x3dd2d3e8, v74
	v_fma_f32 v59, -v59, v74, s33
	v_mul_f32_e32 v59, v59, v74
	v_exp_f32_e32 v59, v59
	v_and_b32_e32 v58, 0xffff0000, v58
	v_lshlrev_b32_e32 v78, 16, v60
	v_and_b32_e32 v79, 0xffff0000, v60
	v_add_f32_e32 v59, 1.0, v59
	v_rcp_f32_e32 v59, v59
	v_mul_f32_e32 v60, 0x3dd2d3e8, v77
	v_fma_f32 v60, -v60, v77, s33
	v_mul_f32_e32 v60, v60, v77
	v_mul_f32_e32 v76, v59, v74
	v_mul_f32_e32 v59, 0x3dd2d3e8, v58
	v_fma_f32 v59, -v59, v58, s33
	v_mul_f32_e32 v59, v59, v58
	v_exp_f32_e32 v59, v59
	v_exp_f32_e32 v60, v60
	v_lshlrev_b32_e32 v80, 16, v61
	v_and_b32_e32 v81, 0xffff0000, v61
	v_add_f32_e32 v59, 1.0, v59
	v_rcp_f32_e32 v59, v59
	v_add_f32_e32 v60, 1.0, v60
	v_rcp_f32_e32 v60, v60
	v_mul_f32_e32 v61, 0x3dd2d3e8, v78
	v_mul_f32_e32 v59, v59, v58
	v_mul_f32_e32 v58, 0x3dd2d3e8, v75
	v_fma_f32 v58, -v58, v75, s33
	v_mul_f32_e32 v58, v58, v75
	v_exp_f32_e32 v58, v58
	v_fma_f32 v61, -v61, v78, s33
	v_mul_f32_e32 v74, 0x3dd2d3e8, v79
	v_mul_f32_e32 v61, v61, v78
	v_add_f32_e32 v58, 1.0, v58
	v_rcp_f32_e32 v58, v58
	v_fma_f32 v74, -v74, v79, s33
	v_mul_f32_e32 v60, v60, v77
	v_exp_f32_e32 v61, v61
	v_mul_f32_e32 v58, v58, v75
	v_mul_f32_e32 v75, 0x3dd2d3e8, v80
	v_mul_f32_e32 v74, v74, v79
	v_fma_f32 v75, -v75, v80, s33
	v_mul_f32_e32 v77, 0x3dd2d3e8, v81
	v_exp_f32_e32 v74, v74
	v_mul_f32_e32 v75, v75, v80
	v_fma_f32 v77, -v77, v81, s33
	v_exp_f32_e32 v75, v75
	v_mul_f32_e32 v77, v77, v81
	v_exp_f32_e32 v77, v77
	v_add_f32_e32 v61, 1.0, v61
	v_rcp_f32_e32 v61, v61
	v_add_f32_e32 v74, 1.0, v74
	v_mul_f32_e32 v82, v59, v59
	v_rcp_f32_e32 v74, v74
	v_add_f32_e32 v75, 1.0, v75
	v_fmac_f32_e32 v82, v76, v76
	v_rcp_f32_e32 v75, v75
	v_add_f32_e32 v77, 1.0, v77
	v_fmac_f32_e32 v82, v58, v58
	v_rcp_f32_e32 v77, v77
	v_fmac_f32_e32 v82, v60, v60
	v_mul_f32_e32 v61, v61, v78
	v_fmac_f32_e32 v82, v61, v61
	v_mul_f32_e32 v74, v74, v79
	v_fmac_f32_e32 v82, v74, v74
	v_mul_f32_e32 v75, v75, v80
	v_fmac_f32_e32 v82, v75, v75
	v_mul_f32_e32 v77, v77, v81
	v_fmac_f32_e32 v82, v77, v77
	ds_bpermute_b32 v78, v68, v82
	s_waitcnt lgkmcnt(0)
	v_add_f32_e32 v78, v82, v78
	v_mov_b32_e32 v79, v78
	s_nop 1
	v_permlane16_swap_b32_e32 v79, v78
	s_waitcnt lgkmcnt(0)
	v_add_f32_e32 v78, v78, v79
	s_nop 1
	v_mov_b32_dpp v79, v78 row_ror:8 row_mask:0xf bank_mask:0xf
	s_waitcnt lgkmcnt(0)
	v_add_f32_e32 v78, v78, v79
	s_nop 1
	v_mov_b32_dpp v79, v78 row_shl:4 row_mask:0xf bank_mask:0x5
	v_mov_b32_dpp v79, v78 row_shr:4 row_mask:0xf bank_mask:0xa
	s_waitcnt lgkmcnt(0)
	v_add_f32_e32 v78, v78, v79
	s_nop 1
	v_mov_b32_dpp v79, v78 quad_perm:[2,3,0,1] row_mask:0xf bank_mask:0xf
	s_waitcnt lgkmcnt(0)
	v_add_f32_e32 v78, v78, v79
	s_nop 1
	v_mov_b32_dpp v79, v78 quad_perm:[1,0,3,2] row_mask:0xf bank_mask:0xf
	s_and_saveexec_b64 s[0:1], vcc
	s_cbranch_execz .LBB0_1264
	s_waitcnt lgkmcnt(0)
	v_add_f32_e32 v78, v78, v79
	v_fmamk_f32 v78, v78, 0x3b000000, v246
	s_mov_b32 s2, 0x800000
	v_cmp_gt_f32_e64 s[2:3], s2, v78
	v_mul_f32_e32 v79, 0x4b800000, v78
	s_nop 0
	v_cndmask_b32_e64 v78, v78, v79, s[2:3]
	v_rsq_f32_e32 v78, v78
	s_nop 0
	v_mul_f32_e32 v79, 0x45800000, v78
	v_cndmask_b32_e64 v86, v78, v79, s[2:3]
	global_load_dwordx4 v[78:81], v[62:63], off offset:16
	global_load_dwordx4 v[82:85], v[62:63], off
	v_mul_f32_e32 v58, v58, v86
	v_mul_f32_e32 v76, v76, v86
	v_mul_f32_e32 v59, v59, v86
	s_waitcnt vmcnt(0)
	v_mul_f32_e32 v58, v58, v84
	v_cvt_pk_bf16_f32 v58, v58, s0
	ds_write_b16 v168, v58 offset:35362
	v_mul_f32_e32 v58, v60, v86
	v_mul_f32_e32 v58, v58, v85
	v_cvt_pk_bf16_f32 v58, v58, s0
	ds_write_b16 v168, v58 offset:35634
	v_mul_f32_e32 v58, v61, v86
	v_mul_f32_e32 v58, v58, v78
	v_cvt_pk_bf16_f32 v58, v58, s0
	ds_write_b16 v168, v58 offset:35906
	v_mul_f32_e32 v58, v74, v86
	v_mul_f32_e32 v58, v58, v79
	v_cvt_pk_bf16_f32 v58, v58, s0
	ds_write_b16 v168, v58 offset:36178
	v_mul_f32_e32 v58, v75, v86
	v_mul_f32_e32 v58, v58, v80
	v_cvt_pk_bf16_f32 v58, v58, s0
	ds_write_b16 v168, v58 offset:36450
	v_mul_f32_e32 v58, v77, v86
	v_mul_f32_e32 v76, v76, v82
	v_mul_f32_e32 v59, v59, v83
	v_mul_f32_e32 v58, v58, v81
	v_cvt_pk_bf16_f32 v76, v76, s0
	v_cvt_pk_bf16_f32 v59, v59, s0
	v_cvt_pk_bf16_f32 v58, v58, s0
	ds_write_b16 v168, v76 offset:34818
	ds_write_b16 v168, v59 offset:35090
	ds_write_b16 v168, v58 offset:36722
; __device__ __forceinline__ float bflo(unsigned w) { return __uint_as_float(w << 16); }
; __device__ __forceinline__ float bfhi(unsigned w) { return __uint_as_float(w & 0xffff0000u); }
; __device__ __forceinline__ unsigned short f2bf(float f) { return (unsigned short)(cvt_pk_bf16(f, 0.f) & 0xffffu); }
; __device__ __forceinline__ void sgu_unit(const Params& p, int l, int un, LAS unsigned char* lds) {
;     ...
;     for (int qi = 0; qi < 16; ++qi) { const int q = wave * 16 + qi;
;         const u32x4 v = vv[qi]; float f[8] = {bflo(v.x), bfhi(v.x), bflo(v.y), bfhi(v.y), bflo(v.z), bfhi(v.z), bflo(v.w), bfhi(v.w)}; float ss = 0.f;
; #pragma unroll
;         for (int j = 0; j < 8; ++j) { f[j] = gelu_tanh(f[j]); ss += f[j] * f[j]; }
;         ss = wave_sum(ss); const float rinv = rsqrtf(ss * (1.0f / 512.0f) + EPS);
;         if ((lane >> 4) == h) { const int c0 = (lane & 15) * 8; const float* g = p.in[I_SGUNG] + l * 512 + h * 128 + c0;
; #pragma unroll
;             for (int j = 0; j < 8; ++j) Vl[(c0 + j) * 136 + q] = f2bf(f[j] * rinv * g[j]); } }
.LBB0_1264:
	s_or_b64 exec, exec, s[0:1]
	s_waitcnt vmcnt(13)
	v_lshlrev_b32_e32 v58, 16, v54
	v_lshlrev_b32_e32 v59, 16, v55
	v_and_b32_e32 v61, 0xffff0000, v55
	v_mul_f32_e32 v55, 0x3dd2d3e8, v58
	v_fma_f32 v55, -v55, v58, s33
	v_mul_f32_e32 v55, v55, v58
	v_exp_f32_e32 v55, v55
	v_and_b32_e32 v54, 0xffff0000, v54
	v_lshlrev_b32_e32 v74, 16, v56
	v_and_b32_e32 v75, 0xffff0000, v56
	v_add_f32_e32 v55, 1.0, v55
	v_rcp_f32_e32 v55, v55
	v_mul_f32_e32 v56, 0x3dd2d3e8, v61
	v_fma_f32 v56, -v56, v61, s33
	v_mul_f32_e32 v56, v56, v61
	v_mul_f32_e32 v60, v55, v58
	v_mul_f32_e32 v55, 0x3dd2d3e8, v54
	v_fma_f32 v55, -v55, v54, s33
	v_mul_f32_e32 v55, v55, v54
	v_exp_f32_e32 v55, v55
	v_exp_f32_e32 v56, v56
	v_lshlrev_b32_e32 v76, 16, v57
	v_and_b32_e32 v77, 0xffff0000, v57
	v_add_f32_e32 v55, 1.0, v55
	v_rcp_f32_e32 v55, v55
	v_add_f32_e32 v56, 1.0, v56
	v_rcp_f32_e32 v56, v56
	v_mul_f32_e32 v57, 0x3dd2d3e8, v74
	v_mul_f32_e32 v55, v55, v54
	v_mul_f32_e32 v54, 0x3dd2d3e8, v59
	v_fma_f32 v54, -v54, v59, s33
	v_mul_f32_e32 v54, v54, v59
	v_exp_f32_e32 v54, v54
	v_fma_f32 v57, -v57, v74, s33
	v_mul_f32_e32 v58, 0x3dd2d3e8, v75
	v_mul_f32_e32 v57, v57, v74
	v_add_f32_e32 v54, 1.0, v54
	v_rcp_f32_e32 v54, v54
	v_fma_f32 v58, -v58, v75, s33
	v_mul_f32_e32 v56, v56, v61
	v_exp_f32_e32 v57, v57
	v_mul_f32_e32 v54, v54, v59
	v_mul_f32_e32 v59, 0x3dd2d3e8, v76
	v_mul_f32_e32 v58, v58, v75
	v_fma_f32 v59, -v59, v76, s33
	v_mul_f32_e32 v61, 0x3dd2d3e8, v77
	v_exp_f32_e32 v58, v58
	v_mul_f32_e32 v59, v59, v76
	v_fma_f32 v61, -v61, v77, s33
	v_exp_f32_e32 v59, v59
	v_mul_f32_e32 v61, v61, v77
	v_exp_f32_e32 v61, v61
	v_add_f32_e32 v57, 1.0, v57
	v_rcp_f32_e32 v57, v57
	v_add_f32_e32 v58, 1.0, v58
	v_mul_f32_e32 v78, v55, v55
	v_rcp_f32_e32 v58, v58
	v_add_f32_e32 v59, 1.0, v59
	v_fmac_f32_e32 v78, v60, v60
	v_rcp_f32_e32 v59, v59
	v_add_f32_e32 v61, 1.0, v61
	v_fmac_f32_e32 v78, v54, v54
	v_rcp_f32_e32 v61, v61
	v_fmac_f32_e32 v78, v56, v56
	v_mul_f32_e32 v57, v57, v74
	v_fmac_f32_e32 v78, v57, v57
	v_mul_f32_e32 v58, v58, v75
	v_fmac_f32_e32 v78, v58, v58
	v_mul_f32_e32 v59, v59, v76
	v_fmac_f32_e32 v78, v59, v59
	v_mul_f32_e32 v61, v61, v77
	v_fmac_f32_e32 v78, v61, v61
	ds_bpermute_b32 v74, v68, v78
	s_waitcnt lgkmcnt(0)
	v_add_f32_e32 v74, v78, v74
	v_mov_b32_e32 v75, v74
	s_nop 1
	v_permlane16_swap_b32_e32 v75, v74
	s_waitcnt lgkmcnt(0)
	v_add_f32_e32 v74, v74, v75
	s_nop 1
	v_mov_b32_dpp v75, v74 row_ror:8 row_mask:0xf bank_mask:0xf
	s_waitcnt lgkmcnt(0)
	v_add_f32_e32 v74, v74, v75
	s_nop 1
	v_mov_b32_dpp v75, v74 row_shl:4 row_mask:0xf bank_mask:0x5
	v_mov_b32_dpp v75, v74 row_shr:4 row_mask:0xf bank_mask:0xa
	s_waitcnt lgkmcnt(0)
	v_add_f32_e32 v74, v74, v75
	s_nop 1
	v_mov_b32_dpp v75, v74 quad_perm:[2,3,0,1] row_mask:0xf bank_mask:0xf
	s_waitcnt lgkmcnt(0)
	v_add_f32_e32 v74, v74, v75
	s_nop 1
	v_mov_b32_dpp v75, v74 quad_perm:[1,0,3,2] row_mask:0xf bank_mask:0xf
	s_and_saveexec_b64 s[0:1], vcc
	s_cbranch_execz .LBB0_1266
	s_waitcnt lgkmcnt(0)
	v_add_f32_e32 v74, v74, v75
	v_fmamk_f32 v74, v74, 0x3b000000, v246
	s_mov_b32 s2, 0x800000
	v_cmp_gt_f32_e64 s[2:3], s2, v74
	v_mul_f32_e32 v75, 0x4b800000, v74
	s_nop 0
	v_cndmask_b32_e64 v74, v74, v75, s[2:3]
	v_rsq_f32_e32 v74, v74
	s_nop 0
	v_mul_f32_e32 v75, 0x45800000, v74
	v_cndmask_b32_e64 v82, v74, v75, s[2:3]
	global_load_dwordx4 v[74:77], v[62:63], off offset:16
	global_load_dwordx4 v[78:81], v[62:63], off
	v_mul_f32_e32 v54, v54, v82
	v_mul_f32_e32 v60, v60, v82
	v_mul_f32_e32 v55, v55, v82
	s_waitcnt vmcnt(0)
	v_mul_f32_e32 v54, v54, v80
	v_cvt_pk_bf16_f32 v54, v54, s0
	ds_write_b16 v168, v54 offset:35364
	v_mul_f32_e32 v54, v56, v82
	v_mul_f32_e32 v54, v54, v81
	v_cvt_pk_bf16_f32 v54, v54, s0
	ds_write_b16 v168, v54 offset:35636
	v_mul_f32_e32 v54, v57, v82
	v_mul_f32_e32 v54, v54, v74
	v_cvt_pk_bf16_f32 v54, v54, s0
	ds_write_b16 v168, v54 offset:35908
	v_mul_f32_e32 v54, v58, v82
	v_mul_f32_e32 v54, v54, v75
	v_cvt_pk_bf16_f32 v54, v54, s0
	ds_write_b16 v168, v54 offset:36180
	v_mul_f32_e32 v54, v59, v82
	v_mul_f32_e32 v54, v54, v76
	v_cvt_pk_bf16_f32 v54, v54, s0
	ds_write_b16 v168, v54 offset:36452
	v_mul_f32_e32 v54, v61, v82
	v_mul_f32_e32 v60, v60, v78
	v_mul_f32_e32 v55, v55, v79
	v_mul_f32_e32 v54, v54, v77
	v_cvt_pk_bf16_f32 v60, v60, s0
	v_cvt_pk_bf16_f32 v55, v55, s0
	v_cvt_pk_bf16_f32 v54, v54, s0
	ds_write_b16 v168, v60 offset:34820
	ds_write_b16 v168, v55 offset:35092
	ds_write_b16 v168, v54 offset:36724
; __device__ __forceinline__ float bflo(unsigned w) { return __uint_as_float(w << 16); }
; __device__ __forceinline__ float bfhi(unsigned w) { return __uint_as_float(w & 0xffff0000u); }
; __device__ __forceinline__ unsigned short f2bf(float f) { return (unsigned short)(cvt_pk_bf16(f, 0.f) & 0xffffu); }
; __device__ __forceinline__ void sgu_unit(const Params& p, int l, int un, LAS unsigned char* lds) {
;     ...
;     for (int qi = 0; qi < 16; ++qi) { const int q = wave * 16 + qi;
;         const u32x4 v = vv[qi]; float f[8] = {bflo(v.x), bfhi(v.x), bflo(v.y), bfhi(v.y), bflo(v.z), bfhi(v.z), bflo(v.w), bfhi(v.w)}; float ss = 0.f;
; #pragma unroll
;         for (int j = 0; j < 8; ++j) { f[j] = gelu_tanh(f[j]); ss += f[j] * f[j]; }
;         ss = wave_sum(ss); const float rinv = rsqrtf(ss * (1.0f / 512.0f) + EPS);
;         if ((lane >> 4) == h) { const int c0 = (lane & 15) * 8; const float* g = p.in[I_SGUNG] + l * 512 + h * 128 + c0;
; #pragma unroll
;             for (int j = 0; j < 8; ++j) Vl[(c0 + j) * 136 + q] = f2bf(f[j] * rinv * g[j]); } }
.LBB0_1266:
	s_or_b64 exec, exec, s[0:1]
	s_waitcnt vmcnt(12)
	v_lshlrev_b32_e32 v54, 16, v50
	v_lshlrev_b32_e32 v55, 16, v51
	v_and_b32_e32 v57, 0xffff0000, v51
	v_mul_f32_e32 v51, 0x3dd2d3e8, v54
	v_fma_f32 v51, -v51, v54, s33
	v_mul_f32_e32 v51, v51, v54
	v_exp_f32_e32 v51, v51
	v_and_b32_e32 v50, 0xffff0000, v50
	v_lshlrev_b32_e32 v58, 16, v52
	v_and_b32_e32 v59, 0xffff0000, v52
	v_add_f32_e32 v51, 1.0, v51
	v_rcp_f32_e32 v51, v51
	v_mul_f32_e32 v52, 0x3dd2d3e8, v57
	v_fma_f32 v52, -v52, v57, s33
	v_mul_f32_e32 v52, v52, v57
	v_mul_f32_e32 v56, v51, v54
	v_mul_f32_e32 v51, 0x3dd2d3e8, v50
	v_fma_f32 v51, -v51, v50, s33
	v_mul_f32_e32 v51, v51, v50
	v_exp_f32_e32 v51, v51
	v_exp_f32_e32 v52, v52
	v_lshlrev_b32_e32 v60, 16, v53
	v_and_b32_e32 v61, 0xffff0000, v53
	v_add_f32_e32 v51, 1.0, v51
	v_rcp_f32_e32 v51, v51
	v_add_f32_e32 v52, 1.0, v52
	v_rcp_f32_e32 v52, v52
	v_mul_f32_e32 v53, 0x3dd2d3e8, v58
	v_mul_f32_e32 v51, v51, v50
	v_mul_f32_e32 v50, 0x3dd2d3e8, v55
	v_fma_f32 v50, -v50, v55, s33
	v_mul_f32_e32 v50, v50, v55
	v_exp_f32_e32 v50, v50
	v_fma_f32 v53, -v53, v58, s33
	v_mul_f32_e32 v54, 0x3dd2d3e8, v59
	v_mul_f32_e32 v53, v53, v58
	v_add_f32_e32 v50, 1.0, v50
	v_rcp_f32_e32 v50, v50
	v_fma_f32 v54, -v54, v59, s33
	v_mul_f32_e32 v52, v52, v57
	v_exp_f32_e32 v53, v53
	v_mul_f32_e32 v50, v50, v55
	v_mul_f32_e32 v55, 0x3dd2d3e8, v60
	v_mul_f32_e32 v54, v54, v59
	v_fma_f32 v55, -v55, v60, s33
	v_mul_f32_e32 v57, 0x3dd2d3e8, v61
	v_exp_f32_e32 v54, v54
	v_mul_f32_e32 v55, v55, v60
	v_fma_f32 v57, -v57, v61, s33
	v_exp_f32_e32 v55, v55
	v_mul_f32_e32 v57, v57, v61
	v_exp_f32_e32 v57, v57
	v_add_f32_e32 v53, 1.0, v53
	v_rcp_f32_e32 v53, v53
	v_add_f32_e32 v54, 1.0, v54
	v_mul_f32_e32 v74, v51, v51
	v_rcp_f32_e32 v54, v54
	v_add_f32_e32 v55, 1.0, v55
	v_fmac_f32_e32 v74, v56, v56
	v_rcp_f32_e32 v55, v55
	v_add_f32_e32 v57, 1.0, v57
	v_fmac_f32_e32 v74, v50, v50
	v_rcp_f32_e32 v57, v57
	v_fmac_f32_e32 v74, v52, v52
	v_mul_f32_e32 v53, v53, v58
	v_fmac_f32_e32 v74, v53, v53
	v_mul_f32_e32 v54, v54, v59
	v_fmac_f32_e32 v74, v54, v54
	v_mul_f32_e32 v55, v55, v60
	v_fmac_f32_e32 v74, v55, v55
	v_mul_f32_e32 v57, v57, v61
	v_fmac_f32_e32 v74, v57, v57
	ds_bpermute_b32 v58, v68, v74
	s_waitcnt lgkmcnt(0)
	v_add_f32_e32 v58, v74, v58
	v_mov_b32_e32 v59, v58
	s_nop 1
	v_permlane16_swap_b32_e32 v59, v58
	s_waitcnt lgkmcnt(0)
	v_add_f32_e32 v58, v58, v59
	s_nop 1
	v_mov_b32_dpp v59, v58 row_ror:8 row_mask:0xf bank_mask:0xf
	s_waitcnt lgkmcnt(0)
	v_add_f32_e32 v58, v58, v59
	s_nop 1
	v_mov_b32_dpp v59, v58 row_shl:4 row_mask:0xf bank_mask:0x5
	v_mov_b32_dpp v59, v58 row_shr:4 row_mask:0xf bank_mask:0xa
	s_waitcnt lgkmcnt(0)
	v_add_f32_e32 v58, v58, v59
	s_nop 1
	v_mov_b32_dpp v59, v58 quad_perm:[2,3,0,1] row_mask:0xf bank_mask:0xf
	s_waitcnt lgkmcnt(0)
	v_add_f32_e32 v58, v58, v59
	s_nop 1
	v_mov_b32_dpp v59, v58 quad_perm:[1,0,3,2] row_mask:0xf bank_mask:0xf
	s_and_saveexec_b64 s[0:1], vcc
	s_cbranch_execz .LBB0_1268
	s_waitcnt lgkmcnt(0)
	v_add_f32_e32 v58, v58, v59
	v_fmamk_f32 v58, v58, 0x3b000000, v246
	s_mov_b32 s2, 0x800000
	v_cmp_gt_f32_e64 s[2:3], s2, v58
	v_mul_f32_e32 v59, 0x4b800000, v58
	s_nop 0
	v_cndmask_b32_e64 v58, v58, v59, s[2:3]
	v_rsq_f32_e32 v58, v58
	s_nop 0
	v_mul_f32_e32 v59, 0x45800000, v58
	v_cndmask_b32_e64 v78, v58, v59, s[2:3]
	global_load_dwordx4 v[58:61], v[62:63], off offset:16
	global_load_dwordx4 v[74:77], v[62:63], off
	v_mul_f32_e32 v50, v50, v78
	v_mul_f32_e32 v56, v56, v78
	v_mul_f32_e32 v51, v51, v78
	s_waitcnt vmcnt(0)
	v_mul_f32_e32 v50, v50, v76
	v_cvt_pk_bf16_f32 v50, v50, s0
	ds_write_b16 v168, v50 offset:35366
	v_mul_f32_e32 v50, v52, v78
	v_mul_f32_e32 v50, v50, v77
	v_cvt_pk_bf16_f32 v50, v50, s0
	ds_write_b16 v168, v50 offset:35638
	v_mul_f32_e32 v50, v53, v78
	v_mul_f32_e32 v50, v50, v58
	v_cvt_pk_bf16_f32 v50, v50, s0
	ds_write_b16 v168, v50 offset:35910
	v_mul_f32_e32 v50, v54, v78
	v_mul_f32_e32 v50, v50, v59
	v_cvt_pk_bf16_f32 v50, v50, s0
	ds_write_b16 v168, v50 offset:36182
	v_mul_f32_e32 v50, v55, v78
	v_mul_f32_e32 v50, v50, v60
	v_cvt_pk_bf16_f32 v50, v50, s0
	ds_write_b16 v168, v50 offset:36454
	v_mul_f32_e32 v50, v57, v78
	v_mul_f32_e32 v56, v56, v74
	v_mul_f32_e32 v51, v51, v75
	v_mul_f32_e32 v50, v50, v61
	v_cvt_pk_bf16_f32 v56, v56, s0
	v_cvt_pk_bf16_f32 v51, v51, s0
	v_cvt_pk_bf16_f32 v50, v50, s0
	ds_write_b16 v168, v56 offset:34822
	ds_write_b16 v168, v51 offset:35094
	ds_write_b16 v168, v50 offset:36726
; __device__ __forceinline__ float bflo(unsigned w) { return __uint_as_float(w << 16); }
; __device__ __forceinline__ float bfhi(unsigned w) { return __uint_as_float(w & 0xffff0000u); }
; __device__ __forceinline__ unsigned short f2bf(float f) { return (unsigned short)(cvt_pk_bf16(f, 0.f) & 0xffffu); }
; __device__ __forceinline__ void sgu_unit(const Params& p, int l, int un, LAS unsigned char* lds) {
;     ...
;     for (int qi = 0; qi < 16; ++qi) { const int q = wave * 16 + qi;
;         const u32x4 v = vv[qi]; float f[8] = {bflo(v.x), bfhi(v.x), bflo(v.y), bfhi(v.y), bflo(v.z), bfhi(v.z), bflo(v.w), bfhi(v.w)}; float ss = 0.f;
; #pragma unroll
;         for (int j = 0; j < 8; ++j) { f[j] = gelu_tanh(f[j]); ss += f[j] * f[j]; }
;         ss = wave_sum(ss); const float rinv = rsqrtf(ss * (1.0f / 512.0f) + EPS);
;         if ((lane >> 4) == h) { const int c0 = (lane & 15) * 8; const float* g = p.in[I_SGUNG] + l * 512 + h * 128 + c0;
; #pragma unroll
;             for (int j = 0; j < 8; ++j) Vl[(c0 + j) * 136 + q] = f2bf(f[j] * rinv * g[j]); } }
.LBB0_1268:
	s_or_b64 exec, exec, s[0:1]
	s_waitcnt vmcnt(11)
	v_lshlrev_b32_e32 v50, 16, v46
	v_lshlrev_b32_e32 v51, 16, v47
	v_and_b32_e32 v53, 0xffff0000, v47
	v_mul_f32_e32 v47, 0x3dd2d3e8, v50
	v_fma_f32 v47, -v47, v50, s33
	v_mul_f32_e32 v47, v47, v50
	v_exp_f32_e32 v47, v47
	v_and_b32_e32 v46, 0xffff0000, v46
	v_lshlrev_b32_e32 v54, 16, v48
	v_and_b32_e32 v55, 0xffff0000, v48
	v_add_f32_e32 v47, 1.0, v47
	v_rcp_f32_e32 v47, v47
	v_mul_f32_e32 v48, 0x3dd2d3e8, v53
	v_fma_f32 v48, -v48, v53, s33
	v_mul_f32_e32 v48, v48, v53
	v_mul_f32_e32 v52, v47, v50
	v_mul_f32_e32 v47, 0x3dd2d3e8, v46
	v_fma_f32 v47, -v47, v46, s33
	v_mul_f32_e32 v47, v47, v46
	v_exp_f32_e32 v47, v47
	v_exp_f32_e32 v48, v48
	v_lshlrev_b32_e32 v56, 16, v49
	v_and_b32_e32 v57, 0xffff0000, v49
	v_add_f32_e32 v47, 1.0, v47
	v_rcp_f32_e32 v47, v47
	v_add_f32_e32 v48, 1.0, v48
	v_rcp_f32_e32 v48, v48
	v_mul_f32_e32 v49, 0x3dd2d3e8, v54
	v_mul_f32_e32 v47, v47, v46
	v_mul_f32_e32 v46, 0x3dd2d3e8, v51
	v_fma_f32 v46, -v46, v51, s33
	v_mul_f32_e32 v46, v46, v51
	v_exp_f32_e32 v46, v46
	v_fma_f32 v49, -v49, v54, s33
	v_mul_f32_e32 v50, 0x3dd2d3e8, v55
	v_mul_f32_e32 v49, v49, v54
	v_add_f32_e32 v46, 1.0, v46
	v_rcp_f32_e32 v46, v46
	v_fma_f32 v50, -v50, v55, s33
	v_mul_f32_e32 v48, v48, v53
	v_exp_f32_e32 v49, v49
	v_mul_f32_e32 v46, v46, v51
	v_mul_f32_e32 v51, 0x3dd2d3e8, v56
	v_mul_f32_e32 v50, v50, v55
	v_fma_f32 v51, -v51, v56, s33
	v_mul_f32_e32 v53, 0x3dd2d3e8, v57
	v_exp_f32_e32 v50, v50
	v_mul_f32_e32 v51, v51, v56
	v_fma_f32 v53, -v53, v57, s33
	v_exp_f32_e32 v51, v51
	v_mul_f32_e32 v53, v53, v57
	v_exp_f32_e32 v53, v53
	v_add_f32_e32 v49, 1.0, v49
	v_rcp_f32_e32 v49, v49
	v_add_f32_e32 v50, 1.0, v50
	v_mul_f32_e32 v58, v47, v47
	v_rcp_f32_e32 v50, v50
	v_add_f32_e32 v51, 1.0, v51
	v_fmac_f32_e32 v58, v52, v52
	v_rcp_f32_e32 v51, v51
	v_add_f32_e32 v53, 1.0, v53
	v_fmac_f32_e32 v58, v46, v46
	v_rcp_f32_e32 v53, v53
	v_fmac_f32_e32 v58, v48, v48
	v_mul_f32_e32 v49, v49, v54
	v_fmac_f32_e32 v58, v49, v49
	v_mul_f32_e32 v50, v50, v55
	v_fmac_f32_e32 v58, v50, v50
	v_mul_f32_e32 v51, v51, v56
	v_fmac_f32_e32 v58, v51, v51
	v_mul_f32_e32 v53, v53, v57
	v_fmac_f32_e32 v58, v53, v53
	ds_bpermute_b32 v54, v68, v58
	s_waitcnt lgkmcnt(0)
	v_add_f32_e32 v54, v58, v54
	v_mov_b32_e32 v55, v54
	s_nop 1
	v_permlane16_swap_b32_e32 v55, v54
	s_waitcnt lgkmcnt(0)
	v_add_f32_e32 v54, v54, v55
	s_nop 1
	v_mov_b32_dpp v55, v54 row_ror:8 row_mask:0xf bank_mask:0xf
	s_waitcnt lgkmcnt(0)
	v_add_f32_e32 v54, v54, v55
	s_nop 1
	v_mov_b32_dpp v55, v54 row_shl:4 row_mask:0xf bank_mask:0x5
	v_mov_b32_dpp v55, v54 row_shr:4 row_mask:0xf bank_mask:0xa
	s_waitcnt lgkmcnt(0)
	v_add_f32_e32 v54, v54, v55
	s_nop 1
	v_mov_b32_dpp v55, v54 quad_perm:[2,3,0,1] row_mask:0xf bank_mask:0xf
	s_waitcnt lgkmcnt(0)
	v_add_f32_e32 v54, v54, v55
	s_nop 1
	v_mov_b32_dpp v55, v54 quad_perm:[1,0,3,2] row_mask:0xf bank_mask:0xf
	s_and_saveexec_b64 s[0:1], vcc
	s_cbranch_execz .LBB0_1270
	s_waitcnt lgkmcnt(0)
	v_add_f32_e32 v54, v54, v55
	v_fmamk_f32 v54, v54, 0x3b000000, v246
	s_mov_b32 s2, 0x800000
	v_cmp_gt_f32_e64 s[2:3], s2, v54
	v_mul_f32_e32 v55, 0x4b800000, v54
	s_nop 0
	v_cndmask_b32_e64 v54, v54, v55, s[2:3]
	v_rsq_f32_e32 v54, v54
	s_nop 0
	v_mul_f32_e32 v55, 0x45800000, v54
	v_cndmask_b32_e64 v74, v54, v55, s[2:3]
	global_load_dwordx4 v[54:57], v[62:63], off offset:16
	global_load_dwordx4 v[58:61], v[62:63], off
	v_mul_f32_e32 v46, v46, v74
	v_mul_f32_e32 v52, v52, v74
	v_mul_f32_e32 v47, v47, v74
	s_waitcnt vmcnt(0)
	v_mul_f32_e32 v46, v46, v60
	v_cvt_pk_bf16_f32 v46, v46, s0
	ds_write_b16 v168, v46 offset:35368
	v_mul_f32_e32 v46, v48, v74
	v_mul_f32_e32 v46, v46, v61
	v_cvt_pk_bf16_f32 v46, v46, s0
	ds_write_b16 v168, v46 offset:35640
	v_mul_f32_e32 v46, v49, v74
	v_mul_f32_e32 v46, v46, v54
	v_cvt_pk_bf16_f32 v46, v46, s0
	ds_write_b16 v168, v46 offset:35912
	v_mul_f32_e32 v46, v50, v74
	v_mul_f32_e32 v46, v46, v55
	v_cvt_pk_bf16_f32 v46, v46, s0
	ds_write_b16 v168, v46 offset:36184
	v_mul_f32_e32 v46, v51, v74
	v_mul_f32_e32 v46, v46, v56
	v_cvt_pk_bf16_f32 v46, v46, s0
	ds_write_b16 v168, v46 offset:36456
	v_mul_f32_e32 v46, v53, v74
	v_mul_f32_e32 v52, v52, v58
	v_mul_f32_e32 v47, v47, v59
	v_mul_f32_e32 v46, v46, v57
	v_cvt_pk_bf16_f32 v52, v52, s0
	v_cvt_pk_bf16_f32 v47, v47, s0
	v_cvt_pk_bf16_f32 v46, v46, s0
	ds_write_b16 v168, v52 offset:34824
	ds_write_b16 v168, v47 offset:35096
	ds_write_b16 v168, v46 offset:36728
; __device__ __forceinline__ float bflo(unsigned w) { return __uint_as_float(w << 16); }
; __device__ __forceinline__ float bfhi(unsigned w) { return __uint_as_float(w & 0xffff0000u); }
; __device__ __forceinline__ unsigned short f2bf(float f) { return (unsigned short)(cvt_pk_bf16(f, 0.f) & 0xffffu); }
; __device__ __forceinline__ void sgu_unit(const Params& p, int l, int un, LAS unsigned char* lds) {
;     ...
;     for (int qi = 0; qi < 16; ++qi) { const int q = wave * 16 + qi;
;         const u32x4 v = vv[qi]; float f[8] = {bflo(v.x), bfhi(v.x), bflo(v.y), bfhi(v.y), bflo(v.z), bfhi(v.z), bflo(v.w), bfhi(v.w)}; float ss = 0.f;
; #pragma unroll
;         for (int j = 0; j < 8; ++j) { f[j] = gelu_tanh(f[j]); ss += f[j] * f[j]; }
;         ss = wave_sum(ss); const float rinv = rsqrtf(ss * (1.0f / 512.0f) + EPS);
;         if ((lane >> 4) == h) { const int c0 = (lane & 15) * 8; const float* g = p.in[I_SGUNG] + l * 512 + h * 128 + c0;
; #pragma unroll
;             for (int j = 0; j < 8; ++j) Vl[(c0 + j) * 136 + q] = f2bf(f[j] * rinv * g[j]); } }
.LBB0_1270:
	s_or_b64 exec, exec, s[0:1]
	s_waitcnt vmcnt(10)
	v_lshlrev_b32_e32 v46, 16, v42
	v_lshlrev_b32_e32 v47, 16, v43
	v_and_b32_e32 v49, 0xffff0000, v43
	v_mul_f32_e32 v43, 0x3dd2d3e8, v46
	v_fma_f32 v43, -v43, v46, s33
	v_mul_f32_e32 v43, v43, v46
	v_exp_f32_e32 v43, v43
	v_and_b32_e32 v42, 0xffff0000, v42
	v_lshlrev_b32_e32 v50, 16, v44
	v_and_b32_e32 v51, 0xffff0000, v44
	v_add_f32_e32 v43, 1.0, v43
	v_rcp_f32_e32 v43, v43
	v_mul_f32_e32 v44, 0x3dd2d3e8, v49
	v_fma_f32 v44, -v44, v49, s33
	v_mul_f32_e32 v44, v44, v49
	v_mul_f32_e32 v48, v43, v46
	v_mul_f32_e32 v43, 0x3dd2d3e8, v42
	v_fma_f32 v43, -v43, v42, s33
	v_mul_f32_e32 v43, v43, v42
	v_exp_f32_e32 v43, v43
	v_exp_f32_e32 v44, v44
	v_lshlrev_b32_e32 v52, 16, v45
	v_and_b32_e32 v53, 0xffff0000, v45
	v_add_f32_e32 v43, 1.0, v43
	v_rcp_f32_e32 v43, v43
	v_add_f32_e32 v44, 1.0, v44
	v_rcp_f32_e32 v44, v44
	v_mul_f32_e32 v45, 0x3dd2d3e8, v50
	v_mul_f32_e32 v43, v43, v42
	v_mul_f32_e32 v42, 0x3dd2d3e8, v47
	v_fma_f32 v42, -v42, v47, s33
	v_mul_f32_e32 v42, v42, v47
	v_exp_f32_e32 v42, v42
	v_fma_f32 v45, -v45, v50, s33
	v_mul_f32_e32 v46, 0x3dd2d3e8, v51
	v_mul_f32_e32 v45, v45, v50
	v_add_f32_e32 v42, 1.0, v42
	v_rcp_f32_e32 v42, v42
	v_fma_f32 v46, -v46, v51, s33
	v_mul_f32_e32 v44, v44, v49
	v_exp_f32_e32 v45, v45
	v_mul_f32_e32 v42, v42, v47
	v_mul_f32_e32 v47, 0x3dd2d3e8, v52
	v_mul_f32_e32 v46, v46, v51
	v_fma_f32 v47, -v47, v52, s33
	v_mul_f32_e32 v49, 0x3dd2d3e8, v53
	v_exp_f32_e32 v46, v46
	v_mul_f32_e32 v47, v47, v52
	v_fma_f32 v49, -v49, v53, s33
	v_exp_f32_e32 v47, v47
	v_mul_f32_e32 v49, v49, v53
	v_exp_f32_e32 v49, v49
	v_add_f32_e32 v45, 1.0, v45
	v_rcp_f32_e32 v45, v45
	v_add_f32_e32 v46, 1.0, v46
	v_mul_f32_e32 v54, v43, v43
	v_rcp_f32_e32 v46, v46
	v_add_f32_e32 v47, 1.0, v47
	v_fmac_f32_e32 v54, v48, v48
	v_rcp_f32_e32 v47, v47
	v_add_f32_e32 v49, 1.0, v49
	v_fmac_f32_e32 v54, v42, v42
	v_rcp_f32_e32 v49, v49
	v_fmac_f32_e32 v54, v44, v44
	v_mul_f32_e32 v45, v45, v50
	v_fmac_f32_e32 v54, v45, v45
	v_mul_f32_e32 v46, v46, v51
	v_fmac_f32_e32 v54, v46, v46
	v_mul_f32_e32 v47, v47, v52
	v_fmac_f32_e32 v54, v47, v47
	v_mul_f32_e32 v49, v49, v53
	v_fmac_f32_e32 v54, v49, v49
	v_mov_b32_e32 v50, v54
	s_nop 1
	v_permlane32_swap_b32_e32 v50, v54
	s_waitcnt lgkmcnt(0)
	v_add_f32_e32 v50, v54, v50
	v_mov_b32_e32 v51, v50
	s_nop 1
	v_permlane16_swap_b32_e32 v51, v50
	s_waitcnt lgkmcnt(0)
	v_add_f32_e32 v50, v50, v51
	s_nop 1
	v_mov_b32_dpp v51, v50 row_ror:8 row_mask:0xf bank_mask:0xf
	s_waitcnt lgkmcnt(0)
	v_add_f32_e32 v50, v50, v51
	s_nop 1
	v_mov_b32_dpp v51, v50 row_shl:4 row_mask:0xf bank_mask:0x5
	v_mov_b32_dpp v51, v50 row_shr:4 row_mask:0xf bank_mask:0xa
	s_waitcnt lgkmcnt(0)
	v_add_f32_e32 v50, v50, v51
	s_nop 1
	v_mov_b32_dpp v51, v50 quad_perm:[2,3,0,1] row_mask:0xf bank_mask:0xf
	s_waitcnt lgkmcnt(0)
	v_add_f32_e32 v50, v50, v51
	s_nop 1
	v_mov_b32_dpp v51, v50 quad_perm:[1,0,3,2] row_mask:0xf bank_mask:0xf
	s_and_saveexec_b64 s[0:1], vcc
	s_cbranch_execz .LBB0_1272
	s_waitcnt lgkmcnt(0)
	v_add_f32_e32 v50, v50, v51
	v_fmamk_f32 v50, v50, 0x3b000000, v246
	s_mov_b32 s2, 0x800000
	v_cmp_gt_f32_e64 s[2:3], s2, v50
	v_mul_f32_e32 v51, 0x4b800000, v50
	s_nop 0
	v_cndmask_b32_e64 v50, v50, v51, s[2:3]
	v_rsq_f32_e32 v50, v50
	s_nop 0
	v_mul_f32_e32 v51, 0x45800000, v50
	v_cndmask_b32_e64 v58, v50, v51, s[2:3]
	global_load_dwordx4 v[50:53], v[62:63], off offset:16
	global_load_dwordx4 v[54:57], v[62:63], off
	v_mul_f32_e32 v42, v42, v58
	v_mul_f32_e32 v48, v48, v58
	v_mul_f32_e32 v43, v43, v58
	s_waitcnt vmcnt(0)
	v_mul_f32_e32 v42, v42, v56
	v_cvt_pk_bf16_f32 v42, v42, s0
	ds_write_b16 v168, v42 offset:35370
	v_mul_f32_e32 v42, v44, v58
	v_mul_f32_e32 v42, v42, v57
	v_cvt_pk_bf16_f32 v42, v42, s0
	ds_write_b16 v168, v42 offset:35642
	v_mul_f32_e32 v42, v45, v58
	v_mul_f32_e32 v42, v42, v50
	v_cvt_pk_bf16_f32 v42, v42, s0
	ds_write_b16 v168, v42 offset:35914
	v_mul_f32_e32 v42, v46, v58
	v_mul_f32_e32 v42, v42, v51
	v_cvt_pk_bf16_f32 v42, v42, s0
	ds_write_b16 v168, v42 offset:36186
	v_mul_f32_e32 v42, v47, v58
	v_mul_f32_e32 v42, v42, v52
	v_cvt_pk_bf16_f32 v42, v42, s0
	ds_write_b16 v168, v42 offset:36458
	v_mul_f32_e32 v42, v49, v58
	v_mul_f32_e32 v48, v48, v54
	v_mul_f32_e32 v43, v43, v55
	v_mul_f32_e32 v42, v42, v53
	v_cvt_pk_bf16_f32 v48, v48, s0
	v_cvt_pk_bf16_f32 v43, v43, s0
	v_cvt_pk_bf16_f32 v42, v42, s0
	ds_write_b16 v168, v48 offset:34826
	ds_write_b16 v168, v43 offset:35098
	ds_write_b16 v168, v42 offset:36730
; __device__ __forceinline__ float bflo(unsigned w) { return __uint_as_float(w << 16); }
; __device__ __forceinline__ float bfhi(unsigned w) { return __uint_as_float(w & 0xffff0000u); }
; __device__ __forceinline__ unsigned short f2bf(float f) { return (unsigned short)(cvt_pk_bf16(f, 0.f) & 0xffffu); }
; __device__ __forceinline__ void sgu_unit(const Params& p, int l, int un, LAS unsigned char* lds) {
;     ...
;     for (int qi = 0; qi < 16; ++qi) { const int q = wave * 16 + qi;
;         const u32x4 v = vv[qi]; float f[8] = {bflo(v.x), bfhi(v.x), bflo(v.y), bfhi(v.y), bflo(v.z), bfhi(v.z), bflo(v.w), bfhi(v.w)}; float ss = 0.f;
; #pragma unroll
;         for (int j = 0; j < 8; ++j) { f[j] = gelu_tanh(f[j]); ss += f[j] * f[j]; }
;         ss = wave_sum(ss); const float rinv = rsqrtf(ss * (1.0f / 512.0f) + EPS);
;         if ((lane >> 4) == h) { const int c0 = (lane & 15) * 8; const float* g = p.in[I_SGUNG] + l * 512 + h * 128 + c0;
; #pragma unroll
;             for (int j = 0; j < 8; ++j) Vl[(c0 + j) * 136 + q] = f2bf(f[j] * rinv * g[j]); } }
.LBB0_1272:
	s_or_b64 exec, exec, s[0:1]
	s_waitcnt vmcnt(9)
	v_lshlrev_b32_e32 v42, 16, v38
	v_lshlrev_b32_e32 v43, 16, v39
	v_and_b32_e32 v45, 0xffff0000, v39
	v_mul_f32_e32 v39, 0x3dd2d3e8, v42
	v_fma_f32 v39, -v39, v42, s33
	v_mul_f32_e32 v39, v39, v42
	v_exp_f32_e32 v39, v39
	v_and_b32_e32 v38, 0xffff0000, v38
	v_lshlrev_b32_e32 v46, 16, v40
	v_and_b32_e32 v47, 0xffff0000, v40
	v_add_f32_e32 v39, 1.0, v39
	v_rcp_f32_e32 v39, v39
	v_mul_f32_e32 v40, 0x3dd2d3e8, v45
	v_fma_f32 v40, -v40, v45, s33
	v_mul_f32_e32 v40, v40, v45
	v_mul_f32_e32 v44, v39, v42
	v_mul_f32_e32 v39, 0x3dd2d3e8, v38
	v_fma_f32 v39, -v39, v38, s33
	v_mul_f32_e32 v39, v39, v38
	v_exp_f32_e32 v39, v39
	v_exp_f32_e32 v40, v40
	v_lshlrev_b32_e32 v48, 16, v41
	v_and_b32_e32 v49, 0xffff0000, v41
	v_add_f32_e32 v39, 1.0, v39
	v_rcp_f32_e32 v39, v39
	v_add_f32_e32 v40, 1.0, v40
	v_rcp_f32_e32 v40, v40
	v_mul_f32_e32 v41, 0x3dd2d3e8, v46
	v_mul_f32_e32 v39, v39, v38
	v_mul_f32_e32 v38, 0x3dd2d3e8, v43
	v_fma_f32 v38, -v38, v43, s33
	v_mul_f32_e32 v38, v38, v43
	v_exp_f32_e32 v38, v38
	v_fma_f32 v41, -v41, v46, s33
	v_mul_f32_e32 v42, 0x3dd2d3e8, v47
	v_mul_f32_e32 v41, v41, v46
	v_add_f32_e32 v38, 1.0, v38
	v_rcp_f32_e32 v38, v38
	v_fma_f32 v42, -v42, v47, s33
	v_mul_f32_e32 v40, v40, v45
	v_exp_f32_e32 v41, v41
	v_mul_f32_e32 v38, v38, v43
	v_mul_f32_e32 v43, 0x3dd2d3e8, v48
	v_mul_f32_e32 v42, v42, v47
	v_fma_f32 v43, -v43, v48, s33
	v_mul_f32_e32 v45, 0x3dd2d3e8, v49
	v_exp_f32_e32 v42, v42
	v_mul_f32_e32 v43, v43, v48
	v_fma_f32 v45, -v45, v49, s33
	v_exp_f32_e32 v43, v43
	v_mul_f32_e32 v45, v45, v49
	v_exp_f32_e32 v45, v45
	v_add_f32_e32 v41, 1.0, v41
	v_rcp_f32_e32 v41, v41
	v_add_f32_e32 v42, 1.0, v42
	v_mul_f32_e32 v50, v39, v39
	v_rcp_f32_e32 v42, v42
	v_add_f32_e32 v43, 1.0, v43
	v_fmac_f32_e32 v50, v44, v44
	v_rcp_f32_e32 v43, v43
	v_add_f32_e32 v45, 1.0, v45
	v_fmac_f32_e32 v50, v38, v38
	v_rcp_f32_e32 v45, v45
	v_fmac_f32_e32 v50, v40, v40
	v_mul_f32_e32 v41, v41, v46
	v_fmac_f32_e32 v50, v41, v41
	v_mul_f32_e32 v42, v42, v47
	v_fmac_f32_e32 v50, v42, v42
	v_mul_f32_e32 v43, v43, v48
	v_fmac_f32_e32 v50, v43, v43
	v_mul_f32_e32 v45, v45, v49
	v_fmac_f32_e32 v50, v45, v45
	v_mov_b32_e32 v46, v50
	s_nop 1
	v_permlane32_swap_b32_e32 v46, v50
	s_waitcnt lgkmcnt(0)
	v_add_f32_e32 v46, v50, v46
	v_mov_b32_e32 v47, v46
	s_nop 1
	v_permlane16_swap_b32_e32 v47, v46
	s_waitcnt lgkmcnt(0)
	v_add_f32_e32 v46, v46, v47
	s_nop 1
	v_mov_b32_dpp v47, v46 row_ror:8 row_mask:0xf bank_mask:0xf
	s_waitcnt lgkmcnt(0)
	v_add_f32_e32 v46, v46, v47
	s_nop 1
	v_mov_b32_dpp v47, v46 row_shl:4 row_mask:0xf bank_mask:0x5
	v_mov_b32_dpp v47, v46 row_shr:4 row_mask:0xf bank_mask:0xa
	s_waitcnt lgkmcnt(0)
	v_add_f32_e32 v46, v46, v47
	s_nop 1
	v_mov_b32_dpp v47, v46 quad_perm:[2,3,0,1] row_mask:0xf bank_mask:0xf
	s_waitcnt lgkmcnt(0)
	v_add_f32_e32 v46, v46, v47
	s_nop 1
	v_mov_b32_dpp v47, v46 quad_perm:[1,0,3,2] row_mask:0xf bank_mask:0xf
	s_and_saveexec_b64 s[0:1], vcc
	s_cbranch_execz .LBB0_1274
	s_waitcnt lgkmcnt(0)
	v_add_f32_e32 v46, v46, v47
	v_fmamk_f32 v46, v46, 0x3b000000, v246
	s_mov_b32 s2, 0x800000
	v_cmp_gt_f32_e64 s[2:3], s2, v46
	v_mul_f32_e32 v47, 0x4b800000, v46
	s_nop 0
	v_cndmask_b32_e64 v46, v46, v47, s[2:3]
	v_rsq_f32_e32 v46, v46
	s_nop 0
	v_mul_f32_e32 v47, 0x45800000, v46
	v_cndmask_b32_e64 v54, v46, v47, s[2:3]
	global_load_dwordx4 v[46:49], v[62:63], off offset:16
	global_load_dwordx4 v[50:53], v[62:63], off
	v_mul_f32_e32 v38, v38, v54
	v_mul_f32_e32 v44, v44, v54
	v_mul_f32_e32 v39, v39, v54
	s_waitcnt vmcnt(0)
	v_mul_f32_e32 v38, v38, v52
	v_cvt_pk_bf16_f32 v38, v38, s0
	ds_write_b16 v168, v38 offset:35372
	v_mul_f32_e32 v38, v40, v54
	v_mul_f32_e32 v38, v38, v53
	v_cvt_pk_bf16_f32 v38, v38, s0
	ds_write_b16 v168, v38 offset:35644
	v_mul_f32_e32 v38, v41, v54
	v_mul_f32_e32 v38, v38, v46
	v_cvt_pk_bf16_f32 v38, v38, s0
	ds_write_b16 v168, v38 offset:35916
	v_mul_f32_e32 v38, v42, v54
	v_mul_f32_e32 v38, v38, v47
	v_cvt_pk_bf16_f32 v38, v38, s0
	ds_write_b16 v168, v38 offset:36188
	v_mul_f32_e32 v38, v43, v54
	v_mul_f32_e32 v38, v38, v48
	v_cvt_pk_bf16_f32 v38, v38, s0
	ds_write_b16 v168, v38 offset:36460
	v_mul_f32_e32 v38, v45, v54
	v_mul_f32_e32 v44, v44, v50
	v_mul_f32_e32 v39, v39, v51
	v_mul_f32_e32 v38, v38, v49
	v_cvt_pk_bf16_f32 v44, v44, s0
	v_cvt_pk_bf16_f32 v39, v39, s0
	v_cvt_pk_bf16_f32 v38, v38, s0
	ds_write_b16 v168, v44 offset:34828
	ds_write_b16 v168, v39 offset:35100
	ds_write_b16 v168, v38 offset:36732
; __device__ __forceinline__ float bflo(unsigned w) { return __uint_as_float(w << 16); }
; __device__ __forceinline__ float bfhi(unsigned w) { return __uint_as_float(w & 0xffff0000u); }
; __device__ __forceinline__ unsigned short f2bf(float f) { return (unsigned short)(cvt_pk_bf16(f, 0.f) & 0xffffu); }
; __device__ __forceinline__ void sgu_unit(const Params& p, int l, int un, LAS unsigned char* lds) {
;     ...
;     for (int qi = 0; qi < 16; ++qi) { const int q = wave * 16 + qi;
;         const u32x4 v = vv[qi]; float f[8] = {bflo(v.x), bfhi(v.x), bflo(v.y), bfhi(v.y), bflo(v.z), bfhi(v.z), bflo(v.w), bfhi(v.w)}; float ss = 0.f;
; #pragma unroll
;         for (int j = 0; j < 8; ++j) { f[j] = gelu_tanh(f[j]); ss += f[j] * f[j]; }
;         ss = wave_sum(ss); const float rinv = rsqrtf(ss * (1.0f / 512.0f) + EPS);
;         if ((lane >> 4) == h) { const int c0 = (lane & 15) * 8; const float* g = p.in[I_SGUNG] + l * 512 + h * 128 + c0;
; #pragma unroll
;             for (int j = 0; j < 8; ++j) Vl[(c0 + j) * 136 + q] = f2bf(f[j] * rinv * g[j]); } }
.LBB0_1274:
	s_or_b64 exec, exec, s[0:1]
	s_waitcnt vmcnt(8)
	v_lshlrev_b32_e32 v38, 16, v34
	v_lshlrev_b32_e32 v39, 16, v35
	v_and_b32_e32 v41, 0xffff0000, v35
	v_mul_f32_e32 v35, 0x3dd2d3e8, v38
	v_fma_f32 v35, -v35, v38, s33
	v_mul_f32_e32 v35, v35, v38
	v_exp_f32_e32 v35, v35
	v_and_b32_e32 v34, 0xffff0000, v34
	v_lshlrev_b32_e32 v42, 16, v36
	v_and_b32_e32 v43, 0xffff0000, v36
	v_add_f32_e32 v35, 1.0, v35
	v_rcp_f32_e32 v35, v35
	v_mul_f32_e32 v36, 0x3dd2d3e8, v41
	v_fma_f32 v36, -v36, v41, s33
	v_mul_f32_e32 v36, v36, v41
	v_mul_f32_e32 v40, v35, v38
	v_mul_f32_e32 v35, 0x3dd2d3e8, v34
	v_fma_f32 v35, -v35, v34, s33
	v_mul_f32_e32 v35, v35, v34
	v_exp_f32_e32 v35, v35
	v_exp_f32_e32 v36, v36
	v_lshlrev_b32_e32 v44, 16, v37
	v_and_b32_e32 v45, 0xffff0000, v37
	v_add_f32_e32 v35, 1.0, v35
	v_rcp_f32_e32 v35, v35
	v_add_f32_e32 v36, 1.0, v36
	v_rcp_f32_e32 v36, v36
	v_mul_f32_e32 v37, 0x3dd2d3e8, v42
	v_mul_f32_e32 v35, v35, v34
	v_mul_f32_e32 v34, 0x3dd2d3e8, v39
	v_fma_f32 v34, -v34, v39, s33
	v_mul_f32_e32 v34, v34, v39
	v_exp_f32_e32 v34, v34
	v_fma_f32 v37, -v37, v42, s33
	v_mul_f32_e32 v38, 0x3dd2d3e8, v43
	v_mul_f32_e32 v37, v37, v42
	v_add_f32_e32 v34, 1.0, v34
	v_rcp_f32_e32 v34, v34
	v_fma_f32 v38, -v38, v43, s33
	v_mul_f32_e32 v36, v36, v41
	v_exp_f32_e32 v37, v37
	v_mul_f32_e32 v34, v34, v39
	v_mul_f32_e32 v39, 0x3dd2d3e8, v44
	v_mul_f32_e32 v38, v38, v43
	v_fma_f32 v39, -v39, v44, s33
	v_mul_f32_e32 v41, 0x3dd2d3e8, v45
	v_exp_f32_e32 v38, v38
	v_mul_f32_e32 v39, v39, v44
	v_fma_f32 v41, -v41, v45, s33
	v_exp_f32_e32 v39, v39
	v_mul_f32_e32 v41, v41, v45
	v_exp_f32_e32 v41, v41
	v_add_f32_e32 v37, 1.0, v37
	v_rcp_f32_e32 v37, v37
	v_add_f32_e32 v38, 1.0, v38
	v_mul_f32_e32 v46, v35, v35
	v_rcp_f32_e32 v38, v38
	v_add_f32_e32 v39, 1.0, v39
	v_fmac_f32_e32 v46, v40, v40
	v_rcp_f32_e32 v39, v39
	v_add_f32_e32 v41, 1.0, v41
	v_fmac_f32_e32 v46, v34, v34
	v_rcp_f32_e32 v41, v41
	v_fmac_f32_e32 v46, v36, v36
	v_mul_f32_e32 v37, v37, v42
	v_fmac_f32_e32 v46, v37, v37
	v_mul_f32_e32 v38, v38, v43
	v_fmac_f32_e32 v46, v38, v38
	v_mul_f32_e32 v39, v39, v44
	v_fmac_f32_e32 v46, v39, v39
	v_mul_f32_e32 v41, v41, v45
	v_fmac_f32_e32 v46, v41, v41
	v_mov_b32_e32 v42, v46
	s_nop 1
	v_permlane32_swap_b32_e32 v42, v46
	s_waitcnt lgkmcnt(0)
	v_add_f32_e32 v42, v46, v42
	v_mov_b32_e32 v43, v42
	s_nop 1
	v_permlane16_swap_b32_e32 v43, v42
	s_waitcnt lgkmcnt(0)
	v_add_f32_e32 v42, v42, v43
	s_nop 1
	v_mov_b32_dpp v43, v42 row_ror:8 row_mask:0xf bank_mask:0xf
	s_waitcnt lgkmcnt(0)
	v_add_f32_e32 v42, v42, v43
	s_nop 1
	v_mov_b32_dpp v43, v42 row_shl:4 row_mask:0xf bank_mask:0x5
	v_mov_b32_dpp v43, v42 row_shr:4 row_mask:0xf bank_mask:0xa
	s_waitcnt lgkmcnt(0)
	v_add_f32_e32 v42, v42, v43
	s_nop 1
	v_mov_b32_dpp v43, v42 quad_perm:[2,3,0,1] row_mask:0xf bank_mask:0xf
	s_waitcnt lgkmcnt(0)
	v_add_f32_e32 v42, v42, v43
	s_nop 1
	v_mov_b32_dpp v43, v42 quad_perm:[1,0,3,2] row_mask:0xf bank_mask:0xf
	s_and_saveexec_b64 s[0:1], vcc
	s_cbranch_execz .LBB0_1276
	s_waitcnt lgkmcnt(0)
	v_add_f32_e32 v42, v42, v43
	v_fmamk_f32 v42, v42, 0x3b000000, v246
	s_mov_b32 s2, 0x800000
	v_cmp_gt_f32_e64 s[2:3], s2, v42
	v_mul_f32_e32 v43, 0x4b800000, v42
	s_nop 0
	v_cndmask_b32_e64 v42, v42, v43, s[2:3]
	v_rsq_f32_e32 v42, v42
	s_nop 0
	v_mul_f32_e32 v43, 0x45800000, v42
	v_cndmask_b32_e64 v50, v42, v43, s[2:3]
	global_load_dwordx4 v[42:45], v[62:63], off offset:16
	global_load_dwordx4 v[46:49], v[62:63], off
	v_mul_f32_e32 v34, v34, v50
	v_mul_f32_e32 v40, v40, v50
	v_mul_f32_e32 v35, v35, v50
	s_waitcnt vmcnt(0)
	v_mul_f32_e32 v34, v34, v48
	v_cvt_pk_bf16_f32 v34, v34, s0
	ds_write_b16 v168, v34 offset:35374
	v_mul_f32_e32 v34, v36, v50
	v_mul_f32_e32 v34, v34, v49
	v_cvt_pk_bf16_f32 v34, v34, s0
	ds_write_b16 v168, v34 offset:35646
	v_mul_f32_e32 v34, v37, v50
	v_mul_f32_e32 v34, v34, v42
	v_cvt_pk_bf16_f32 v34, v34, s0
	ds_write_b16 v168, v34 offset:35918
	v_mul_f32_e32 v34, v38, v50
	v_mul_f32_e32 v34, v34, v43
	v_cvt_pk_bf16_f32 v34, v34, s0
	ds_write_b16 v168, v34 offset:36190
	v_mul_f32_e32 v34, v39, v50
	v_mul_f32_e32 v34, v34, v44
	v_cvt_pk_bf16_f32 v34, v34, s0
	ds_write_b16 v168, v34 offset:36462
	v_mul_f32_e32 v34, v41, v50
	v_mul_f32_e32 v40, v40, v46
	v_mul_f32_e32 v35, v35, v47
	v_mul_f32_e32 v34, v34, v45
	v_cvt_pk_bf16_f32 v40, v40, s0
	v_cvt_pk_bf16_f32 v35, v35, s0
	v_cvt_pk_bf16_f32 v34, v34, s0
	ds_write_b16 v168, v40 offset:34830
	ds_write_b16 v168, v35 offset:35102
	ds_write_b16 v168, v34 offset:36734
; __device__ __forceinline__ float bflo(unsigned w) { return __uint_as_float(w << 16); }
; __device__ __forceinline__ float bfhi(unsigned w) { return __uint_as_float(w & 0xffff0000u); }
; __device__ __forceinline__ unsigned short f2bf(float f) { return (unsigned short)(cvt_pk_bf16(f, 0.f) & 0xffffu); }
; __device__ __forceinline__ void sgu_unit(const Params& p, int l, int un, LAS unsigned char* lds) {
;     ...
;     for (int qi = 0; qi < 16; ++qi) { const int q = wave * 16 + qi;
;         const u32x4 v = vv[qi]; float f[8] = {bflo(v.x), bfhi(v.x), bflo(v.y), bfhi(v.y), bflo(v.z), bfhi(v.z), bflo(v.w), bfhi(v.w)}; float ss = 0.f;
; #pragma unroll
;         for (int j = 0; j < 8; ++j) { f[j] = gelu_tanh(f[j]); ss += f[j] * f[j]; }
;         ss = wave_sum(ss); const float rinv = rsqrtf(ss * (1.0f / 512.0f) + EPS);
;         if ((lane >> 4) == h) { const int c0 = (lane & 15) * 8; const float* g = p.in[I_SGUNG] + l * 512 + h * 128 + c0;
; #pragma unroll
;             for (int j = 0; j < 8; ++j) Vl[(c0 + j) * 136 + q] = f2bf(f[j] * rinv * g[j]); } }
.LBB0_1276:
	s_or_b64 exec, exec, s[0:1]
	s_waitcnt vmcnt(7)
	v_lshlrev_b32_e32 v34, 16, v30
	v_lshlrev_b32_e32 v35, 16, v31
	v_and_b32_e32 v37, 0xffff0000, v31
	v_mul_f32_e32 v31, 0x3dd2d3e8, v34
	v_fma_f32 v31, -v31, v34, s33
	v_mul_f32_e32 v31, v31, v34
	v_exp_f32_e32 v31, v31
	v_and_b32_e32 v30, 0xffff0000, v30
	v_lshlrev_b32_e32 v38, 16, v32
	v_and_b32_e32 v39, 0xffff0000, v32
	v_add_f32_e32 v31, 1.0, v31
	v_rcp_f32_e32 v31, v31
	v_mul_f32_e32 v32, 0x3dd2d3e8, v37
	v_fma_f32 v32, -v32, v37, s33
	v_mul_f32_e32 v32, v32, v37
	v_mul_f32_e32 v36, v31, v34
	v_mul_f32_e32 v31, 0x3dd2d3e8, v30
	v_fma_f32 v31, -v31, v30, s33
	v_mul_f32_e32 v31, v31, v30
	v_exp_f32_e32 v31, v31
	v_exp_f32_e32 v32, v32
	v_lshlrev_b32_e32 v40, 16, v33
	v_and_b32_e32 v41, 0xffff0000, v33
	v_add_f32_e32 v31, 1.0, v31
	v_rcp_f32_e32 v31, v31
	v_add_f32_e32 v32, 1.0, v32
	v_rcp_f32_e32 v32, v32
	v_mul_f32_e32 v33, 0x3dd2d3e8, v38
	v_mul_f32_e32 v31, v31, v30
	v_mul_f32_e32 v30, 0x3dd2d3e8, v35
	v_fma_f32 v30, -v30, v35, s33
	v_mul_f32_e32 v30, v30, v35
	v_exp_f32_e32 v30, v30
	v_fma_f32 v33, -v33, v38, s33
	v_mul_f32_e32 v34, 0x3dd2d3e8, v39
	v_mul_f32_e32 v33, v33, v38
	v_add_f32_e32 v30, 1.0, v30
	v_rcp_f32_e32 v30, v30
	v_fma_f32 v34, -v34, v39, s33
	v_mul_f32_e32 v32, v32, v37
	v_exp_f32_e32 v33, v33
	v_mul_f32_e32 v30, v30, v35
	v_mul_f32_e32 v35, 0x3dd2d3e8, v40
	v_mul_f32_e32 v34, v34, v39
	v_fma_f32 v35, -v35, v40, s33
	v_mul_f32_e32 v37, 0x3dd2d3e8, v41
	v_exp_f32_e32 v34, v34
	v_mul_f32_e32 v35, v35, v40
	v_fma_f32 v37, -v37, v41, s33
	v_exp_f32_e32 v35, v35
	v_mul_f32_e32 v37, v37, v41
	v_exp_f32_e32 v37, v37
	v_add_f32_e32 v33, 1.0, v33
	v_rcp_f32_e32 v33, v33
	v_add_f32_e32 v34, 1.0, v34
	v_mul_f32_e32 v42, v31, v31
	v_rcp_f32_e32 v34, v34
	v_add_f32_e32 v35, 1.0, v35
	v_fmac_f32_e32 v42, v36, v36
	v_rcp_f32_e32 v35, v35
	v_add_f32_e32 v37, 1.0, v37
	v_fmac_f32_e32 v42, v30, v30
	v_rcp_f32_e32 v37, v37
	v_fmac_f32_e32 v42, v32, v32
	v_mul_f32_e32 v33, v33, v38
	v_fmac_f32_e32 v42, v33, v33
	v_mul_f32_e32 v34, v34, v39
	v_fmac_f32_e32 v42, v34, v34
	v_mul_f32_e32 v35, v35, v40
	v_fmac_f32_e32 v42, v35, v35
	v_mul_f32_e32 v37, v37, v41
	v_fmac_f32_e32 v42, v37, v37
	v_mov_b32_e32 v38, v42
	s_nop 1
	v_permlane32_swap_b32_e32 v38, v42
	s_waitcnt lgkmcnt(0)
	v_add_f32_e32 v38, v42, v38
	v_mov_b32_e32 v39, v38
	s_nop 1
	v_permlane16_swap_b32_e32 v39, v38
	s_waitcnt lgkmcnt(0)
	v_add_f32_e32 v38, v38, v39
	s_nop 1
	v_mov_b32_dpp v39, v38 row_ror:8 row_mask:0xf bank_mask:0xf
	s_waitcnt lgkmcnt(0)
	v_add_f32_e32 v38, v38, v39
	s_nop 1
	v_mov_b32_dpp v39, v38 row_shl:4 row_mask:0xf bank_mask:0x5
	v_mov_b32_dpp v39, v38 row_shr:4 row_mask:0xf bank_mask:0xa
	s_waitcnt lgkmcnt(0)
	v_add_f32_e32 v38, v38, v39
	s_nop 1
	v_mov_b32_dpp v39, v38 quad_perm:[2,3,0,1] row_mask:0xf bank_mask:0xf
	s_waitcnt lgkmcnt(0)
	v_add_f32_e32 v38, v38, v39
	s_nop 1
	v_mov_b32_dpp v39, v38 quad_perm:[1,0,3,2] row_mask:0xf bank_mask:0xf
	s_and_saveexec_b64 s[0:1], vcc
	s_cbranch_execz .LBB0_1278
	s_waitcnt lgkmcnt(0)
	v_add_f32_e32 v38, v38, v39
	v_fmamk_f32 v38, v38, 0x3b000000, v246
	s_mov_b32 s2, 0x800000
	v_cmp_gt_f32_e64 s[2:3], s2, v38
	v_mul_f32_e32 v39, 0x4b800000, v38
	s_nop 0
	v_cndmask_b32_e64 v38, v38, v39, s[2:3]
	v_rsq_f32_e32 v38, v38
	s_nop 0
	v_mul_f32_e32 v39, 0x45800000, v38
	v_cndmask_b32_e64 v46, v38, v39, s[2:3]
	global_load_dwordx4 v[38:41], v[62:63], off offset:16
	global_load_dwordx4 v[42:45], v[62:63], off
	v_mul_f32_e32 v30, v30, v46
	v_mul_f32_e32 v36, v36, v46
	v_mul_f32_e32 v31, v31, v46
	s_waitcnt vmcnt(0)
	v_mul_f32_e32 v30, v30, v44
	v_cvt_pk_bf16_f32 v30, v30, s0
	ds_write_b16 v169, v30 offset:35376
	v_mul_f32_e32 v30, v32, v46
	v_mul_f32_e32 v30, v30, v45
	v_cvt_pk_bf16_f32 v30, v30, s0
	ds_write_b16 v169, v30 offset:35648
	v_mul_f32_e32 v30, v33, v46
	v_mul_f32_e32 v30, v30, v38
	v_cvt_pk_bf16_f32 v30, v30, s0
	ds_write_b16 v169, v30 offset:35920
	v_mul_f32_e32 v30, v34, v46
	v_mul_f32_e32 v30, v30, v39
	v_cvt_pk_bf16_f32 v30, v30, s0
	ds_write_b16 v169, v30 offset:36192
	v_mul_f32_e32 v30, v35, v46
	v_mul_f32_e32 v30, v30, v40
	v_cvt_pk_bf16_f32 v30, v30, s0
	ds_write_b16 v169, v30 offset:36464
	v_mul_f32_e32 v30, v37, v46
	v_mul_f32_e32 v36, v36, v42
	v_mul_f32_e32 v31, v31, v43
	v_mul_f32_e32 v30, v30, v41
	v_cvt_pk_bf16_f32 v36, v36, s0
	v_cvt_pk_bf16_f32 v31, v31, s0
	v_cvt_pk_bf16_f32 v30, v30, s0
	ds_write_b16 v169, v36 offset:34832
	ds_write_b16 v169, v31 offset:35104
	ds_write_b16 v169, v30 offset:36736
; __device__ __forceinline__ float bflo(unsigned w) { return __uint_as_float(w << 16); }
; __device__ __forceinline__ float bfhi(unsigned w) { return __uint_as_float(w & 0xffff0000u); }
; __device__ __forceinline__ unsigned short f2bf(float f) { return (unsigned short)(cvt_pk_bf16(f, 0.f) & 0xffffu); }
; __device__ __forceinline__ void sgu_unit(const Params& p, int l, int un, LAS unsigned char* lds) {
;     ...
;     for (int qi = 0; qi < 16; ++qi) { const int q = wave * 16 + qi;
;         const u32x4 v = vv[qi]; float f[8] = {bflo(v.x), bfhi(v.x), bflo(v.y), bfhi(v.y), bflo(v.z), bfhi(v.z), bflo(v.w), bfhi(v.w)}; float ss = 0.f;
; #pragma unroll
;         for (int j = 0; j < 8; ++j) { f[j] = gelu_tanh(f[j]); ss += f[j] * f[j]; }
;         ss = wave_sum(ss); const float rinv = rsqrtf(ss * (1.0f / 512.0f) + EPS);
;         if ((lane >> 4) == h) { const int c0 = (lane & 15) * 8; const float* g = p.in[I_SGUNG] + l * 512 + h * 128 + c0;
; #pragma unroll
;             for (int j = 0; j < 8; ++j) Vl[(c0 + j) * 136 + q] = f2bf(f[j] * rinv * g[j]); } }
.LBB0_1278:
	s_or_b64 exec, exec, s[0:1]
	s_waitcnt vmcnt(6)
	v_lshlrev_b32_e32 v30, 16, v26
	v_lshlrev_b32_e32 v31, 16, v27
	v_and_b32_e32 v33, 0xffff0000, v27
	v_mul_f32_e32 v27, 0x3dd2d3e8, v30
	v_fma_f32 v27, -v27, v30, s33
	v_mul_f32_e32 v27, v27, v30
	v_exp_f32_e32 v27, v27
	v_and_b32_e32 v26, 0xffff0000, v26
	v_lshlrev_b32_e32 v34, 16, v28
	v_and_b32_e32 v35, 0xffff0000, v28
	v_add_f32_e32 v27, 1.0, v27
	v_rcp_f32_e32 v27, v27
	v_mul_f32_e32 v28, 0x3dd2d3e8, v33
	v_fma_f32 v28, -v28, v33, s33
	v_mul_f32_e32 v28, v28, v33
	v_mul_f32_e32 v32, v27, v30
	v_mul_f32_e32 v27, 0x3dd2d3e8, v26
	v_fma_f32 v27, -v27, v26, s33
	v_mul_f32_e32 v27, v27, v26
	v_exp_f32_e32 v27, v27
	v_exp_f32_e32 v28, v28
	v_lshlrev_b32_e32 v36, 16, v29
	v_and_b32_e32 v37, 0xffff0000, v29
	v_add_f32_e32 v27, 1.0, v27
	v_rcp_f32_e32 v27, v27
	v_add_f32_e32 v28, 1.0, v28
	v_rcp_f32_e32 v28, v28
	v_mul_f32_e32 v29, 0x3dd2d3e8, v34
	v_mul_f32_e32 v27, v27, v26
	v_mul_f32_e32 v26, 0x3dd2d3e8, v31
	v_fma_f32 v26, -v26, v31, s33
	v_mul_f32_e32 v26, v26, v31
	v_exp_f32_e32 v26, v26
	v_fma_f32 v29, -v29, v34, s33
	v_mul_f32_e32 v30, 0x3dd2d3e8, v35
	v_mul_f32_e32 v29, v29, v34
	v_add_f32_e32 v26, 1.0, v26
	v_rcp_f32_e32 v26, v26
	v_fma_f32 v30, -v30, v35, s33
	v_mul_f32_e32 v28, v28, v33
	v_exp_f32_e32 v29, v29
	v_mul_f32_e32 v26, v26, v31
	v_mul_f32_e32 v31, 0x3dd2d3e8, v36
	v_mul_f32_e32 v30, v30, v35
	v_fma_f32 v31, -v31, v36, s33
	v_mul_f32_e32 v33, 0x3dd2d3e8, v37
	v_exp_f32_e32 v30, v30
	v_mul_f32_e32 v31, v31, v36
	v_fma_f32 v33, -v33, v37, s33
	v_exp_f32_e32 v31, v31
	v_mul_f32_e32 v33, v33, v37
	v_exp_f32_e32 v33, v33
	v_add_f32_e32 v29, 1.0, v29
	v_rcp_f32_e32 v29, v29
	v_add_f32_e32 v30, 1.0, v30
	v_mul_f32_e32 v38, v27, v27
	v_rcp_f32_e32 v30, v30
	v_add_f32_e32 v31, 1.0, v31
	v_fmac_f32_e32 v38, v32, v32
	v_rcp_f32_e32 v31, v31
	v_add_f32_e32 v33, 1.0, v33
	v_fmac_f32_e32 v38, v26, v26
	v_rcp_f32_e32 v33, v33
	v_fmac_f32_e32 v38, v28, v28
	v_mul_f32_e32 v29, v29, v34
	v_fmac_f32_e32 v38, v29, v29
	v_mul_f32_e32 v30, v30, v35
	v_fmac_f32_e32 v38, v30, v30
	v_mul_f32_e32 v31, v31, v36
	v_fmac_f32_e32 v38, v31, v31
	v_mul_f32_e32 v33, v33, v37
	v_fmac_f32_e32 v38, v33, v33
	v_mov_b32_e32 v34, v38
	s_nop 1
	v_permlane32_swap_b32_e32 v34, v38
	s_waitcnt lgkmcnt(0)
	v_add_f32_e32 v34, v38, v34
	v_mov_b32_e32 v35, v34
	s_nop 1
	v_permlane16_swap_b32_e32 v35, v34
	s_waitcnt lgkmcnt(0)
	v_add_f32_e32 v34, v34, v35
	s_nop 1
	v_mov_b32_dpp v35, v34 row_ror:8 row_mask:0xf bank_mask:0xf
	s_waitcnt lgkmcnt(0)
	v_add_f32_e32 v34, v34, v35
	s_nop 1
	v_mov_b32_dpp v35, v34 row_shl:4 row_mask:0xf bank_mask:0x5
	v_mov_b32_dpp v35, v34 row_shr:4 row_mask:0xf bank_mask:0xa
	s_waitcnt lgkmcnt(0)
	v_add_f32_e32 v34, v34, v35
	s_nop 1
	v_mov_b32_dpp v35, v34 quad_perm:[2,3,0,1] row_mask:0xf bank_mask:0xf
	s_waitcnt lgkmcnt(0)
	v_add_f32_e32 v34, v34, v35
	s_nop 1
	v_mov_b32_dpp v35, v34 quad_perm:[1,0,3,2] row_mask:0xf bank_mask:0xf
	s_and_saveexec_b64 s[0:1], vcc
	s_cbranch_execz .LBB0_1280
	s_waitcnt lgkmcnt(0)
	v_add_f32_e32 v34, v34, v35
	v_fmamk_f32 v34, v34, 0x3b000000, v246
	s_mov_b32 s2, 0x800000
	v_cmp_gt_f32_e64 s[2:3], s2, v34
	v_mul_f32_e32 v35, 0x4b800000, v34
	s_nop 0
	v_cndmask_b32_e64 v34, v34, v35, s[2:3]
	v_rsq_f32_e32 v34, v34
	s_nop 0
	v_mul_f32_e32 v35, 0x45800000, v34
	v_cndmask_b32_e64 v42, v34, v35, s[2:3]
	global_load_dwordx4 v[34:37], v[62:63], off offset:16
	global_load_dwordx4 v[38:41], v[62:63], off
	v_mul_f32_e32 v26, v26, v42
	v_mul_f32_e32 v32, v32, v42
	v_mul_f32_e32 v27, v27, v42
	s_waitcnt vmcnt(0)
	v_mul_f32_e32 v26, v26, v40
	v_cvt_pk_bf16_f32 v26, v26, s0
	ds_write_b16 v169, v26 offset:35378
	v_mul_f32_e32 v26, v28, v42
	v_mul_f32_e32 v26, v26, v41
	v_cvt_pk_bf16_f32 v26, v26, s0
	ds_write_b16 v169, v26 offset:35650
	v_mul_f32_e32 v26, v29, v42
	v_mul_f32_e32 v26, v26, v34
	v_cvt_pk_bf16_f32 v26, v26, s0
	ds_write_b16 v169, v26 offset:35922
	v_mul_f32_e32 v26, v30, v42
	v_mul_f32_e32 v26, v26, v35
	v_cvt_pk_bf16_f32 v26, v26, s0
	ds_write_b16 v169, v26 offset:36194
	v_mul_f32_e32 v26, v31, v42
	v_mul_f32_e32 v26, v26, v36
	v_cvt_pk_bf16_f32 v26, v26, s0
	ds_write_b16 v169, v26 offset:36466
	v_mul_f32_e32 v26, v33, v42
	v_mul_f32_e32 v32, v32, v38
	v_mul_f32_e32 v27, v27, v39
	v_mul_f32_e32 v26, v26, v37
	v_cvt_pk_bf16_f32 v32, v32, s0
	v_cvt_pk_bf16_f32 v27, v27, s0
	v_cvt_pk_bf16_f32 v26, v26, s0
	ds_write_b16 v169, v32 offset:34834
	ds_write_b16 v169, v27 offset:35106
	ds_write_b16 v169, v26 offset:36738
; __device__ __forceinline__ float bflo(unsigned w) { return __uint_as_float(w << 16); }
; __device__ __forceinline__ float bfhi(unsigned w) { return __uint_as_float(w & 0xffff0000u); }
; __device__ __forceinline__ unsigned short f2bf(float f) { return (unsigned short)(cvt_pk_bf16(f, 0.f) & 0xffffu); }
; __device__ __forceinline__ void sgu_unit(const Params& p, int l, int un, LAS unsigned char* lds) {
;     ...
;     for (int qi = 0; qi < 16; ++qi) { const int q = wave * 16 + qi;
;         const u32x4 v = vv[qi]; float f[8] = {bflo(v.x), bfhi(v.x), bflo(v.y), bfhi(v.y), bflo(v.z), bfhi(v.z), bflo(v.w), bfhi(v.w)}; float ss = 0.f;
; #pragma unroll
;         for (int j = 0; j < 8; ++j) { f[j] = gelu_tanh(f[j]); ss += f[j] * f[j]; }
;         ss = wave_sum(ss); const float rinv = rsqrtf(ss * (1.0f / 512.0f) + EPS);
;         if ((lane >> 4) == h) { const int c0 = (lane & 15) * 8; const float* g = p.in[I_SGUNG] + l * 512 + h * 128 + c0;
; #pragma unroll
;             for (int j = 0; j < 8; ++j) Vl[(c0 + j) * 136 + q] = f2bf(f[j] * rinv * g[j]); } }
.LBB0_1280:
	s_or_b64 exec, exec, s[0:1]
	s_waitcnt vmcnt(5)
	v_lshlrev_b32_e32 v26, 16, v22
	v_lshlrev_b32_e32 v27, 16, v23
	v_and_b32_e32 v29, 0xffff0000, v23
	v_mul_f32_e32 v23, 0x3dd2d3e8, v26
	v_fma_f32 v23, -v23, v26, s33
	v_mul_f32_e32 v23, v23, v26
	v_exp_f32_e32 v23, v23
	v_and_b32_e32 v22, 0xffff0000, v22
	v_lshlrev_b32_e32 v30, 16, v24
	v_and_b32_e32 v31, 0xffff0000, v24
	v_add_f32_e32 v23, 1.0, v23
	v_rcp_f32_e32 v23, v23
	v_mul_f32_e32 v24, 0x3dd2d3e8, v29
	v_fma_f32 v24, -v24, v29, s33
	v_mul_f32_e32 v24, v24, v29
	v_mul_f32_e32 v28, v23, v26
	v_mul_f32_e32 v23, 0x3dd2d3e8, v22
	v_fma_f32 v23, -v23, v22, s33
	v_mul_f32_e32 v23, v23, v22
	v_exp_f32_e32 v23, v23
	v_exp_f32_e32 v24, v24
	v_lshlrev_b32_e32 v32, 16, v25
	v_and_b32_e32 v33, 0xffff0000, v25
	v_add_f32_e32 v23, 1.0, v23
	v_rcp_f32_e32 v23, v23
	v_add_f32_e32 v24, 1.0, v24
	v_rcp_f32_e32 v24, v24
	v_mul_f32_e32 v25, 0x3dd2d3e8, v30
	v_mul_f32_e32 v23, v23, v22
	v_mul_f32_e32 v22, 0x3dd2d3e8, v27
	v_fma_f32 v22, -v22, v27, s33
	v_mul_f32_e32 v22, v22, v27
	v_exp_f32_e32 v22, v22
	v_fma_f32 v25, -v25, v30, s33
	v_mul_f32_e32 v26, 0x3dd2d3e8, v31
	v_mul_f32_e32 v25, v25, v30
	v_add_f32_e32 v22, 1.0, v22
	v_rcp_f32_e32 v22, v22
	v_fma_f32 v26, -v26, v31, s33
	v_mul_f32_e32 v24, v24, v29
	v_exp_f32_e32 v25, v25
	v_mul_f32_e32 v22, v22, v27
	v_mul_f32_e32 v27, 0x3dd2d3e8, v32
	v_mul_f32_e32 v26, v26, v31
	v_fma_f32 v27, -v27, v32, s33
	v_mul_f32_e32 v29, 0x3dd2d3e8, v33
	v_exp_f32_e32 v26, v26
	v_mul_f32_e32 v27, v27, v32
	v_fma_f32 v29, -v29, v33, s33
	v_exp_f32_e32 v27, v27
	v_mul_f32_e32 v29, v29, v33
	v_exp_f32_e32 v29, v29
	v_add_f32_e32 v25, 1.0, v25
	v_rcp_f32_e32 v25, v25
	v_add_f32_e32 v26, 1.0, v26
	v_mul_f32_e32 v34, v23, v23
	v_rcp_f32_e32 v26, v26
	v_add_f32_e32 v27, 1.0, v27
	v_fmac_f32_e32 v34, v28, v28
	v_rcp_f32_e32 v27, v27
	v_add_f32_e32 v29, 1.0, v29
	v_fmac_f32_e32 v34, v22, v22
	v_rcp_f32_e32 v29, v29
	v_fmac_f32_e32 v34, v24, v24
	v_mul_f32_e32 v25, v25, v30
	v_fmac_f32_e32 v34, v25, v25
	v_mul_f32_e32 v26, v26, v31
	v_fmac_f32_e32 v34, v26, v26
	v_mul_f32_e32 v27, v27, v32
	v_fmac_f32_e32 v34, v27, v27
	v_mul_f32_e32 v29, v29, v33
	v_fmac_f32_e32 v34, v29, v29
	v_mov_b32_e32 v30, v34
	s_nop 1
	v_permlane32_swap_b32_e32 v30, v34
	s_waitcnt lgkmcnt(0)
	v_add_f32_e32 v30, v34, v30
	v_mov_b32_e32 v31, v30
	s_nop 1
	v_permlane16_swap_b32_e32 v31, v30
	s_waitcnt lgkmcnt(0)
	v_add_f32_e32 v30, v30, v31
	s_nop 1
	v_mov_b32_dpp v31, v30 row_ror:8 row_mask:0xf bank_mask:0xf
	s_waitcnt lgkmcnt(0)
	v_add_f32_e32 v30, v30, v31
	s_nop 1
	v_mov_b32_dpp v31, v30 row_shl:4 row_mask:0xf bank_mask:0x5
	v_mov_b32_dpp v31, v30 row_shr:4 row_mask:0xf bank_mask:0xa
	s_waitcnt lgkmcnt(0)
	v_add_f32_e32 v30, v30, v31
	s_nop 1
	v_mov_b32_dpp v31, v30 quad_perm:[2,3,0,1] row_mask:0xf bank_mask:0xf
	s_waitcnt lgkmcnt(0)
	v_add_f32_e32 v30, v30, v31
	s_nop 1
	v_mov_b32_dpp v31, v30 quad_perm:[1,0,3,2] row_mask:0xf bank_mask:0xf
	s_and_saveexec_b64 s[0:1], vcc
	s_cbranch_execz .LBB0_1282
	s_waitcnt lgkmcnt(0)
	v_add_f32_e32 v30, v30, v31
	v_fmamk_f32 v30, v30, 0x3b000000, v246
	s_mov_b32 s2, 0x800000
	v_cmp_gt_f32_e64 s[2:3], s2, v30
	v_mul_f32_e32 v31, 0x4b800000, v30
	s_nop 0
	v_cndmask_b32_e64 v30, v30, v31, s[2:3]
	v_rsq_f32_e32 v30, v30
	s_nop 0
	v_mul_f32_e32 v31, 0x45800000, v30
	v_cndmask_b32_e64 v38, v30, v31, s[2:3]
	global_load_dwordx4 v[30:33], v[62:63], off offset:16
	global_load_dwordx4 v[34:37], v[62:63], off
	v_mul_f32_e32 v22, v22, v38
	v_mul_f32_e32 v28, v28, v38
	v_mul_f32_e32 v23, v23, v38
	s_waitcnt vmcnt(0)
	v_mul_f32_e32 v22, v22, v36
	v_cvt_pk_bf16_f32 v22, v22, s0
	ds_write_b16 v169, v22 offset:35380
	v_mul_f32_e32 v22, v24, v38
	v_mul_f32_e32 v22, v22, v37
	v_cvt_pk_bf16_f32 v22, v22, s0
	ds_write_b16 v169, v22 offset:35652
	v_mul_f32_e32 v22, v25, v38
	v_mul_f32_e32 v22, v22, v30
	v_cvt_pk_bf16_f32 v22, v22, s0
	ds_write_b16 v169, v22 offset:35924
	v_mul_f32_e32 v22, v26, v38
	v_mul_f32_e32 v22, v22, v31
	v_cvt_pk_bf16_f32 v22, v22, s0
	ds_write_b16 v169, v22 offset:36196
	v_mul_f32_e32 v22, v27, v38
	v_mul_f32_e32 v22, v22, v32
	v_cvt_pk_bf16_f32 v22, v22, s0
	ds_write_b16 v169, v22 offset:36468
	v_mul_f32_e32 v22, v29, v38
	v_mul_f32_e32 v28, v28, v34
	v_mul_f32_e32 v23, v23, v35
	v_mul_f32_e32 v22, v22, v33
	v_cvt_pk_bf16_f32 v28, v28, s0
	v_cvt_pk_bf16_f32 v23, v23, s0
	v_cvt_pk_bf16_f32 v22, v22, s0
	ds_write_b16 v169, v28 offset:34836
	ds_write_b16 v169, v23 offset:35108
	ds_write_b16 v169, v22 offset:36740
; __device__ __forceinline__ float bflo(unsigned w) { return __uint_as_float(w << 16); }
; __device__ __forceinline__ float bfhi(unsigned w) { return __uint_as_float(w & 0xffff0000u); }
; __device__ __forceinline__ unsigned short f2bf(float f) { return (unsigned short)(cvt_pk_bf16(f, 0.f) & 0xffffu); }
; __device__ __forceinline__ void sgu_unit(const Params& p, int l, int un, LAS unsigned char* lds) {
;     ...
;     for (int qi = 0; qi < 16; ++qi) { const int q = wave * 16 + qi;
;         const u32x4 v = vv[qi]; float f[8] = {bflo(v.x), bfhi(v.x), bflo(v.y), bfhi(v.y), bflo(v.z), bfhi(v.z), bflo(v.w), bfhi(v.w)}; float ss = 0.f;
; #pragma unroll
;         for (int j = 0; j < 8; ++j) { f[j] = gelu_tanh(f[j]); ss += f[j] * f[j]; }
;         ss = wave_sum(ss); const float rinv = rsqrtf(ss * (1.0f / 512.0f) + EPS);
;         if ((lane >> 4) == h) { const int c0 = (lane & 15) * 8; const float* g = p.in[I_SGUNG] + l * 512 + h * 128 + c0;
; #pragma unroll
;             for (int j = 0; j < 8; ++j) Vl[(c0 + j) * 136 + q] = f2bf(f[j] * rinv * g[j]); } }
.LBB0_1282:
	s_or_b64 exec, exec, s[0:1]
	s_waitcnt vmcnt(4)
	v_lshlrev_b32_e32 v22, 16, v18
	v_lshlrev_b32_e32 v23, 16, v19
	v_and_b32_e32 v25, 0xffff0000, v19
	v_mul_f32_e32 v19, 0x3dd2d3e8, v22
	v_fma_f32 v19, -v19, v22, s33
	v_mul_f32_e32 v19, v19, v22
	v_exp_f32_e32 v19, v19
	v_and_b32_e32 v18, 0xffff0000, v18
	v_lshlrev_b32_e32 v26, 16, v20
	v_and_b32_e32 v27, 0xffff0000, v20
	v_add_f32_e32 v19, 1.0, v19
	v_rcp_f32_e32 v19, v19
	v_mul_f32_e32 v20, 0x3dd2d3e8, v25
	v_fma_f32 v20, -v20, v25, s33
	v_mul_f32_e32 v20, v20, v25
	v_mul_f32_e32 v24, v19, v22
	v_mul_f32_e32 v19, 0x3dd2d3e8, v18
	v_fma_f32 v19, -v19, v18, s33
	v_mul_f32_e32 v19, v19, v18
	v_exp_f32_e32 v19, v19
	v_exp_f32_e32 v20, v20
	v_lshlrev_b32_e32 v28, 16, v21
	v_and_b32_e32 v29, 0xffff0000, v21
	v_add_f32_e32 v19, 1.0, v19
	v_rcp_f32_e32 v19, v19
	v_add_f32_e32 v20, 1.0, v20
	v_rcp_f32_e32 v20, v20
	v_mul_f32_e32 v21, 0x3dd2d3e8, v26
	v_mul_f32_e32 v19, v19, v18
	v_mul_f32_e32 v18, 0x3dd2d3e8, v23
	v_fma_f32 v18, -v18, v23, s33
	v_mul_f32_e32 v18, v18, v23
	v_exp_f32_e32 v18, v18
	v_fma_f32 v21, -v21, v26, s33
	v_mul_f32_e32 v22, 0x3dd2d3e8, v27
	v_mul_f32_e32 v21, v21, v26
	v_add_f32_e32 v18, 1.0, v18
	v_rcp_f32_e32 v18, v18
	v_fma_f32 v22, -v22, v27, s33
	v_mul_f32_e32 v20, v20, v25
	v_exp_f32_e32 v21, v21
	v_mul_f32_e32 v18, v18, v23
	v_mul_f32_e32 v23, 0x3dd2d3e8, v28
	v_mul_f32_e32 v22, v22, v27
	v_fma_f32 v23, -v23, v28, s33
	v_mul_f32_e32 v25, 0x3dd2d3e8, v29
	v_exp_f32_e32 v22, v22
	v_mul_f32_e32 v23, v23, v28
	v_fma_f32 v25, -v25, v29, s33
	v_exp_f32_e32 v23, v23
	v_mul_f32_e32 v25, v25, v29
	v_exp_f32_e32 v25, v25
	v_add_f32_e32 v21, 1.0, v21
	v_rcp_f32_e32 v21, v21
	v_add_f32_e32 v22, 1.0, v22
	v_mul_f32_e32 v30, v19, v19
	v_rcp_f32_e32 v22, v22
	v_add_f32_e32 v23, 1.0, v23
	v_fmac_f32_e32 v30, v24, v24
	v_rcp_f32_e32 v23, v23
	v_add_f32_e32 v25, 1.0, v25
	v_fmac_f32_e32 v30, v18, v18
	v_rcp_f32_e32 v25, v25
	v_fmac_f32_e32 v30, v20, v20
	v_mul_f32_e32 v21, v21, v26
	v_fmac_f32_e32 v30, v21, v21
	v_mul_f32_e32 v22, v22, v27
	v_fmac_f32_e32 v30, v22, v22
	v_mul_f32_e32 v23, v23, v28
	v_fmac_f32_e32 v30, v23, v23
	v_mul_f32_e32 v25, v25, v29
	v_fmac_f32_e32 v30, v25, v25
	v_mov_b32_e32 v26, v30
	s_nop 1
	v_permlane32_swap_b32_e32 v26, v30
	s_waitcnt lgkmcnt(0)
	v_add_f32_e32 v26, v30, v26
	v_mov_b32_e32 v27, v26
	s_nop 1
	v_permlane16_swap_b32_e32 v27, v26
	s_waitcnt lgkmcnt(0)
	v_add_f32_e32 v26, v26, v27
	s_nop 1
	v_mov_b32_dpp v27, v26 row_ror:8 row_mask:0xf bank_mask:0xf
	s_waitcnt lgkmcnt(0)
	v_add_f32_e32 v26, v26, v27
	s_nop 1
	v_mov_b32_dpp v27, v26 row_shl:4 row_mask:0xf bank_mask:0x5
	v_mov_b32_dpp v27, v26 row_shr:4 row_mask:0xf bank_mask:0xa
	s_waitcnt lgkmcnt(0)
	v_add_f32_e32 v26, v26, v27
	s_nop 1
	v_mov_b32_dpp v27, v26 quad_perm:[2,3,0,1] row_mask:0xf bank_mask:0xf
	s_waitcnt lgkmcnt(0)
	v_add_f32_e32 v26, v26, v27
	s_nop 1
	v_mov_b32_dpp v27, v26 quad_perm:[1,0,3,2] row_mask:0xf bank_mask:0xf
	s_and_saveexec_b64 s[0:1], vcc
	s_cbranch_execz .LBB0_1284
	s_waitcnt lgkmcnt(0)
	v_add_f32_e32 v26, v26, v27
	v_fmamk_f32 v26, v26, 0x3b000000, v246
	s_mov_b32 s2, 0x800000
	v_cmp_gt_f32_e64 s[2:3], s2, v26
	v_mul_f32_e32 v27, 0x4b800000, v26
	s_nop 0
	v_cndmask_b32_e64 v26, v26, v27, s[2:3]
	v_rsq_f32_e32 v26, v26
	s_nop 0
	v_mul_f32_e32 v27, 0x45800000, v26
	v_cndmask_b32_e64 v34, v26, v27, s[2:3]
	global_load_dwordx4 v[26:29], v[62:63], off offset:16
	global_load_dwordx4 v[30:33], v[62:63], off
	v_mul_f32_e32 v18, v18, v34
	v_mul_f32_e32 v24, v24, v34
	v_mul_f32_e32 v19, v19, v34
	s_waitcnt vmcnt(0)
	v_mul_f32_e32 v18, v18, v32
	v_cvt_pk_bf16_f32 v18, v18, s0
	ds_write_b16 v169, v18 offset:35382
	v_mul_f32_e32 v18, v20, v34
	v_mul_f32_e32 v18, v18, v33
	v_cvt_pk_bf16_f32 v18, v18, s0
	ds_write_b16 v169, v18 offset:35654
	v_mul_f32_e32 v18, v21, v34
	v_mul_f32_e32 v18, v18, v26
	v_cvt_pk_bf16_f32 v18, v18, s0
	ds_write_b16 v169, v18 offset:35926
	v_mul_f32_e32 v18, v22, v34
	v_mul_f32_e32 v18, v18, v27
	v_cvt_pk_bf16_f32 v18, v18, s0
	ds_write_b16 v169, v18 offset:36198
	v_mul_f32_e32 v18, v23, v34
	v_mul_f32_e32 v18, v18, v28
	v_cvt_pk_bf16_f32 v18, v18, s0
	ds_write_b16 v169, v18 offset:36470
	v_mul_f32_e32 v18, v25, v34
	v_mul_f32_e32 v24, v24, v30
	v_mul_f32_e32 v19, v19, v31
	v_mul_f32_e32 v18, v18, v29
	v_cvt_pk_bf16_f32 v24, v24, s0
	v_cvt_pk_bf16_f32 v19, v19, s0
	v_cvt_pk_bf16_f32 v18, v18, s0
	ds_write_b16 v169, v24 offset:34838
	ds_write_b16 v169, v19 offset:35110
	ds_write_b16 v169, v18 offset:36742
; __device__ __forceinline__ float bflo(unsigned w) { return __uint_as_float(w << 16); }
; __device__ __forceinline__ float bfhi(unsigned w) { return __uint_as_float(w & 0xffff0000u); }
; __device__ __forceinline__ unsigned short f2bf(float f) { return (unsigned short)(cvt_pk_bf16(f, 0.f) & 0xffffu); }
; __device__ __forceinline__ void sgu_unit(const Params& p, int l, int un, LAS unsigned char* lds) {
;     ...
;     for (int qi = 0; qi < 16; ++qi) { const int q = wave * 16 + qi;
;         const u32x4 v = vv[qi]; float f[8] = {bflo(v.x), bfhi(v.x), bflo(v.y), bfhi(v.y), bflo(v.z), bfhi(v.z), bflo(v.w), bfhi(v.w)}; float ss = 0.f;
; #pragma unroll
;         for (int j = 0; j < 8; ++j) { f[j] = gelu_tanh(f[j]); ss += f[j] * f[j]; }
;         ss = wave_sum(ss); const float rinv = rsqrtf(ss * (1.0f / 512.0f) + EPS);
;         if ((lane >> 4) == h) { const int c0 = (lane & 15) * 8; const float* g = p.in[I_SGUNG] + l * 512 + h * 128 + c0;
; #pragma unroll
;             for (int j = 0; j < 8; ++j) Vl[(c0 + j) * 136 + q] = f2bf(f[j] * rinv * g[j]); } }
.LBB0_1284:
	s_or_b64 exec, exec, s[0:1]
	s_waitcnt vmcnt(3)
	v_lshlrev_b32_e32 v18, 16, v14
	v_lshlrev_b32_e32 v19, 16, v15
	v_and_b32_e32 v21, 0xffff0000, v15
	v_mul_f32_e32 v15, 0x3dd2d3e8, v18
	v_fma_f32 v15, -v15, v18, s33
	v_mul_f32_e32 v15, v15, v18
	v_exp_f32_e32 v15, v15
	v_and_b32_e32 v14, 0xffff0000, v14
	v_lshlrev_b32_e32 v22, 16, v16
	v_and_b32_e32 v23, 0xffff0000, v16
	v_add_f32_e32 v15, 1.0, v15
	v_rcp_f32_e32 v15, v15
	v_mul_f32_e32 v16, 0x3dd2d3e8, v21
	v_fma_f32 v16, -v16, v21, s33
	v_mul_f32_e32 v16, v16, v21
	v_mul_f32_e32 v20, v15, v18
	v_mul_f32_e32 v15, 0x3dd2d3e8, v14
	v_fma_f32 v15, -v15, v14, s33
	v_mul_f32_e32 v15, v15, v14
	v_exp_f32_e32 v15, v15
	v_exp_f32_e32 v16, v16
	v_lshlrev_b32_e32 v24, 16, v17
	v_and_b32_e32 v25, 0xffff0000, v17
	v_add_f32_e32 v15, 1.0, v15
	v_rcp_f32_e32 v15, v15
	v_add_f32_e32 v16, 1.0, v16
	v_rcp_f32_e32 v16, v16
	v_mul_f32_e32 v17, 0x3dd2d3e8, v22
	v_mul_f32_e32 v15, v15, v14
	v_mul_f32_e32 v14, 0x3dd2d3e8, v19
	v_fma_f32 v14, -v14, v19, s33
	v_mul_f32_e32 v14, v14, v19
	v_exp_f32_e32 v14, v14
	v_fma_f32 v17, -v17, v22, s33
	v_mul_f32_e32 v18, 0x3dd2d3e8, v23
	v_mul_f32_e32 v17, v17, v22
	v_add_f32_e32 v14, 1.0, v14
	v_rcp_f32_e32 v14, v14
	v_fma_f32 v18, -v18, v23, s33
	v_mul_f32_e32 v16, v16, v21
	v_exp_f32_e32 v17, v17
	v_mul_f32_e32 v14, v14, v19
	v_mul_f32_e32 v19, 0x3dd2d3e8, v24
	v_mul_f32_e32 v18, v18, v23
	v_fma_f32 v19, -v19, v24, s33
	v_mul_f32_e32 v21, 0x3dd2d3e8, v25
	v_exp_f32_e32 v18, v18
	v_mul_f32_e32 v19, v19, v24
	v_fma_f32 v21, -v21, v25, s33
	v_exp_f32_e32 v19, v19
	v_mul_f32_e32 v21, v21, v25
	v_exp_f32_e32 v21, v21
	v_add_f32_e32 v17, 1.0, v17
	v_rcp_f32_e32 v17, v17
	v_add_f32_e32 v18, 1.0, v18
	v_mul_f32_e32 v26, v15, v15
	v_rcp_f32_e32 v18, v18
	v_add_f32_e32 v19, 1.0, v19
	v_fmac_f32_e32 v26, v20, v20
	v_rcp_f32_e32 v19, v19
	v_add_f32_e32 v21, 1.0, v21
	v_fmac_f32_e32 v26, v14, v14
	v_rcp_f32_e32 v21, v21
	v_fmac_f32_e32 v26, v16, v16
	v_mul_f32_e32 v17, v17, v22
	v_fmac_f32_e32 v26, v17, v17
	v_mul_f32_e32 v18, v18, v23
	v_fmac_f32_e32 v26, v18, v18
	v_mul_f32_e32 v19, v19, v24
	v_fmac_f32_e32 v26, v19, v19
	v_mul_f32_e32 v21, v21, v25
	v_fmac_f32_e32 v26, v21, v21
	v_mov_b32_e32 v22, v26
	s_nop 1
	v_permlane32_swap_b32_e32 v22, v26
	s_waitcnt lgkmcnt(0)
	v_add_f32_e32 v22, v26, v22
	v_mov_b32_e32 v23, v22
	s_nop 1
	v_permlane16_swap_b32_e32 v23, v22
	s_waitcnt lgkmcnt(0)
	v_add_f32_e32 v22, v22, v23
	s_nop 1
	v_mov_b32_dpp v23, v22 row_ror:8 row_mask:0xf bank_mask:0xf
	s_waitcnt lgkmcnt(0)
	v_add_f32_e32 v22, v22, v23
	s_nop 1
	v_mov_b32_dpp v23, v22 row_shl:4 row_mask:0xf bank_mask:0x5
	v_mov_b32_dpp v23, v22 row_shr:4 row_mask:0xf bank_mask:0xa
	s_waitcnt lgkmcnt(0)
	v_add_f32_e32 v22, v22, v23
	s_nop 1
	v_mov_b32_dpp v23, v22 quad_perm:[2,3,0,1] row_mask:0xf bank_mask:0xf
	s_waitcnt lgkmcnt(0)
	v_add_f32_e32 v22, v22, v23
	s_nop 1
	v_mov_b32_dpp v23, v22 quad_perm:[1,0,3,2] row_mask:0xf bank_mask:0xf
	s_and_saveexec_b64 s[0:1], vcc
	s_cbranch_execz .LBB0_1286
	s_waitcnt lgkmcnt(0)
	v_add_f32_e32 v22, v22, v23
	v_fmamk_f32 v22, v22, 0x3b000000, v246
	s_mov_b32 s2, 0x800000
	v_cmp_gt_f32_e64 s[2:3], s2, v22
	v_mul_f32_e32 v23, 0x4b800000, v22
	s_nop 0
	v_cndmask_b32_e64 v22, v22, v23, s[2:3]
	v_rsq_f32_e32 v22, v22
	s_nop 0
	v_mul_f32_e32 v23, 0x45800000, v22
	v_cndmask_b32_e64 v30, v22, v23, s[2:3]
	global_load_dwordx4 v[22:25], v[62:63], off offset:16
	global_load_dwordx4 v[26:29], v[62:63], off
	v_mul_f32_e32 v14, v14, v30
	v_mul_f32_e32 v20, v20, v30
	v_mul_f32_e32 v15, v15, v30
	s_waitcnt vmcnt(0)
	v_mul_f32_e32 v14, v14, v28
	v_cvt_pk_bf16_f32 v14, v14, s0
	ds_write_b16 v169, v14 offset:35384
	v_mul_f32_e32 v14, v16, v30
	v_mul_f32_e32 v14, v14, v29
	v_cvt_pk_bf16_f32 v14, v14, s0
	ds_write_b16 v169, v14 offset:35656
	v_mul_f32_e32 v14, v17, v30
	v_mul_f32_e32 v14, v14, v22
	v_cvt_pk_bf16_f32 v14, v14, s0
	ds_write_b16 v169, v14 offset:35928
	v_mul_f32_e32 v14, v18, v30
	v_mul_f32_e32 v14, v14, v23
	v_cvt_pk_bf16_f32 v14, v14, s0
	ds_write_b16 v169, v14 offset:36200
	v_mul_f32_e32 v14, v19, v30
	v_mul_f32_e32 v14, v14, v24
	v_cvt_pk_bf16_f32 v14, v14, s0
	ds_write_b16 v169, v14 offset:36472
	v_mul_f32_e32 v14, v21, v30
	v_mul_f32_e32 v20, v20, v26
	v_mul_f32_e32 v15, v15, v27
	v_mul_f32_e32 v14, v14, v25
	v_cvt_pk_bf16_f32 v20, v20, s0
	v_cvt_pk_bf16_f32 v15, v15, s0
	v_cvt_pk_bf16_f32 v14, v14, s0
	ds_write_b16 v169, v20 offset:34840
	ds_write_b16 v169, v15 offset:35112
	ds_write_b16 v169, v14 offset:36744
; __device__ __forceinline__ float bflo(unsigned w) { return __uint_as_float(w << 16); }
; __device__ __forceinline__ float bfhi(unsigned w) { return __uint_as_float(w & 0xffff0000u); }
; __device__ __forceinline__ unsigned short f2bf(float f) { return (unsigned short)(cvt_pk_bf16(f, 0.f) & 0xffffu); }
; __device__ __forceinline__ void sgu_unit(const Params& p, int l, int un, LAS unsigned char* lds) {
;     ...
;     for (int qi = 0; qi < 16; ++qi) { const int q = wave * 16 + qi;
;         const u32x4 v = vv[qi]; float f[8] = {bflo(v.x), bfhi(v.x), bflo(v.y), bfhi(v.y), bflo(v.z), bfhi(v.z), bflo(v.w), bfhi(v.w)}; float ss = 0.f;
; #pragma unroll
;         for (int j = 0; j < 8; ++j) { f[j] = gelu_tanh(f[j]); ss += f[j] * f[j]; }
;         ss = wave_sum(ss); const float rinv = rsqrtf(ss * (1.0f / 512.0f) + EPS);
;         if ((lane >> 4) == h) { const int c0 = (lane & 15) * 8; const float* g = p.in[I_SGUNG] + l * 512 + h * 128 + c0;
; #pragma unroll
;             for (int j = 0; j < 8; ++j) Vl[(c0 + j) * 136 + q] = f2bf(f[j] * rinv * g[j]); } }
.LBB0_1286:
	s_or_b64 exec, exec, s[0:1]
	s_waitcnt vmcnt(2)
	v_lshlrev_b32_e32 v14, 16, v10
	v_lshlrev_b32_e32 v15, 16, v11
	v_and_b32_e32 v17, 0xffff0000, v11
	v_mul_f32_e32 v11, 0x3dd2d3e8, v14
	v_fma_f32 v11, -v11, v14, s33
	v_mul_f32_e32 v11, v11, v14
	v_exp_f32_e32 v11, v11
	v_and_b32_e32 v10, 0xffff0000, v10
	v_lshlrev_b32_e32 v18, 16, v12
	v_and_b32_e32 v19, 0xffff0000, v12
	v_add_f32_e32 v11, 1.0, v11
	v_rcp_f32_e32 v11, v11
	v_mul_f32_e32 v12, 0x3dd2d3e8, v17
	v_fma_f32 v12, -v12, v17, s33
	v_mul_f32_e32 v12, v12, v17
	v_mul_f32_e32 v16, v11, v14
	v_mul_f32_e32 v11, 0x3dd2d3e8, v10
	v_fma_f32 v11, -v11, v10, s33
	v_mul_f32_e32 v11, v11, v10
	v_exp_f32_e32 v11, v11
	v_exp_f32_e32 v12, v12
	v_lshlrev_b32_e32 v20, 16, v13
	v_and_b32_e32 v21, 0xffff0000, v13
	v_add_f32_e32 v11, 1.0, v11
	v_rcp_f32_e32 v11, v11
	v_add_f32_e32 v12, 1.0, v12
	v_rcp_f32_e32 v12, v12
	v_mul_f32_e32 v13, 0x3dd2d3e8, v18
	v_mul_f32_e32 v11, v11, v10
	v_mul_f32_e32 v10, 0x3dd2d3e8, v15
	v_fma_f32 v10, -v10, v15, s33
	v_mul_f32_e32 v10, v10, v15
	v_exp_f32_e32 v10, v10
	v_fma_f32 v13, -v13, v18, s33
	v_mul_f32_e32 v14, 0x3dd2d3e8, v19
	v_mul_f32_e32 v13, v13, v18
	v_add_f32_e32 v10, 1.0, v10
	v_rcp_f32_e32 v10, v10
	v_fma_f32 v14, -v14, v19, s33
	v_mul_f32_e32 v12, v12, v17
	v_exp_f32_e32 v13, v13
	v_mul_f32_e32 v10, v10, v15
	v_mul_f32_e32 v15, 0x3dd2d3e8, v20
	v_mul_f32_e32 v14, v14, v19
	v_fma_f32 v15, -v15, v20, s33
	v_mul_f32_e32 v17, 0x3dd2d3e8, v21
	v_exp_f32_e32 v14, v14
	v_mul_f32_e32 v15, v15, v20
	v_fma_f32 v17, -v17, v21, s33
	v_exp_f32_e32 v15, v15
	v_mul_f32_e32 v17, v17, v21
	v_exp_f32_e32 v17, v17
	v_add_f32_e32 v13, 1.0, v13
	v_rcp_f32_e32 v13, v13
	v_add_f32_e32 v14, 1.0, v14
	v_mul_f32_e32 v22, v11, v11
	v_rcp_f32_e32 v14, v14
	v_add_f32_e32 v15, 1.0, v15
	v_fmac_f32_e32 v22, v16, v16
	v_rcp_f32_e32 v15, v15
	v_add_f32_e32 v17, 1.0, v17
	v_fmac_f32_e32 v22, v10, v10
	v_rcp_f32_e32 v17, v17
	v_fmac_f32_e32 v22, v12, v12
	v_mul_f32_e32 v13, v13, v18
	v_fmac_f32_e32 v22, v13, v13
	v_mul_f32_e32 v14, v14, v19
	v_fmac_f32_e32 v22, v14, v14
	v_mul_f32_e32 v15, v15, v20
	v_fmac_f32_e32 v22, v15, v15
	v_mul_f32_e32 v17, v17, v21
	v_fmac_f32_e32 v22, v17, v17
	v_mov_b32_e32 v18, v22
	s_nop 1
	v_permlane32_swap_b32_e32 v18, v22
	s_waitcnt lgkmcnt(0)
	v_add_f32_e32 v18, v22, v18
	v_mov_b32_e32 v19, v18
	s_nop 1
	v_permlane16_swap_b32_e32 v19, v18
	s_waitcnt lgkmcnt(0)
	v_add_f32_e32 v18, v18, v19
	s_nop 1
	v_mov_b32_dpp v19, v18 row_ror:8 row_mask:0xf bank_mask:0xf
	s_waitcnt lgkmcnt(0)
	v_add_f32_e32 v18, v18, v19
	s_nop 1
	v_mov_b32_dpp v19, v18 row_shl:4 row_mask:0xf bank_mask:0x5
	v_mov_b32_dpp v19, v18 row_shr:4 row_mask:0xf bank_mask:0xa
	s_waitcnt lgkmcnt(0)
	v_add_f32_e32 v18, v18, v19
	s_nop 1
	v_mov_b32_dpp v19, v18 quad_perm:[2,3,0,1] row_mask:0xf bank_mask:0xf
	s_waitcnt lgkmcnt(0)
	v_add_f32_e32 v18, v18, v19
	s_nop 1
	v_mov_b32_dpp v19, v18 quad_perm:[1,0,3,2] row_mask:0xf bank_mask:0xf
	s_and_saveexec_b64 s[0:1], vcc
	s_cbranch_execz .LBB0_1288
	s_waitcnt lgkmcnt(0)
	v_add_f32_e32 v18, v18, v19
	v_fmamk_f32 v18, v18, 0x3b000000, v246
	s_mov_b32 s2, 0x800000
	v_cmp_gt_f32_e64 s[2:3], s2, v18
	v_mul_f32_e32 v19, 0x4b800000, v18
	s_nop 0
	v_cndmask_b32_e64 v18, v18, v19, s[2:3]
	v_rsq_f32_e32 v18, v18
	s_nop 0
	v_mul_f32_e32 v19, 0x45800000, v18
	v_cndmask_b32_e64 v26, v18, v19, s[2:3]
	global_load_dwordx4 v[18:21], v[62:63], off offset:16
	global_load_dwordx4 v[22:25], v[62:63], off
	v_mul_f32_e32 v10, v10, v26
	v_mul_f32_e32 v16, v16, v26
	v_mul_f32_e32 v11, v11, v26
	s_waitcnt vmcnt(0)
	v_mul_f32_e32 v10, v10, v24
	v_cvt_pk_bf16_f32 v10, v10, s0
	ds_write_b16 v169, v10 offset:35386
	v_mul_f32_e32 v10, v12, v26
	v_mul_f32_e32 v10, v10, v25
	v_cvt_pk_bf16_f32 v10, v10, s0
	ds_write_b16 v169, v10 offset:35658
	v_mul_f32_e32 v10, v13, v26
	v_mul_f32_e32 v10, v10, v18
	v_cvt_pk_bf16_f32 v10, v10, s0
	ds_write_b16 v169, v10 offset:35930
	v_mul_f32_e32 v10, v14, v26
	v_mul_f32_e32 v10, v10, v19
	v_cvt_pk_bf16_f32 v10, v10, s0
	ds_write_b16 v169, v10 offset:36202
	v_mul_f32_e32 v10, v15, v26
	v_mul_f32_e32 v10, v10, v20
	v_cvt_pk_bf16_f32 v10, v10, s0
	ds_write_b16 v169, v10 offset:36474
	v_mul_f32_e32 v10, v17, v26
	v_mul_f32_e32 v16, v16, v22
	v_mul_f32_e32 v11, v11, v23
	v_mul_f32_e32 v10, v10, v21
	v_cvt_pk_bf16_f32 v16, v16, s0
	v_cvt_pk_bf16_f32 v11, v11, s0
	v_cvt_pk_bf16_f32 v10, v10, s0
	ds_write_b16 v169, v16 offset:34842
	ds_write_b16 v169, v11 offset:35114
	ds_write_b16 v169, v10 offset:36746
; __device__ __forceinline__ float bflo(unsigned w) { return __uint_as_float(w << 16); }
; __device__ __forceinline__ float bfhi(unsigned w) { return __uint_as_float(w & 0xffff0000u); }
; __device__ __forceinline__ unsigned short f2bf(float f) { return (unsigned short)(cvt_pk_bf16(f, 0.f) & 0xffffu); }
; __device__ __forceinline__ void sgu_unit(const Params& p, int l, int un, LAS unsigned char* lds) {
;     ...
;     for (int qi = 0; qi < 16; ++qi) { const int q = wave * 16 + qi;
;         const u32x4 v = vv[qi]; float f[8] = {bflo(v.x), bfhi(v.x), bflo(v.y), bfhi(v.y), bflo(v.z), bfhi(v.z), bflo(v.w), bfhi(v.w)}; float ss = 0.f;
; #pragma unroll
;         for (int j = 0; j < 8; ++j) { f[j] = gelu_tanh(f[j]); ss += f[j] * f[j]; }
;         ss = wave_sum(ss); const float rinv = rsqrtf(ss * (1.0f / 512.0f) + EPS);
;         if ((lane >> 4) == h) { const int c0 = (lane & 15) * 8; const float* g = p.in[I_SGUNG] + l * 512 + h * 128 + c0;
; #pragma unroll
;             for (int j = 0; j < 8; ++j) Vl[(c0 + j) * 136 + q] = f2bf(f[j] * rinv * g[j]); } }
.LBB0_1288:
	s_or_b64 exec, exec, s[0:1]
	s_waitcnt vmcnt(1)
	v_lshlrev_b32_e32 v10, 16, v6
	v_lshlrev_b32_e32 v11, 16, v7
	v_and_b32_e32 v13, 0xffff0000, v7
	v_mul_f32_e32 v7, 0x3dd2d3e8, v10
	v_fma_f32 v7, -v7, v10, s33
	v_mul_f32_e32 v7, v7, v10
	v_exp_f32_e32 v7, v7
	v_and_b32_e32 v6, 0xffff0000, v6
	v_lshlrev_b32_e32 v14, 16, v8
	v_and_b32_e32 v15, 0xffff0000, v8
	v_add_f32_e32 v7, 1.0, v7
	v_rcp_f32_e32 v7, v7
	v_mul_f32_e32 v8, 0x3dd2d3e8, v13
	v_fma_f32 v8, -v8, v13, s33
	v_mul_f32_e32 v8, v8, v13
	v_mul_f32_e32 v12, v7, v10
	v_mul_f32_e32 v7, 0x3dd2d3e8, v6
	v_fma_f32 v7, -v7, v6, s33
	v_mul_f32_e32 v7, v7, v6
	v_exp_f32_e32 v7, v7
	v_exp_f32_e32 v8, v8
	v_lshlrev_b32_e32 v16, 16, v9
	v_and_b32_e32 v17, 0xffff0000, v9
	v_add_f32_e32 v7, 1.0, v7
	v_rcp_f32_e32 v7, v7
	v_add_f32_e32 v8, 1.0, v8
	v_rcp_f32_e32 v8, v8
	v_mul_f32_e32 v9, 0x3dd2d3e8, v14
	v_mul_f32_e32 v7, v7, v6
	v_mul_f32_e32 v6, 0x3dd2d3e8, v11
	v_fma_f32 v6, -v6, v11, s33
	v_mul_f32_e32 v6, v6, v11
	v_exp_f32_e32 v6, v6
	v_fma_f32 v9, -v9, v14, s33
	v_mul_f32_e32 v10, 0x3dd2d3e8, v15
	v_mul_f32_e32 v9, v9, v14
	v_add_f32_e32 v6, 1.0, v6
	v_rcp_f32_e32 v6, v6
	v_fma_f32 v10, -v10, v15, s33
	v_mul_f32_e32 v8, v8, v13
	v_exp_f32_e32 v9, v9
	v_mul_f32_e32 v6, v6, v11
	v_mul_f32_e32 v11, 0x3dd2d3e8, v16
	v_mul_f32_e32 v10, v10, v15
	v_fma_f32 v11, -v11, v16, s33
	v_mul_f32_e32 v13, 0x3dd2d3e8, v17
	v_exp_f32_e32 v10, v10
	v_mul_f32_e32 v11, v11, v16
	v_fma_f32 v13, -v13, v17, s33
	v_exp_f32_e32 v11, v11
	v_mul_f32_e32 v13, v13, v17
	v_exp_f32_e32 v13, v13
	v_add_f32_e32 v9, 1.0, v9
	v_rcp_f32_e32 v9, v9
	v_add_f32_e32 v10, 1.0, v10
	v_mul_f32_e32 v18, v7, v7
	v_rcp_f32_e32 v10, v10
	v_add_f32_e32 v11, 1.0, v11
	v_fmac_f32_e32 v18, v12, v12
	v_rcp_f32_e32 v11, v11
	v_add_f32_e32 v13, 1.0, v13
	v_fmac_f32_e32 v18, v6, v6
	v_rcp_f32_e32 v13, v13
	v_fmac_f32_e32 v18, v8, v8
	v_mul_f32_e32 v9, v9, v14
	v_fmac_f32_e32 v18, v9, v9
	v_mul_f32_e32 v10, v10, v15
	v_fmac_f32_e32 v18, v10, v10
	v_mul_f32_e32 v11, v11, v16
	v_fmac_f32_e32 v18, v11, v11
	v_mul_f32_e32 v13, v13, v17
	v_fmac_f32_e32 v18, v13, v13
	v_mov_b32_e32 v14, v18
	s_nop 1
	v_permlane32_swap_b32_e32 v14, v18
	s_waitcnt lgkmcnt(0)
	v_add_f32_e32 v14, v18, v14
	v_mov_b32_e32 v15, v14
	s_nop 1
	v_permlane16_swap_b32_e32 v15, v14
	s_waitcnt lgkmcnt(0)
	v_add_f32_e32 v14, v14, v15
	s_nop 1
	v_mov_b32_dpp v15, v14 row_ror:8 row_mask:0xf bank_mask:0xf
	s_waitcnt lgkmcnt(0)
	v_add_f32_e32 v14, v14, v15
	s_nop 1
	v_mov_b32_dpp v15, v14 row_shl:4 row_mask:0xf bank_mask:0x5
	v_mov_b32_dpp v15, v14 row_shr:4 row_mask:0xf bank_mask:0xa
	s_waitcnt lgkmcnt(0)
	v_add_f32_e32 v14, v14, v15
	s_nop 1
	v_mov_b32_dpp v15, v14 quad_perm:[2,3,0,1] row_mask:0xf bank_mask:0xf
	s_waitcnt lgkmcnt(0)
	v_add_f32_e32 v14, v14, v15
	s_nop 1
	v_mov_b32_dpp v15, v14 quad_perm:[1,0,3,2] row_mask:0xf bank_mask:0xf
	s_and_saveexec_b64 s[0:1], vcc
	s_cbranch_execz .LBB0_1290
	s_waitcnt lgkmcnt(0)
	v_add_f32_e32 v14, v14, v15
	v_fmamk_f32 v14, v14, 0x3b000000, v246
	s_mov_b32 s2, 0x800000
	v_cmp_gt_f32_e64 s[2:3], s2, v14
	v_mul_f32_e32 v15, 0x4b800000, v14
	s_nop 0
	v_cndmask_b32_e64 v14, v14, v15, s[2:3]
	v_rsq_f32_e32 v14, v14
	s_nop 0
	v_mul_f32_e32 v15, 0x45800000, v14
	v_cndmask_b32_e64 v22, v14, v15, s[2:3]
	global_load_dwordx4 v[14:17], v[62:63], off offset:16
	global_load_dwordx4 v[18:21], v[62:63], off
	v_mul_f32_e32 v6, v6, v22
	v_mul_f32_e32 v12, v12, v22
	v_mul_f32_e32 v7, v7, v22
	s_waitcnt vmcnt(0)
	v_mul_f32_e32 v6, v6, v20
	v_cvt_pk_bf16_f32 v6, v6, s0
	ds_write_b16 v169, v6 offset:35388
	v_mul_f32_e32 v6, v8, v22
	v_mul_f32_e32 v6, v6, v21
	v_cvt_pk_bf16_f32 v6, v6, s0
	ds_write_b16 v169, v6 offset:35660
	v_mul_f32_e32 v6, v9, v22
	v_mul_f32_e32 v6, v6, v14
	v_cvt_pk_bf16_f32 v6, v6, s0
	ds_write_b16 v169, v6 offset:35932
	v_mul_f32_e32 v6, v10, v22
	v_mul_f32_e32 v6, v6, v15
	v_cvt_pk_bf16_f32 v6, v6, s0
	ds_write_b16 v169, v6 offset:36204
	v_mul_f32_e32 v6, v11, v22
	v_mul_f32_e32 v6, v6, v16
	v_cvt_pk_bf16_f32 v6, v6, s0
	ds_write_b16 v169, v6 offset:36476
	v_mul_f32_e32 v6, v13, v22
	v_mul_f32_e32 v12, v12, v18
	v_mul_f32_e32 v7, v7, v19
	v_mul_f32_e32 v6, v6, v17
	v_cvt_pk_bf16_f32 v12, v12, s0
	v_cvt_pk_bf16_f32 v7, v7, s0
	v_cvt_pk_bf16_f32 v6, v6, s0
	ds_write_b16 v169, v12 offset:34844
	ds_write_b16 v169, v7 offset:35116
	ds_write_b16 v169, v6 offset:36748
; __device__ __forceinline__ float bflo(unsigned w) { return __uint_as_float(w << 16); }
; __device__ __forceinline__ float bfhi(unsigned w) { return __uint_as_float(w & 0xffff0000u); }
; __device__ __forceinline__ unsigned short f2bf(float f) { return (unsigned short)(cvt_pk_bf16(f, 0.f) & 0xffffu); }
; __device__ __forceinline__ void sgu_unit(const Params& p, int l, int un, LAS unsigned char* lds) {
;     ...
;     for (int qi = 0; qi < 16; ++qi) { const int q = wave * 16 + qi;
;         const u32x4 v = vv[qi]; float f[8] = {bflo(v.x), bfhi(v.x), bflo(v.y), bfhi(v.y), bflo(v.z), bfhi(v.z), bflo(v.w), bfhi(v.w)}; float ss = 0.f;
; #pragma unroll
;         for (int j = 0; j < 8; ++j) { f[j] = gelu_tanh(f[j]); ss += f[j] * f[j]; }
;         ss = wave_sum(ss); const float rinv = rsqrtf(ss * (1.0f / 512.0f) + EPS);
;         if ((lane >> 4) == h) { const int c0 = (lane & 15) * 8; const float* g = p.in[I_SGUNG] + l * 512 + h * 128 + c0;
; #pragma unroll
;             for (int j = 0; j < 8; ++j) Vl[(c0 + j) * 136 + q] = f2bf(f[j] * rinv * g[j]); } }
.LBB0_1290:
	s_or_b64 exec, exec, s[0:1]
	s_waitcnt vmcnt(0)
	v_lshlrev_b32_e32 v6, 16, v2
	v_lshlrev_b32_e32 v7, 16, v3
	v_and_b32_e32 v9, 0xffff0000, v3
	v_mul_f32_e32 v3, 0x3dd2d3e8, v6
	v_fma_f32 v3, -v3, v6, s33
	v_mul_f32_e32 v3, v3, v6
	v_exp_f32_e32 v3, v3
	v_and_b32_e32 v2, 0xffff0000, v2
	v_lshlrev_b32_e32 v10, 16, v4
	v_and_b32_e32 v11, 0xffff0000, v4
	v_add_f32_e32 v3, 1.0, v3
	v_rcp_f32_e32 v3, v3
	v_mul_f32_e32 v4, 0x3dd2d3e8, v9
	v_fma_f32 v4, -v4, v9, s33
	v_mul_f32_e32 v4, v4, v9
	v_mul_f32_e32 v8, v3, v6
	v_mul_f32_e32 v3, 0x3dd2d3e8, v2
	v_fma_f32 v3, -v3, v2, s33
	v_mul_f32_e32 v3, v3, v2
	v_exp_f32_e32 v3, v3
	v_exp_f32_e32 v4, v4
	v_lshlrev_b32_e32 v12, 16, v5
	v_and_b32_e32 v13, 0xffff0000, v5
	v_add_f32_e32 v3, 1.0, v3
	v_rcp_f32_e32 v3, v3
	v_add_f32_e32 v4, 1.0, v4
	v_rcp_f32_e32 v4, v4
	v_mul_f32_e32 v5, 0x3dd2d3e8, v10
	v_mul_f32_e32 v3, v3, v2
	v_mul_f32_e32 v2, 0x3dd2d3e8, v7
	v_fma_f32 v2, -v2, v7, s33
	v_mul_f32_e32 v2, v2, v7
	v_exp_f32_e32 v2, v2
	v_fma_f32 v5, -v5, v10, s33
	v_mul_f32_e32 v6, 0x3dd2d3e8, v11
	v_mul_f32_e32 v5, v5, v10
	v_add_f32_e32 v2, 1.0, v2
	v_rcp_f32_e32 v2, v2
	v_fma_f32 v6, -v6, v11, s33
	v_mul_f32_e32 v4, v4, v9
	v_exp_f32_e32 v5, v5
	v_mul_f32_e32 v2, v2, v7
	v_mul_f32_e32 v7, 0x3dd2d3e8, v12
	v_mul_f32_e32 v6, v6, v11
	v_fma_f32 v7, -v7, v12, s33
	v_mul_f32_e32 v9, 0x3dd2d3e8, v13
	v_exp_f32_e32 v6, v6
	v_mul_f32_e32 v7, v7, v12
	v_fma_f32 v9, -v9, v13, s33
	v_exp_f32_e32 v7, v7
	v_mul_f32_e32 v9, v9, v13
	v_exp_f32_e32 v9, v9
	v_add_f32_e32 v5, 1.0, v5
	v_rcp_f32_e32 v5, v5
	v_add_f32_e32 v6, 1.0, v6
	v_mul_f32_e32 v14, v3, v3
	v_rcp_f32_e32 v6, v6
	v_add_f32_e32 v7, 1.0, v7
	v_fmac_f32_e32 v14, v8, v8
	v_rcp_f32_e32 v7, v7
	v_add_f32_e32 v9, 1.0, v9
	v_fmac_f32_e32 v14, v2, v2
	v_rcp_f32_e32 v9, v9
	v_fmac_f32_e32 v14, v4, v4
	v_mul_f32_e32 v5, v5, v10
	v_fmac_f32_e32 v14, v5, v5
	v_mul_f32_e32 v6, v6, v11
	v_fmac_f32_e32 v14, v6, v6
	v_mul_f32_e32 v7, v7, v12
	v_fmac_f32_e32 v14, v7, v7
	v_mul_f32_e32 v9, v9, v13
	v_fmac_f32_e32 v14, v9, v9
	v_mov_b32_e32 v10, v14
	s_nop 1
	v_permlane32_swap_b32_e32 v10, v14
	s_waitcnt lgkmcnt(0)
	v_add_f32_e32 v10, v14, v10
	v_mov_b32_e32 v11, v10
	s_nop 1
	v_permlane16_swap_b32_e32 v11, v10
	s_waitcnt lgkmcnt(0)
	v_add_f32_e32 v10, v10, v11
	s_nop 1
	v_mov_b32_dpp v11, v10 row_ror:8 row_mask:0xf bank_mask:0xf
	s_waitcnt lgkmcnt(0)
	v_add_f32_e32 v10, v10, v11
	s_nop 1
	v_mov_b32_dpp v11, v10 row_shl:4 row_mask:0xf bank_mask:0x5
	v_mov_b32_dpp v11, v10 row_shr:4 row_mask:0xf bank_mask:0xa
	s_waitcnt lgkmcnt(0)
	v_add_f32_e32 v10, v10, v11
	s_nop 1
	v_mov_b32_dpp v11, v10 quad_perm:[2,3,0,1] row_mask:0xf bank_mask:0xf
	s_waitcnt lgkmcnt(0)
	v_add_f32_e32 v10, v10, v11
	s_nop 1
	v_mov_b32_dpp v11, v10 quad_perm:[1,0,3,2] row_mask:0xf bank_mask:0xf
	s_and_saveexec_b64 s[0:1], vcc
	s_cbranch_execz .LBB0_1292
	s_waitcnt lgkmcnt(0)
	v_add_f32_e32 v10, v10, v11
	v_fmamk_f32 v10, v10, 0x3b000000, v246
	s_mov_b32 s2, 0x800000
	v_cmp_gt_f32_e32 vcc, s2, v10
	v_mul_f32_e32 v11, 0x4b800000, v10
	s_nop 0
	v_cndmask_b32_e32 v10, v10, v11, vcc
	v_rsq_f32_e32 v10, v10
	s_nop 0
	v_mul_f32_e32 v11, 0x45800000, v10
	v_cndmask_b32_e32 v18, v10, v11, vcc
	global_load_dwordx4 v[10:13], v[62:63], off offset:16
	global_load_dwordx4 v[14:17], v[62:63], off
	v_mul_f32_e32 v2, v2, v18
	v_mul_f32_e32 v8, v8, v18
	v_mul_f32_e32 v3, v3, v18
	s_waitcnt vmcnt(0)
	v_mul_f32_e32 v2, v2, v16
	v_cvt_pk_bf16_f32 v2, v2, s0
	ds_write_b16 v169, v2 offset:35390
	v_mul_f32_e32 v2, v4, v18
	v_mul_f32_e32 v2, v2, v17
	v_cvt_pk_bf16_f32 v2, v2, s0
	ds_write_b16 v169, v2 offset:35662
	v_mul_f32_e32 v2, v5, v18
	v_mul_f32_e32 v2, v2, v10
	v_cvt_pk_bf16_f32 v2, v2, s0
	ds_write_b16 v169, v2 offset:35934
	v_mul_f32_e32 v2, v6, v18
	v_mul_f32_e32 v2, v2, v11
	v_cvt_pk_bf16_f32 v2, v2, s0
	ds_write_b16 v169, v2 offset:36206
	v_mul_f32_e32 v2, v7, v18
	v_mul_f32_e32 v2, v2, v12
	v_cvt_pk_bf16_f32 v2, v2, s0
	ds_write_b16 v169, v2 offset:36478
	v_mul_f32_e32 v2, v9, v18
	v_mul_f32_e32 v8, v8, v14
	v_mul_f32_e32 v3, v3, v15
	v_mul_f32_e32 v2, v2, v13
	v_cvt_pk_bf16_f32 v8, v8, s0
	v_cvt_pk_bf16_f32 v3, v3, s0
	v_cvt_pk_bf16_f32 v2, v2, s0
	ds_write_b16 v169, v8 offset:34846
	ds_write_b16 v169, v3 offset:35118
	ds_write_b16 v169, v2 offset:36750
; #define LAS __attribute__((address_space(3)))
; __device__ __forceinline__ void sgu_unit(const Params& p, int l, int un, LAS unsigned char* lds) {
;     ...
;     __syncthreads();
;     { const int fr = lane & 15, fq = lane >> 4; f32x4 acc[8];
; #pragma unroll
;       for (int nb = 0; nb < 8; ++nb) acc[nb] = (f32x4){0.f, 0.f, 0.f, 0.f};
; #pragma unroll
;       for (int ks = 0; ks < 4; ++ks) { const bf16x8 af = *(const LAS bf16x8*)(Wl + (wave * 16 + fr) * 136 + ks * 32 + fq * 8);
; #pragma unroll
;           for (int nb = 0; nb < 8; ++nb) { const bf16x8 bfr = *(const LAS bf16x8*)(Vl + (nb * 16 + fr) * 136 + ks * 32 + fq * 8);
;               acc[nb] = __builtin_amdgcn_mfma_f32_16x16x32_bf16(bfr, af, acc[nb], 0, 0, 0); } }
.LBB0_1292:
	s_or_b64 exec, exec, s[0:1]
	v_and_b32_e32 v7, 15, v64
	v_or_b32_e32 v36, v65, v7
	v_lshl_add_u32 v6, v66, 4, 0
	v_mad_u64_u32 v[34:35], s[2:3], v36, s13, v[6:7]
	v_mad_u32_u24 v35, v7, s13, v6
	v_bfe_u32 v170, v0, 4, 2
	v_bfe_u32 v171, v0, 3, 1
	v_xor_b32_e32 v172, v170, v171
	v_sub_u32_e32 v172, v172, v170
	v_lshl_add_u32 v172, v172, 4, v35
	v_xor_b32_e32 v173, 2, v170
	v_xor_b32_e32 v173, v173, v171
	v_sub_u32_e32 v173, v173, v170
	v_lshl_add_u32 v173, v173, 4, v35
	s_waitcnt lgkmcnt(0)
	s_barrier
	ds_read_b128 v[2:5], v34
	ds_read_b128 v[6:9], v172 offset:34816
	ds_read_b128 v[10:13], v173 offset:39168
	ds_read_b128 v[14:17], v172 offset:43584
	ds_read_b128 v[18:21], v173 offset:47936
	ds_read_b128 v[22:25], v172 offset:52352
	ds_read_b128 v[26:29], v173 offset:56704
	ds_read_b128 v[30:33], v172 offset:61120
	ds_read_b128 v[38:41], v173 offset:65472
	s_waitcnt lgkmcnt(7)
	v_mfma_f32_16x16x32_bf16 v[6:9], v[6:9], v[2:5], 0
	s_lshl_b64 s[0:1], s[40:41], 2
	v_readlane_b32 s40, v251, 16
	v_readlane_b32 s41, v251, 17
	s_waitcnt lgkmcnt(6)
	v_mfma_f32_16x16x32_bf16 v[10:13], v[10:13], v[2:5], 0
	v_readlane_b32 s42, v251, 18
	v_readlane_b32 s43, v251, 19
	v_readlane_b32 s44, v251, 20
	s_waitcnt lgkmcnt(5)
	v_mfma_f32_16x16x32_bf16 v[14:17], v[14:17], v[2:5], 0
	v_readlane_b32 s45, v251, 21
	v_readlane_b32 s46, v251, 22
	v_readlane_b32 s47, v251, 23
	s_waitcnt lgkmcnt(4)
	v_mfma_f32_16x16x32_bf16 v[18:21], v[18:21], v[2:5], 0
	v_readlane_b32 s48, v251, 24
	v_readlane_b32 s49, v251, 25
	v_readlane_b32 s50, v251, 26
	s_waitcnt lgkmcnt(3)
	v_mfma_f32_16x16x32_bf16 v[22:25], v[22:25], v[2:5], 0
	v_readlane_b32 s51, v251, 27
	s_mov_b64 s[40:41], s[44:45]
	s_mov_b64 s[42:43], s[46:47]
	s_waitcnt lgkmcnt(2)
	v_mfma_f32_16x16x32_bf16 v[26:29], v[26:29], v[2:5], 0
	s_mov_b64 s[44:45], s[48:49]
	s_add_u32 s0, s44, s0
	s_addc_u32 s1, s45, s1
	s_waitcnt lgkmcnt(1)
	v_mfma_f32_16x16x32_bf16 v[30:33], v[30:33], v[2:5], 0
	v_ashrrev_i32_e32 v37, 31, v36
	v_lshlrev_b32_e32 v206, 3, v66
	v_readlane_b32 s52, v251, 28
	s_waitcnt lgkmcnt(0)
	v_mfma_f32_16x16x32_bf16 v[2:5], v[38:41], v[2:5], 0
	ds_read_b128 v[38:41], v34 offset:64
	ds_read_b128 v[42:45], v172 offset:34880
	v_readlane_b32 s53, v251, 29
	v_readlane_b32 s54, v251, 30
	s_waitcnt lgkmcnt(0)
	v_mfma_f32_16x16x32_bf16 v[6:9], v[42:45], v[38:41], v[6:9]
	ds_read_b128 v[42:45], v173 offset:39232
	v_readlane_b32 s55, v251, 31
	s_mov_b64 s[46:47], s[50:51]
	s_waitcnt lgkmcnt(0)
	v_mfma_f32_16x16x32_bf16 v[10:13], v[42:45], v[38:41], v[10:13]
	ds_read_b128 v[42:45], v172 offset:43520
	s_waitcnt lgkmcnt(0)
	v_mfma_f32_16x16x32_bf16 v[14:17], v[42:45], v[38:41], v[14:17]
	ds_read_b128 v[42:45], v173 offset:47872
	s_waitcnt lgkmcnt(0)
	v_mfma_f32_16x16x32_bf16 v[18:21], v[42:45], v[38:41], v[18:21]
	ds_read_b128 v[42:45], v172 offset:52416
	s_waitcnt lgkmcnt(0)
	v_mfma_f32_16x16x32_bf16 v[22:25], v[42:45], v[38:41], v[22:25]
	ds_read_b128 v[42:45], v173 offset:56768
	s_waitcnt lgkmcnt(0)
	v_mfma_f32_16x16x32_bf16 v[26:29], v[42:45], v[38:41], v[26:29]
	ds_read_b128 v[42:45], v172 offset:61056
	s_waitcnt lgkmcnt(0)
	v_mfma_f32_16x16x32_bf16 v[30:33], v[42:45], v[38:41], v[30:33]
	ds_read_b128 v[42:45], v173 offset:65408
	s_waitcnt lgkmcnt(0)
	v_mfma_f32_16x16x32_bf16 v[2:5], v[42:45], v[38:41], v[2:5]
	ds_read_b128 v[38:41], v34 offset:128
	ds_read_b128 v[42:45], v172 offset:34944
	s_waitcnt lgkmcnt(0)
	v_mfma_f32_16x16x32_bf16 v[6:9], v[42:45], v[38:41], v[6:9]
	ds_read_b128 v[42:45], v173 offset:39296
	s_waitcnt lgkmcnt(0)
	v_mfma_f32_16x16x32_bf16 v[10:13], v[42:45], v[38:41], v[10:13]
	ds_read_b128 v[42:45], v172 offset:43712
	s_waitcnt lgkmcnt(0)
	v_mfma_f32_16x16x32_bf16 v[14:17], v[42:45], v[38:41], v[14:17]
	ds_read_b128 v[42:45], v173 offset:48064
	s_waitcnt lgkmcnt(0)
	v_mfma_f32_16x16x32_bf16 v[18:21], v[42:45], v[38:41], v[18:21]
	ds_read_b128 v[42:45], v172 offset:52224
	s_waitcnt lgkmcnt(0)
	v_mfma_f32_16x16x32_bf16 v[42:45], v[42:45], v[38:41], v[22:25]
	s_nop 2
	ds_read_b128 v[22:25], v173 offset:56576
	s_waitcnt lgkmcnt(0)
	v_mfma_f32_16x16x32_bf16 v[46:49], v[22:25], v[38:41], v[26:29]
	ds_read_b128 v[22:25], v172 offset:60992
	s_waitcnt lgkmcnt(0)
	v_mfma_f32_16x16x32_bf16 v[50:53], v[22:25], v[38:41], v[30:33]
	ds_read_b128 v[22:25], v173 offset:65344
	s_waitcnt lgkmcnt(0)
	v_mfma_f32_16x16x32_bf16 v[2:5], v[22:25], v[38:41], v[2:5]
	ds_read_b128 v[38:41], v34 offset:192
	ds_read_b128 v[22:25], v172 offset:35008
	s_waitcnt lgkmcnt(0)
	v_mfma_f32_16x16x32_bf16 v[30:33], v[22:25], v[38:41], v[6:9]
	s_nop 2
	ds_read_b128 v[6:9], v173 offset:39360
	s_waitcnt lgkmcnt(0)
	v_mfma_f32_16x16x32_bf16 v[26:29], v[6:9], v[38:41], v[10:13]
	ds_read_b128 v[6:9], v172 offset:43648
	s_waitcnt lgkmcnt(0)
	v_mfma_f32_16x16x32_bf16 v[22:25], v[6:9], v[38:41], v[14:17]
	ds_read_b128 v[6:9], v173 offset:48000
	s_waitcnt lgkmcnt(0)
	v_mfma_f32_16x16x32_bf16 v[18:21], v[6:9], v[38:41], v[18:21]
	ds_read_b128 v[6:9], v172 offset:52288
	s_waitcnt lgkmcnt(0)
	v_mfma_f32_16x16x32_bf16 v[14:17], v[6:9], v[38:41], v[42:45]
	ds_read_b128 v[6:9], v173 offset:56640
	s_nop 1
	ds_read_b128 v[42:45], v173 offset:65280
	s_waitcnt lgkmcnt(1)
	v_mfma_f32_16x16x32_bf16 v[10:13], v[6:9], v[38:41], v[46:49]
	ds_read_b128 v[6:9], v172 offset:60928
	v_lshl_add_u64 v[34:35], v[36:37], 2, s[0:1]
	s_movk_i32 s0, 0x1e00
	s_waitcnt lgkmcnt(0)
; __device__ __forceinline__ unsigned cvt_pk_bf16(float lo, float hi) { const f32x2 v = {lo, hi}; const bf16x2_t b = __builtin_convertvector(v, bf16x2_t); return __builtin_bit_cast(unsigned, b); }
; __device__ __forceinline__ float bflo(unsigned w) { return __uint_as_float(w << 16); }
; __device__ __forceinline__ float bfhi(unsigned w) { return __uint_as_float(w & 0xffff0000u); }
; __device__ __forceinline__ void sgu_unit(const Params& p, int l, int un, LAS unsigned char* lds) {
;     ...
;       const int pp = wave * 16 + fr; const float bias = p.in[I_SGUB][((size_t)l * 4 + h) * 128 + pp]; const bf16_t* pr = P + (size_t)(row0 + pp) * INP + C_SGU_U + h * 128;
;       u32x2 uq[8];
; #pragma unroll
;       for (int nb = 0; nb < 8; ++nb) uq[nb] = *(const u32x2*)(pr + nb * 16 + 4 * fq);
; #pragma unroll
;       for (int nb = 0; nb < 8; ++nb) { const int c = nb * 16 + 4 * fq; const u32x2 uv = uq[nb];
;           u32x2 w; w.x = cvt_pk_bf16(gelu_tanh(bflo(uv.x)) * (acc[nb][0] + bias), gelu_tanh(bfhi(uv.x)) * (acc[nb][1] + bias));
;           w.y = cvt_pk_bf16(gelu_tanh(bflo(uv.y)) * (acc[nb][2] + bias), gelu_tanh(bfhi(uv.y)) * (acc[nb][3] + bias));
;           *(u32x2*)(CAT + (size_t)(row0 + pp) * DM + h * 128 + c) = w; } }
	v_mfma_f32_16x16x32_bf16 v[6:9], v[6:9], v[38:41], v[50:53]
	s_nop 2
	v_add_u32_e32 v50, s12, v36
	v_mov_b64_e32 v[36:37], s[38:39]
	v_mad_i64_i32 v[36:37], s[0:1], v50, s0, v[36:37]
	v_readlane_b32 s0, v253, 39
	s_lshl_b32 s0, s0, 1
	s_mov_b32 s1, s5
	v_lshl_add_u64 v[36:37], v[36:37], 0, s[0:1]
	v_lshl_add_u64 v[36:37], v[36:37], 0, v[206:207]
	v_mfma_f32_16x16x32_bf16 v[2:5], v[42:45], v[38:41], v[2:5]
	global_load_dword v34, v[34:35], off
	s_nop 0
	global_load_dwordx2 v[52:53], v[36:37], off
	global_load_dwordx2 v[48:49], v[36:37], off offset:32
	global_load_dwordx2 v[46:47], v[36:37], off offset:64
	global_load_dwordx2 v[44:45], v[36:37], off offset:96
	global_load_dwordx2 v[42:43], v[36:37], off offset:128
	global_load_dwordx2 v[40:41], v[36:37], off offset:160
	global_load_dwordx2 v[38:39], v[36:37], off offset:192
	s_nop 0
	global_load_dwordx2 v[36:37], v[36:37], off offset:224
	v_ashrrev_i32_e32 v51, 31, v50
	v_lshlrev_b64 v[50:51], 12, v[50:51]
	v_lshl_add_u64 v[50:51], s[36:37], 0, v[50:51]
	v_lshl_add_u64 v[50:51], v[50:51], 0, s[0:1]
	s_mov_b64 s[0:1], 0x2d1b8000
	s_waitcnt vmcnt(7)
	v_lshlrev_b32_e32 v54, 16, v52
	v_mul_f32_e32 v35, 0x3dd2d3e8, v54
	v_fma_f32 v35, -v35, v54, s33
	v_mul_f32_e32 v35, v35, v54
	v_exp_f32_e32 v35, v35
	v_and_b32_e32 v55, 0xffff0000, v52
	v_add_f32_e32 v35, 1.0, v35
	v_rcp_f32_e32 v56, v35
	v_mul_f32_e32 v35, 0x3dd2d3e8, v55
	v_fma_f32 v35, -v35, v55, s33
	v_mul_f32_e32 v35, v35, v55
	v_exp_f32_e32 v35, v35
	s_nop 0
	v_add_f32_e32 v35, 1.0, v35
	v_rcp_f32_e32 v57, v35
	v_pk_add_f32 v[30:31], v[30:31], v[34:35] op_sel_hi:[1,0]
	v_pk_mul_f32 v[54:55], v[56:57], v[54:55]
	s_nop 0
	v_pk_mul_f32 v[30:31], v[30:31], v[54:55]
	s_nop 0
	v_cvt_pk_bf16_f32 v52, v30, v31
	v_lshlrev_b32_e32 v30, 16, v53
	v_mul_f32_e32 v35, 0x3dd2d3e8, v30
	v_fma_f32 v35, -v35, v30, s33
	v_mul_f32_e32 v35, v35, v30
	v_exp_f32_e32 v35, v35
	v_and_b32_e32 v31, 0xffff0000, v53
	v_add_f32_e32 v35, 1.0, v35
	v_rcp_f32_e32 v54, v35
	v_mul_f32_e32 v35, 0x3dd2d3e8, v31
	v_fma_f32 v35, -v35, v31, s33
	v_mul_f32_e32 v35, v35, v31
	v_exp_f32_e32 v35, v35
	s_nop 0
	v_add_f32_e32 v35, 1.0, v35
	v_rcp_f32_e32 v55, v35
	v_pk_add_f32 v[32:33], v[32:33], v[34:35] op_sel_hi:[1,0]
	v_pk_mul_f32 v[30:31], v[54:55], v[30:31]
	s_nop 0
	v_pk_mul_f32 v[30:31], v[32:33], v[30:31]
	v_lshl_add_u64 v[32:33], v[50:51], 0, v[206:207]
	v_cvt_pk_bf16_f32 v53, v30, v31
	v_lshl_add_u64 v[30:31], v[32:33], 0, s[0:1]
	s_mov_b32 s0, 0x2d1b8000
	v_add_co_u32_e32 v32, vcc, s0, v32
	s_nop 1
	v_addc_co_u32_e32 v33, vcc, 0, v33, vcc
	global_store_dwordx2 v[32:33], v[52:53], off
	s_waitcnt vmcnt(7)
	v_lshlrev_b32_e32 v32, 16, v48
	v_mul_f32_e32 v35, 0x3dd2d3e8, v32
	v_fma_f32 v35, -v35, v32, s33
	v_mul_f32_e32 v35, v35, v32
	v_exp_f32_e32 v35, v35
	v_and_b32_e32 v33, 0xffff0000, v48
	v_add_f32_e32 v35, 1.0, v35
	v_rcp_f32_e32 v50, v35
	v_mul_f32_e32 v35, 0x3dd2d3e8, v33
	v_fma_f32 v35, -v35, v33, s33
	v_mul_f32_e32 v35, v35, v33
	v_exp_f32_e32 v35, v35
	s_nop 0
	v_add_f32_e32 v35, 1.0, v35
	v_rcp_f32_e32 v51, v35
	v_pk_add_f32 v[26:27], v[26:27], v[34:35] op_sel_hi:[1,0]
	v_pk_add_f32 v[28:29], v[28:29], v[34:35] op_sel_hi:[1,0]
	v_pk_add_f32 v[22:23], v[22:23], v[34:35] op_sel_hi:[1,0]
	v_pk_mul_f32 v[32:33], v[50:51], v[32:33]
	v_pk_add_f32 v[24:25], v[24:25], v[34:35] op_sel_hi:[1,0]
	v_pk_mul_f32 v[26:27], v[26:27], v[32:33]
	v_lshlrev_b32_e32 v32, 16, v49
	v_cvt_pk_bf16_f32 v26, v26, v27
	v_mul_f32_e32 v27, 0x3dd2d3e8, v32
	v_fma_f32 v27, -v27, v32, s33
	v_mul_f32_e32 v27, v27, v32
	v_exp_f32_e32 v27, v27
	v_and_b32_e32 v33, 0xffff0000, v49
	v_pk_add_f32 v[18:19], v[18:19], v[34:35] op_sel_hi:[1,0]
	v_pk_add_f32 v[20:21], v[20:21], v[34:35] op_sel_hi:[1,0]
	v_add_f32_e32 v27, 1.0, v27
	v_rcp_f32_e32 v48, v27
	v_mul_f32_e32 v27, 0x3dd2d3e8, v33
	v_fma_f32 v27, -v27, v33, s33
	v_mul_f32_e32 v27, v27, v33
	v_exp_f32_e32 v27, v27
	v_pk_add_f32 v[14:15], v[14:15], v[34:35] op_sel_hi:[1,0]
	v_pk_add_f32 v[16:17], v[16:17], v[34:35] op_sel_hi:[1,0]
	v_pk_add_f32 v[10:11], v[10:11], v[34:35] op_sel_hi:[1,0]
	v_add_f32_e32 v27, 1.0, v27
	v_rcp_f32_e32 v49, v27
	v_pk_add_f32 v[12:13], v[12:13], v[34:35] op_sel_hi:[1,0]
	v_pk_add_f32 v[6:7], v[6:7], v[34:35] op_sel_hi:[1,0]
	v_pk_add_f32 v[8:9], v[8:9], v[34:35] op_sel_hi:[1,0]
	v_pk_mul_f32 v[32:33], v[48:49], v[32:33]
	v_pk_add_f32 v[2:3], v[34:35], v[2:3] op_sel_hi:[0,1]
	v_pk_mul_f32 v[28:29], v[28:29], v[32:33]
	v_pk_add_f32 v[4:5], v[34:35], v[4:5] op_sel_hi:[0,1]
	v_cvt_pk_bf16_f32 v27, v28, v29
	global_store_dwordx2 v[30:31], v[26:27], off offset:32
	s_waitcnt vmcnt(7)
	v_lshlrev_b32_e32 v26, 16, v46
	v_and_b32_e32 v27, 0xffff0000, v46
	v_mul_f32_e32 v28, 0x3dd2d3e8, v26
	v_mul_f32_e32 v29, 0x3dd2d3e8, v27
	v_fma_f32 v28, -v28, v26, s33
	v_fma_f32 v29, -v29, v27, s33
	v_mul_f32_e32 v28, v28, v26
	v_mul_f32_e32 v29, v29, v27
	v_exp_f32_e32 v28, v28
	v_exp_f32_e32 v29, v29
	v_add_f32_e32 v28, 1.0, v28
	v_add_f32_e32 v29, 1.0, v29
	v_rcp_f32_e32 v28, v28
	v_rcp_f32_e32 v29, v29
	s_nop 0
	v_pk_mul_f32 v[26:27], v[28:29], v[26:27]
	s_nop 0
	v_pk_mul_f32 v[22:23], v[22:23], v[26:27]
	v_lshlrev_b32_e32 v26, 16, v47
	v_cvt_pk_bf16_f32 v22, v22, v23
	v_mul_f32_e32 v23, 0x3dd2d3e8, v26
	v_fma_f32 v23, -v23, v26, s33
	v_mul_f32_e32 v23, v23, v26
	v_exp_f32_e32 v23, v23
	v_and_b32_e32 v27, 0xffff0000, v47
	v_add_f32_e32 v23, 1.0, v23
	v_rcp_f32_e32 v28, v23
	v_mul_f32_e32 v23, 0x3dd2d3e8, v27
	v_fma_f32 v23, -v23, v27, s33
	v_mul_f32_e32 v23, v23, v27
	v_exp_f32_e32 v23, v23
	s_nop 0
	v_add_f32_e32 v23, 1.0, v23
	v_rcp_f32_e32 v29, v23
	s_nop 0
	v_pk_mul_f32 v[26:27], v[28:29], v[26:27]
	s_nop 0
	v_pk_mul_f32 v[24:25], v[24:25], v[26:27]
	s_nop 0
	v_cvt_pk_bf16_f32 v23, v24, v25
	global_store_dwordx2 v[30:31], v[22:23], off offset:64
	s_waitcnt vmcnt(7)
; __device__ __forceinline__ unsigned cvt_pk_bf16(float lo, float hi) { const f32x2 v = {lo, hi}; const bf16x2_t b = __builtin_convertvector(v, bf16x2_t); return __builtin_bit_cast(unsigned, b); }
; __device__ __forceinline__ float bflo(unsigned w) { return __uint_as_float(w << 16); }
; __device__ __forceinline__ float bfhi(unsigned w) { return __uint_as_float(w & 0xffff0000u); }
; __device__ __forceinline__ void sgu_unit(const Params& p, int l, int un, LAS unsigned char* lds) {
;     ...
;       for (int nb = 0; nb < 8; ++nb) { const int c = nb * 16 + 4 * fq; const u32x2 uv = uq[nb];
;           u32x2 w; w.x = cvt_pk_bf16(gelu_tanh(bflo(uv.x)) * (acc[nb][0] + bias), gelu_tanh(bfhi(uv.x)) * (acc[nb][1] + bias));
;           w.y = cvt_pk_bf16(gelu_tanh(bflo(uv.y)) * (acc[nb][2] + bias), gelu_tanh(bfhi(uv.y)) * (acc[nb][3] + bias));
;           *(u32x2*)(CAT + (size_t)(row0 + pp) * DM + h * 128 + c) = w; } }
;     __syncthreads();
	v_lshlrev_b32_e32 v22, 16, v44
	v_and_b32_e32 v23, 0xffff0000, v44
	v_mul_f32_e32 v24, 0x3dd2d3e8, v22
	v_mul_f32_e32 v25, 0x3dd2d3e8, v23
	v_fma_f32 v24, -v24, v22, s33
	v_fma_f32 v25, -v25, v23, s33
	v_mul_f32_e32 v24, v24, v22
	v_mul_f32_e32 v25, v25, v23
	v_exp_f32_e32 v24, v24
	v_exp_f32_e32 v25, v25
	v_add_f32_e32 v24, 1.0, v24
	v_add_f32_e32 v25, 1.0, v25
	v_rcp_f32_e32 v24, v24
	v_rcp_f32_e32 v25, v25
	s_nop 0
	v_pk_mul_f32 v[22:23], v[24:25], v[22:23]
	s_nop 0
	v_pk_mul_f32 v[18:19], v[18:19], v[22:23]
	v_lshlrev_b32_e32 v22, 16, v45
	v_cvt_pk_bf16_f32 v18, v18, v19
	v_mul_f32_e32 v19, 0x3dd2d3e8, v22
	v_fma_f32 v19, -v19, v22, s33
	v_mul_f32_e32 v19, v19, v22
	v_exp_f32_e32 v19, v19
	v_and_b32_e32 v23, 0xffff0000, v45
	v_add_f32_e32 v19, 1.0, v19
	v_rcp_f32_e32 v24, v19
	v_mul_f32_e32 v19, 0x3dd2d3e8, v23
	v_fma_f32 v19, -v19, v23, s33
	v_mul_f32_e32 v19, v19, v23
	v_exp_f32_e32 v19, v19
	s_nop 0
	v_add_f32_e32 v19, 1.0, v19
	v_rcp_f32_e32 v25, v19
	s_nop 0
	v_pk_mul_f32 v[22:23], v[24:25], v[22:23]
	s_nop 0
	v_pk_mul_f32 v[20:21], v[20:21], v[22:23]
	s_nop 0
	v_cvt_pk_bf16_f32 v19, v20, v21
	global_store_dwordx2 v[30:31], v[18:19], off offset:96
	s_waitcnt vmcnt(7)
	v_lshlrev_b32_e32 v18, 16, v42
	v_and_b32_e32 v19, 0xffff0000, v42
	v_mul_f32_e32 v20, 0x3dd2d3e8, v18
	v_mul_f32_e32 v21, 0x3dd2d3e8, v19
	v_fma_f32 v20, -v20, v18, s33
	v_fma_f32 v21, -v21, v19, s33
	v_mul_f32_e32 v20, v20, v18
	v_mul_f32_e32 v21, v21, v19
	v_exp_f32_e32 v20, v20
	v_exp_f32_e32 v21, v21
	v_add_f32_e32 v20, 1.0, v20
	v_add_f32_e32 v21, 1.0, v21
	v_rcp_f32_e32 v20, v20
	v_rcp_f32_e32 v21, v21
	s_nop 0
	v_pk_mul_f32 v[18:19], v[20:21], v[18:19]
	s_nop 0
	v_pk_mul_f32 v[14:15], v[14:15], v[18:19]
	v_lshlrev_b32_e32 v18, 16, v43
	v_cvt_pk_bf16_f32 v14, v14, v15
	v_mul_f32_e32 v15, 0x3dd2d3e8, v18
	v_fma_f32 v15, -v15, v18, s33
	v_mul_f32_e32 v15, v15, v18
	v_exp_f32_e32 v15, v15
	v_and_b32_e32 v19, 0xffff0000, v43
	v_add_f32_e32 v15, 1.0, v15
	v_rcp_f32_e32 v20, v15
	v_mul_f32_e32 v15, 0x3dd2d3e8, v19
	v_fma_f32 v15, -v15, v19, s33
	v_mul_f32_e32 v15, v15, v19
	v_exp_f32_e32 v15, v15
	s_nop 0
	v_add_f32_e32 v15, 1.0, v15
	v_rcp_f32_e32 v21, v15
	s_nop 0
	v_pk_mul_f32 v[18:19], v[20:21], v[18:19]
	s_nop 0
	v_pk_mul_f32 v[16:17], v[16:17], v[18:19]
	s_nop 0
	v_cvt_pk_bf16_f32 v15, v16, v17
	global_store_dwordx2 v[30:31], v[14:15], off offset:128
	s_waitcnt vmcnt(7)
	v_lshlrev_b32_e32 v14, 16, v40
	v_and_b32_e32 v15, 0xffff0000, v40
	v_mul_f32_e32 v16, 0x3dd2d3e8, v14
	v_mul_f32_e32 v17, 0x3dd2d3e8, v15
	v_fma_f32 v16, -v16, v14, s33
	v_fma_f32 v17, -v17, v15, s33
	v_mul_f32_e32 v16, v16, v14
	v_mul_f32_e32 v17, v17, v15
	v_exp_f32_e32 v16, v16
	v_exp_f32_e32 v17, v17
	v_add_f32_e32 v16, 1.0, v16
	v_add_f32_e32 v17, 1.0, v17
	v_rcp_f32_e32 v16, v16
	v_rcp_f32_e32 v17, v17
	s_nop 0
	v_pk_mul_f32 v[14:15], v[16:17], v[14:15]
	s_nop 0
	v_pk_mul_f32 v[10:11], v[10:11], v[14:15]
	v_lshlrev_b32_e32 v14, 16, v41
	v_cvt_pk_bf16_f32 v10, v10, v11
	v_mul_f32_e32 v11, 0x3dd2d3e8, v14
	v_fma_f32 v11, -v11, v14, s33
	v_mul_f32_e32 v11, v11, v14
	v_exp_f32_e32 v11, v11
	v_and_b32_e32 v15, 0xffff0000, v41
	v_add_f32_e32 v11, 1.0, v11
	v_rcp_f32_e32 v16, v11
	v_mul_f32_e32 v11, 0x3dd2d3e8, v15
	v_fma_f32 v11, -v11, v15, s33
	v_mul_f32_e32 v11, v11, v15
	v_exp_f32_e32 v11, v11
	s_nop 0
	v_add_f32_e32 v11, 1.0, v11
	v_rcp_f32_e32 v17, v11
	s_nop 0
	v_pk_mul_f32 v[14:15], v[16:17], v[14:15]
	s_nop 0
	v_pk_mul_f32 v[12:13], v[12:13], v[14:15]
	s_nop 0
	v_cvt_pk_bf16_f32 v11, v12, v13
	global_store_dwordx2 v[30:31], v[10:11], off offset:160
	s_waitcnt vmcnt(7)
	v_lshlrev_b32_e32 v10, 16, v38
	v_and_b32_e32 v11, 0xffff0000, v38
	v_mul_f32_e32 v12, 0x3dd2d3e8, v10
	v_mul_f32_e32 v13, 0x3dd2d3e8, v11
	v_fma_f32 v12, -v12, v10, s33
	v_fma_f32 v13, -v13, v11, s33
	v_mul_f32_e32 v12, v12, v10
	v_mul_f32_e32 v13, v13, v11
	v_exp_f32_e32 v12, v12
	v_exp_f32_e32 v13, v13
	v_add_f32_e32 v12, 1.0, v12
	v_add_f32_e32 v13, 1.0, v13
	v_rcp_f32_e32 v12, v12
	v_rcp_f32_e32 v13, v13
	s_nop 0
	v_pk_mul_f32 v[10:11], v[12:13], v[10:11]
	s_nop 0
	v_pk_mul_f32 v[6:7], v[6:7], v[10:11]
	v_lshlrev_b32_e32 v10, 16, v39
	v_cvt_pk_bf16_f32 v6, v6, v7
	v_mul_f32_e32 v7, 0x3dd2d3e8, v10
	v_fma_f32 v7, -v7, v10, s33
	v_mul_f32_e32 v7, v7, v10
	v_exp_f32_e32 v7, v7
	v_and_b32_e32 v11, 0xffff0000, v39
	v_add_f32_e32 v7, 1.0, v7
	v_rcp_f32_e32 v12, v7
	v_mul_f32_e32 v7, 0x3dd2d3e8, v11
	v_fma_f32 v7, -v7, v11, s33
	v_mul_f32_e32 v7, v7, v11
	v_exp_f32_e32 v7, v7
	s_nop 0
	v_add_f32_e32 v7, 1.0, v7
	v_rcp_f32_e32 v13, v7
	s_nop 0
	v_pk_mul_f32 v[10:11], v[12:13], v[10:11]
	s_nop 0
	v_pk_mul_f32 v[8:9], v[8:9], v[10:11]
	s_nop 0
	v_cvt_pk_bf16_f32 v7, v8, v9
	global_store_dwordx2 v[30:31], v[6:7], off offset:192
	s_waitcnt vmcnt(7)
	v_lshlrev_b32_e32 v6, 16, v36
	v_and_b32_e32 v7, 0xffff0000, v36
	v_mul_f32_e32 v8, 0x3dd2d3e8, v6
	v_mul_f32_e32 v9, 0x3dd2d3e8, v7
	v_fma_f32 v8, -v8, v6, s33
	v_fma_f32 v9, -v9, v7, s33
	v_mul_f32_e32 v8, v8, v6
	v_mul_f32_e32 v9, v9, v7
	v_exp_f32_e32 v8, v8
	v_exp_f32_e32 v9, v9
	v_add_f32_e32 v8, 1.0, v8
	v_add_f32_e32 v9, 1.0, v9
	v_rcp_f32_e32 v8, v8
	v_rcp_f32_e32 v9, v9
	s_nop 0
	v_pk_mul_f32 v[6:7], v[8:9], v[6:7]
	s_nop 0
	v_pk_mul_f32 v[2:3], v[2:3], v[6:7]
	v_lshlrev_b32_e32 v6, 16, v37
	v_cvt_pk_bf16_f32 v2, v2, v3
	v_mul_f32_e32 v3, 0x3dd2d3e8, v6
	v_fma_f32 v3, -v3, v6, s33
	v_mul_f32_e32 v3, v3, v6
	v_exp_f32_e32 v3, v3
	v_and_b32_e32 v7, 0xffff0000, v37
	v_add_f32_e32 v3, 1.0, v3
	v_rcp_f32_e32 v8, v3
	v_mul_f32_e32 v3, 0x3dd2d3e8, v7
	v_fma_f32 v3, -v3, v7, s33
	v_mul_f32_e32 v3, v3, v7
	v_exp_f32_e32 v3, v3
	s_nop 0
	v_add_f32_e32 v3, 1.0, v3
	v_rcp_f32_e32 v9, v3
	s_nop 0
	v_pk_mul_f32 v[6:7], v[8:9], v[6:7]
	s_nop 0
	v_pk_mul_f32 v[4:5], v[4:5], v[6:7]
	s_nop 0
	v_cvt_pk_bf16_f32 v3, v4, v5
	global_store_dwordx2 v[30:31], v[2:3], off offset:224
	s_barrier

; __device__ __forceinline__ void sgu_unit(const Params& p, int l, int un, LAS unsigned char* lds) {
;     ...
;     const float* Wg = p.in[I_SGUW] + ((size_t)l * 4 + h) * 128 * 128;
;     f32x4 wq[8]; u32x4 vv[16];
; #pragma unroll
;     for (int i = 0; i < 8; ++i) wq[i] = *(const f32x4*)(Wg + (i * 512 + tid) * 4);
; #pragma unroll
;     for (int qi = 0; qi < 16; ++qi) vv[qi] = *(const u32x4*)(P + (size_t)(row0 + wave * 16 + qi) * INP + C_SGU_V + lane * 8);
; __global__ void __launch_bounds__(512, 2) fwd(Params p) {
;     ...
;             if (c < (l == 0 ? 72 : 64) || G != 256) pg8::gemm_phase(lds, pg8::Desc{512, 512, 512}, S, E);
;             else { const int un = (l == 0 ? 128 + (c - 72) : 160 + (c - 64)); if (un < (l == 0 ? B_SGU : 256)) sgu_unit(p, l, un, lds); }
.LBB0_1393:
	s_andn2_b64 vcc, exec, s[0:1]
	s_cbranch_vccnz .LBB0_1501
	v_readlane_b32 s0, v252, 5
	v_readlane_b32 s1, v252, 6
	s_lshl_b32 s4, s0, 9
	v_readlane_b32 s0, v252, 20
	v_readlane_b32 s1, v252, 21
	s_and_b64 s[0:1], s[0:1], exec
	s_cselect_b32 s0, 0x48, 64
	s_cmp_ge_i32 s92, s0
	v_readlane_b32 s12, v255, 40
	s_cselect_b64 s[2:3], -1, 0
	v_readlane_b32 s13, v255, 41
	s_and_b64 s[2:3], s[12:13], s[2:3]
	s_mov_b64 s[0:1], -1
	s_and_b64 vcc, exec, s[2:3]
	s_cbranch_vccz .LBB0_1430
	v_readlane_b32 s2, v252, 20
	v_readlane_b32 s3, v252, 21
	s_and_b64 s[0:1], s[2:3], exec
	s_cselect_b32 s0, 56, 0x60
	s_add_i32 s0, s0, s92
	s_and_b64 s[2:3], s[2:3], exec
	s_movk_i32 s1, 0x120
	s_cselect_b32 s1, s1, 0x100
	s_cmp_ge_u32 s0, s1
	s_cbranch_scc1 .LBB0_1429
	v_readlane_b32 s44, v251, 16
	s_lshl_b32 s12, s0, 5
	v_readlane_b32 s0, v253, 39
	v_readlane_b32 s48, v251, 20
	v_readlane_b32 s49, v251, 21
	s_or_b32 s40, s4, s0
	s_mov_b32 s41, s5
	v_readlane_b32 s50, v251, 22
	v_readlane_b32 s51, v251, 23
	v_readlane_b32 s52, v251, 24
	v_readlane_b32 s53, v251, 25
	v_readlane_b32 s54, v251, 26
	v_readlane_b32 s55, v251, 27
	s_mov_b64 s[16:17], s[48:49]
	s_lshl_b64 s[0:1], s[40:41], 9
	s_mov_b64 s[18:19], s[50:51]
	s_waitcnt vmcnt(0)
	v_mov_b32_e32 v64, v0
	s_add_u32 s2, s18, s0
	s_addc_u32 s3, s19, s1
	v_lshlrev_b32_e32 v2, 2, v64
	v_ashrrev_i32_e32 v3, 31, v2
	v_add_u32_e32 v62, 0x800, v2
	s_mov_b64 s[14:15], 0
	v_lshl_add_u64 v[4:5], v[2:3], 2, s[2:3]
	v_ashrrev_i32_e32 v63, 31, v62
	v_lshl_add_u64 v[6:7], v[62:63], 2, s[2:3]
	global_load_dwordx4 v[66:69], v[4:5], off
	global_load_dwordx4 v[70:73], v[6:7], off
	v_add_u32_e32 v102, 0x1000, v2
	v_ashrrev_i32_e32 v103, 31, v102
	v_add_u32_e32 v104, 0x1800, v2
	v_lshl_add_u64 v[4:5], v[102:103], 2, s[2:3]
	v_ashrrev_i32_e32 v105, 31, v104
	v_lshl_add_u64 v[6:7], v[104:105], 2, s[2:3]
	global_load_dwordx4 v[74:77], v[4:5], off
	global_load_dwordx4 v[78:81], v[6:7], off
	s_and_b32 s12, s12, 0x7fffff80
	s_lshl_b64 s[0:1], s[4:5], 2
	v_readlane_b32 s13, v253, 41
	v_add_u32_e32 v106, 0x2000, v2
	s_add_u32 s0, s13, s0
	v_readlane_b32 s13, v253, 42
	v_ashrrev_i32_e32 v107, 31, v106
	v_add_u32_e32 v108, 0x2800, v2
	s_addc_u32 s1, s13, s1
	v_lshl_add_u64 v[4:5], v[106:107], 2, s[2:3]
	v_ashrrev_i32_e32 v109, 31, v108
	s_add_u32 s36, s84, s14
	v_lshl_add_u64 v[6:7], v[108:109], 2, s[2:3]
	global_load_dwordx4 v[82:85], v[4:5], off
	global_load_dwordx4 v[86:89], v[6:7], off
	s_addc_u32 s37, s85, s15
	v_add_u32_e32 v110, 0x3000, v2
	v_add_u32_e32 v112, 0x3800, v2
	s_add_u32 s38, s36, 0x1f1b8000
	v_ashrrev_i32_e32 v111, 31, v110
	v_ashrrev_i32_e32 v113, 31, v112
	v_ashrrev_i32_e32 v103, 6, v64
	s_addc_u32 s39, s37, 0
	v_lshl_add_u64 v[4:5], v[110:111], 2, s[2:3]
	v_lshl_add_u64 v[2:3], v[112:113], 2, s[2:3]
	v_lshlrev_b32_e32 v65, 4, v103
	v_and_b32_e32 v8, 63, v64
	global_load_dwordx4 v[90:93], v[4:5], off
	global_load_dwordx4 v[94:97], v[2:3], off
	v_add_u32_e32 v9, s12, v65
	v_mov_b64_e32 v[2:3], s[38:39]
	s_movk_i32 s13, 0x1e00
	v_mad_i64_i32 v[4:5], s[2:3], v9, s13, v[2:3]
	v_lshlrev_b32_e32 v206, 4, v8
	v_or_b32_e32 v6, 1, v9
	v_lshl_add_u64 v[4:5], v[4:5], 0, v[206:207]
	v_mad_i64_i32 v[6:7], s[2:3], v6, s13, v[2:3]
	v_lshl_add_u64 v[6:7], v[6:7], 0, v[206:207]
	global_load_dwordx4 v[98:101], v[4:5], off offset:1024
	global_load_dwordx4 v[58:61], v[6:7], off offset:1024
	v_or_b32_e32 v4, 2, v9
	v_or_b32_e32 v6, 3, v9
	v_mad_i64_i32 v[4:5], s[2:3], v4, s13, v[2:3]
	v_mad_i64_i32 v[6:7], s[2:3], v6, s13, v[2:3]
	v_lshl_add_u64 v[4:5], v[4:5], 0, v[206:207]
	v_lshl_add_u64 v[6:7], v[6:7], 0, v[206:207]
	global_load_dwordx4 v[54:57], v[4:5], off offset:1024
	global_load_dwordx4 v[50:53], v[6:7], off offset:1024
	v_or_b32_e32 v4, 4, v9
	v_or_b32_e32 v6, 5, v9
	v_mad_i64_i32 v[4:5], s[2:3], v4, s13, v[2:3]
	v_mad_i64_i32 v[6:7], s[2:3], v6, s13, v[2:3]
	v_lshl_add_u64 v[4:5], v[4:5], 0, v[206:207]
	v_lshl_add_u64 v[6:7], v[6:7], 0, v[206:207]
	global_load_dwordx4 v[46:49], v[4:5], off offset:1024
	global_load_dwordx4 v[42:45], v[6:7], off offset:1024
	v_or_b32_e32 v4, 6, v9
	v_or_b32_e32 v6, 7, v9
	v_mad_i64_i32 v[4:5], s[2:3], v4, s13, v[2:3]
	v_mad_i64_i32 v[6:7], s[2:3], v6, s13, v[2:3]
	v_lshl_add_u64 v[4:5], v[4:5], 0, v[206:207]
	v_lshl_add_u64 v[6:7], v[6:7], 0, v[206:207]
	global_load_dwordx4 v[38:41], v[4:5], off offset:1024
	global_load_dwordx4 v[34:37], v[6:7], off offset:1024
	v_or_b32_e32 v4, 8, v9
	v_or_b32_e32 v6, 9, v9
	v_mad_i64_i32 v[4:5], s[2:3], v4, s13, v[2:3]
	v_mad_i64_i32 v[6:7], s[2:3], v6, s13, v[2:3]
	v_lshl_add_u64 v[4:5], v[4:5], 0, v[206:207]
	v_lshl_add_u64 v[6:7], v[6:7], 0, v[206:207]
	global_load_dwordx4 v[30:33], v[4:5], off offset:1024
	global_load_dwordx4 v[26:29], v[6:7], off offset:1024
	v_or_b32_e32 v4, 10, v9
	v_or_b32_e32 v6, 11, v9
	v_mad_i64_i32 v[4:5], s[2:3], v4, s13, v[2:3]
	v_mad_i64_i32 v[6:7], s[2:3], v6, s13, v[2:3]
	v_lshl_add_u64 v[4:5], v[4:5], 0, v[206:207]
	v_lshl_add_u64 v[6:7], v[6:7], 0, v[206:207]
	global_load_dwordx4 v[22:25], v[4:5], off offset:1024
	global_load_dwordx4 v[18:21], v[6:7], off offset:1024
	v_or_b32_e32 v4, 12, v9
	v_or_b32_e32 v6, 13, v9
	v_mad_i64_i32 v[4:5], s[2:3], v4, s13, v[2:3]
	v_mad_i64_i32 v[6:7], s[2:3], v6, s13, v[2:3]
	v_lshl_add_u64 v[4:5], v[4:5], 0, v[206:207]
	v_lshl_add_u64 v[6:7], v[6:7], 0, v[206:207]
	v_lshlrev_b32_e32 v105, 3, v64
	global_load_dwordx4 v[14:17], v[4:5], off offset:1024
	global_load_dwordx4 v[10:13], v[6:7], off offset:1024
	v_or_b32_e32 v4, 14, v9
	v_or_b32_e32 v6, 15, v9
	v_and_b32_e32 v63, 0xf8, v105
	v_mad_i64_i32 v[4:5], s[2:3], v4, s13, v[2:3]
	v_mad_i64_i32 v[2:3], s[2:3], v6, s13, v[2:3]
	v_add_u32_e32 v114, 0, v63
	v_bfe_i32 v63, v64, 5, 25
	s_movk_i32 s13, 0x110
	v_lshl_add_u64 v[4:5], v[4:5], 0, v[206:207]
	v_lshl_add_u64 v[2:3], v[2:3], 0, v[206:207]
	s_waitcnt vmcnt(21)
; #define LAS __attribute__((address_space(3)))
; __device__ __forceinline__ unsigned cvt_pk_bf16(float lo, float hi) { const f32x2 v = {lo, hi}; const bf16x2_t b = __builtin_convertvector(v, bf16x2_t); return __builtin_bit_cast(unsigned, b); }
; __device__ __forceinline__ float bflo(unsigned w) { return __uint_as_float(w << 16); }
; __device__ __forceinline__ float bfhi(unsigned w) { return __uint_as_float(w & 0xffff0000u); }
; __device__ __forceinline__ unsigned short f2bf(float f) { return (unsigned short)(cvt_pk_bf16(f, 0.f) & 0xffffu); }
; __device__ __forceinline__ void sgu_unit(const Params& p, int l, int un, LAS unsigned char* lds) {
;     ...
;     for (int i = 0; i < 8; ++i) { const int e4 = (i * 512 + tid) * 4, r = e4 >> 7, c = e4 & 127; const f32x4 v = wq[i];
;         u32x2 w; w.x = cvt_pk_bf16(v[0], v[1]); w.y = cvt_pk_bf16(v[2], v[3]); *(LAS u32x2*)(Wl + r * 136 + c) = w; }
; #pragma unroll
;     for (int qi = 0; qi < 16; ++qi) { const int q = wave * 16 + qi;
;         const u32x4 v = vv[qi]; float f[8] = {bflo(v.x), bfhi(v.x), bflo(v.y), bfhi(v.y), bflo(v.z), bfhi(v.z), bflo(v.w), bfhi(v.w)}; float ss = 0.f;
; #pragma unroll
;         for (int j = 0; j < 8; ++j) { f[j] = gelu_tanh(f[j]); ss += f[j] * f[j]; }
;         ss = wave_sum(ss); const float rinv = rsqrtf(ss * (1.0f / 512.0f) + EPS);
;         if ((lane >> 4) == h) { const int c0 = (lane & 15) * 8; const float* g = p.in[I_SGUNG] + l * 512 + h * 128 + c0;
; #pragma unroll
;             for (int j = 0; j < 8; ++j) Vl[(c0 + j) * 136 + q] = f2bf(f[j] * rinv * g[j]); } }
	v_cvt_pk_bf16_f32 v66, v66, v67
	v_cvt_pk_bf16_f32 v67, v68, v69
	v_mad_u64_u32 v[68:69], s[2:3], v63, s13, v[114:115]
	global_load_dwordx4 v[6:9], v[4:5], off offset:1024
	s_nop 0
	global_load_dwordx4 v[2:5], v[2:3], off offset:1024
	ds_write_b64 v68, v[66:67]
	v_ashrrev_i32_e32 v66, 7, v62
	s_waitcnt vmcnt(22)
	v_cvt_pk_bf16_f32 v62, v70, v71
	v_cvt_pk_bf16_f32 v63, v72, v73
	v_mad_u64_u32 v[66:67], s[2:3], v66, s13, v[114:115]
	ds_write_b64 v66, v[62:63]
	v_ashrrev_i32_e32 v66, 7, v102
	s_waitcnt vmcnt(21)
	v_cvt_pk_bf16_f32 v62, v74, v75
	v_cvt_pk_bf16_f32 v63, v76, v77
	v_mad_u64_u32 v[66:67], s[2:3], v66, s13, v[114:115]
	ds_write_b64 v66, v[62:63]
	v_ashrrev_i32_e32 v66, 7, v104
	s_waitcnt vmcnt(20)
	v_cvt_pk_bf16_f32 v62, v78, v79
	v_cvt_pk_bf16_f32 v63, v80, v81
	v_mad_u64_u32 v[66:67], s[2:3], v66, s13, v[114:115]
	ds_write_b64 v66, v[62:63]
	v_ashrrev_i32_e32 v66, 7, v106
	s_waitcnt vmcnt(19)
	v_cvt_pk_bf16_f32 v62, v82, v83
	v_cvt_pk_bf16_f32 v63, v84, v85
	v_mad_u64_u32 v[66:67], s[2:3], v66, s13, v[114:115]
	ds_write_b64 v66, v[62:63]
	v_ashrrev_i32_e32 v66, 7, v108
	s_waitcnt vmcnt(18)
	v_cvt_pk_bf16_f32 v62, v86, v87
	v_cvt_pk_bf16_f32 v63, v88, v89
	v_mad_u64_u32 v[66:67], s[2:3], v66, s13, v[114:115]
	ds_write_b64 v66, v[62:63]
	v_ashrrev_i32_e32 v66, 7, v110
	s_waitcnt vmcnt(17)
	v_cvt_pk_bf16_f32 v62, v90, v91
	v_cvt_pk_bf16_f32 v63, v92, v93
	v_mad_u64_u32 v[66:67], s[2:3], v66, s13, v[114:115]
	ds_write_b64 v66, v[62:63]
	v_ashrrev_i32_e32 v66, 7, v112
	v_mad_u64_u32 v[66:67], s[2:3], v66, s13, v[114:115]
	s_waitcnt vmcnt(15)
	v_and_b32_e32 v67, 0xffff0000, v98
	v_mul_f32_e32 v73, 0x3dd2d3e8, v67
	v_fma_f32 v73, -v73, v67, s33
	v_mul_f32_e32 v73, v73, v67
	v_exp_f32_e32 v73, v73
	v_cvt_pk_bf16_f32 v62, v94, v95
	v_cvt_pk_bf16_f32 v63, v96, v97
	ds_write_b64 v66, v[62:63]
	v_lshlrev_b32_e32 v66, 16, v98
	v_add_f32_e32 v73, 1.0, v73
	v_mul_f32_e32 v72, 0x3dd2d3e8, v66
	v_rcp_f32_e32 v73, v73
	v_fma_f32 v72, -v72, v66, s33
	v_mul_f32_e32 v72, v72, v66
	v_lshlrev_b32_e32 v69, 16, v99
	v_exp_f32_e32 v72, v72
	v_mul_f32_e32 v79, v73, v67
	v_mul_f32_e32 v67, 0x3dd2d3e8, v69
	v_fma_f32 v67, -v67, v69, s33
	v_mul_f32_e32 v67, v67, v69
	v_add_f32_e32 v72, 1.0, v72
	v_exp_f32_e32 v67, v67
	v_rcp_f32_e32 v72, v72
	v_lshlrev_b32_e32 v71, 16, v100
	v_and_b32_e32 v70, 0xffff0000, v99
	v_add_f32_e32 v67, 1.0, v67
	v_mul_f32_e32 v73, 0x3dd2d3e8, v71
	v_mul_f32_e32 v81, v72, v66
	v_mul_f32_e32 v72, 0x3dd2d3e8, v70
	v_rcp_f32_e32 v67, v67
	v_fma_f32 v73, -v73, v71, s33
	v_fma_f32 v72, -v72, v70, s33
	v_mul_f32_e32 v73, v73, v71
	v_mul_f32_e32 v72, v72, v70
	v_exp_f32_e32 v73, v73
	v_and_b32_e32 v74, 0xffff0000, v100
	v_exp_f32_e32 v72, v72
	v_mul_f32_e32 v80, v67, v69
	v_mul_f32_e32 v69, 0x3dd2d3e8, v74
	v_fma_f32 v69, -v69, v74, s33
	v_add_f32_e32 v67, 1.0, v73
	v_mul_f32_e32 v69, v69, v74
	v_add_f32_e32 v72, 1.0, v72
	v_rcp_f32_e32 v67, v67
	v_exp_f32_e32 v69, v69
	v_rcp_f32_e32 v72, v72
	v_lshlrev_b32_e32 v75, 16, v101
	v_and_b32_e32 v82, 0xffff0000, v101
	v_mul_f32_e32 v76, v67, v71
	v_add_f32_e32 v67, 1.0, v69
	v_mul_f32_e32 v69, 0x3dd2d3e8, v75
	v_mul_f32_e32 v78, v72, v70
	v_fma_f32 v69, -v69, v75, s33
	v_mul_f32_e32 v70, 0x3dd2d3e8, v82
	v_mul_f32_e32 v69, v69, v75
	v_fma_f32 v70, -v70, v82, s33
	v_rcp_f32_e32 v67, v67
	v_exp_f32_e32 v69, v69
	v_mul_f32_e32 v70, v70, v82
	v_exp_f32_e32 v70, v70
	v_mul_f32_e32 v66, v79, v79
	v_mul_f32_e32 v77, v67, v74
	v_add_f32_e32 v67, 1.0, v69
	v_fmac_f32_e32 v66, v81, v81
	v_rcp_f32_e32 v67, v67
	v_add_f32_e32 v69, 1.0, v70
	v_fmac_f32_e32 v66, v80, v80
	v_rcp_f32_e32 v69, v69
	v_and_b32_e32 v62, 64, v249
	v_fmac_f32_e32 v66, v78, v78
	v_add_u32_e32 v62, 64, v62
	v_xor_b32_e32 v63, 32, v249
	v_fmac_f32_e32 v66, v76, v76
	v_cmp_lt_i32_e32 vcc, v63, v62
	v_fmac_f32_e32 v66, v77, v77
	v_mul_f32_e32 v75, v67, v75
	v_cndmask_b32_e32 v63, v249, v63, vcc
	v_fmac_f32_e32 v66, v75, v75
	v_mul_f32_e32 v74, v69, v82
	v_lshlrev_b32_e32 v68, 2, v63
	v_fmac_f32_e32 v66, v74, v74
	v_mov_b32_e32 v67, v66
	s_nop 1
	v_permlane32_swap_b32_e32 v67, v66
	v_xor_b32_e32 v63, 16, v249
	v_cmp_lt_i32_e32 vcc, v63, v62
	v_and_b32_e32 v84, 0x78, v105
	v_readlane_b32 s2, v253, 40
	v_cndmask_b32_e32 v63, v249, v63, vcc
	v_lshlrev_b32_e32 v69, 2, v63
	s_waitcnt lgkmcnt(0)
	v_add_f32_e32 v66, v66, v67
	v_mov_b32_e32 v67, v66
	s_nop 1
	v_permlane16_swap_b32_e32 v67, v66
	v_xor_b32_e32 v63, 8, v249
	v_cmp_lt_i32_e32 vcc, v63, v62
	v_lshlrev_b32_e32 v206, 2, v84
	v_readlane_b32 s45, v251, 17
	v_cndmask_b32_e32 v63, v249, v63, vcc
	v_lshlrev_b32_e32 v70, 2, v63
	s_waitcnt lgkmcnt(0)
	v_add_f32_e32 v66, v66, v67
	s_nop 1
	v_mov_b32_dpp v67, v66 row_ror:8 row_mask:0xf bank_mask:0xf
	v_xor_b32_e32 v63, 4, v249
	v_cmp_lt_i32_e32 vcc, v63, v62
	v_readlane_b32 s46, v251, 18
	v_readlane_b32 s47, v251, 19
	v_cndmask_b32_e32 v63, v249, v63, vcc
	v_lshlrev_b32_e32 v71, 2, v63
	s_waitcnt lgkmcnt(0)
	v_add_f32_e32 v66, v66, v67
	v_xor_b32_e32 v63, 2, v249
	s_nop 1
	v_mov_b32_dpp v67, v66 row_shl:4 row_mask:0xf bank_mask:0x5
	v_mov_b32_dpp v67, v66 row_shr:4 row_mask:0xf bank_mask:0xa
	v_cmp_lt_i32_e32 vcc, v63, v62
	v_readlane_b32 s56, v251, 28
	v_readlane_b32 s57, v251, 29
	v_cndmask_b32_e32 v63, v249, v63, vcc
	v_lshlrev_b32_e32 v72, 2, v63
	v_xor_b32_e32 v63, 1, v249
	v_cmp_lt_i32_e32 vcc, v63, v62
	v_readlane_b32 s58, v251, 30
	v_readlane_b32 s59, v251, 31
	v_cndmask_b32_e32 v62, v249, v63, vcc
	s_waitcnt lgkmcnt(0)
	v_add_f32_e32 v63, v66, v67
	s_nop 1
	v_mov_b32_dpp v67, v63 quad_perm:[2,3,0,1] row_mask:0xf bank_mask:0xf
	v_lshlrev_b32_e32 v73, 2, v62
	v_bfe_u32 v66, v64, 4, 2
	v_cmp_eq_u32_e32 vcc, s2, v66
	s_mov_b64 s[20:21], s[52:53]
	s_waitcnt lgkmcnt(0)
	v_add_f32_e32 v82, v63, v67
	s_nop 1
	v_mov_b32_dpp v83, v82 quad_perm:[1,0,3,2] row_mask:0xf bank_mask:0xf
	v_lshl_add_u32 v67, v103, 5, 0
	v_lshl_add_u64 v[62:63], s[0:1], 0, v[206:207]
	v_mad_u32_u24 v67, v84, s13, v67
	v_lshrrev_b32_e32 v170, 6, v0
	v_lshlrev_b32_e32 v170, 1, v170
	v_and_b32_e32 v171, 15, v0
	v_xor_b32_e32 v168, v170, v171
	v_sub_u32_e32 v168, v168, v170
	v_lshl_add_u32 v168, v168, 4, v67
	v_or_b32_e32 v170, 1, v170
	v_xor_b32_e32 v169, v170, v171
	v_sub_u32_e32 v169, v169, v170
	v_lshl_add_u32 v169, v169, 4, v67
	s_mov_b64 s[22:23], s[54:55]
	s_and_saveexec_b64 s[0:1], vcc
	s_cbranch_execz .LBB0_1398
; __device__ __forceinline__ unsigned short f2bf(float f) { return (unsigned short)(cvt_pk_bf16(f, 0.f) & 0xffffu); }
; __device__ __forceinline__ void sgu_unit(const Params& p, int l, int un, LAS unsigned char* lds) {
;     ...
;         ss = wave_sum(ss); const float rinv = rsqrtf(ss * (1.0f / 512.0f) + EPS);
;         if ((lane >> 4) == h) { const int c0 = (lane & 15) * 8; const float* g = p.in[I_SGUNG] + l * 512 + h * 128 + c0;
; #pragma unroll
;             for (int j = 0; j < 8; ++j) Vl[(c0 + j) * 136 + q] = f2bf(f[j] * rinv * g[j]); } }
	s_waitcnt lgkmcnt(0)
	v_add_f32_e32 v82, v82, v83
	v_fmamk_f32 v82, v82, 0x3b000000, v246
	s_mov_b32 s2, 0x800000
	v_cmp_gt_f32_e64 s[2:3], s2, v82
	v_mul_f32_e32 v83, 0x4b800000, v82
	s_nop 0
	v_cndmask_b32_e64 v82, v82, v83, s[2:3]
	v_rsq_f32_e32 v82, v82
	s_nop 0
	v_mul_f32_e32 v83, 0x45800000, v82
	v_cndmask_b32_e64 v90, v82, v83, s[2:3]
	global_load_dwordx4 v[82:85], v[62:63], off offset:16
	global_load_dwordx4 v[86:89], v[62:63], off
	v_mul_f32_e32 v79, v79, v90
	v_mul_f32_e32 v76, v76, v90
	v_mul_f32_e32 v81, v81, v90
	v_mul_f32_e32 v78, v78, v90
	v_mul_f32_e32 v75, v75, v90
	v_mul_f32_e32 v74, v74, v90
	s_waitcnt vmcnt(1)
	v_mul_f32_e32 v76, v76, v82
	s_waitcnt vmcnt(0)
	v_mul_f32_e32 v79, v79, v87
	v_cvt_pk_bf16_f32 v79, v79, s0
	v_cvt_pk_bf16_f32 v76, v76, s0
	ds_write_b16 v168, v79 offset:35088
	v_mul_f32_e32 v79, v80, v90
	ds_write_b16 v168, v76 offset:35904
	v_mul_f32_e32 v76, v77, v90
	v_mul_f32_e32 v81, v81, v86
	v_mul_f32_e32 v79, v79, v88
	v_mul_f32_e32 v78, v78, v89
	v_mul_f32_e32 v76, v76, v83
	v_mul_f32_e32 v75, v75, v84
	v_mul_f32_e32 v74, v74, v85
	v_cvt_pk_bf16_f32 v81, v81, s0
	v_cvt_pk_bf16_f32 v79, v79, s0
	v_cvt_pk_bf16_f32 v78, v78, s0
	v_cvt_pk_bf16_f32 v76, v76, s0
	v_cvt_pk_bf16_f32 v75, v75, s0
	v_cvt_pk_bf16_f32 v74, v74, s0
	ds_write_b16 v168, v81 offset:34816
	ds_write_b16 v168, v79 offset:35360
	ds_write_b16 v168, v78 offset:35632
	ds_write_b16 v168, v76 offset:36176
	ds_write_b16 v168, v75 offset:36448
	ds_write_b16 v168, v74 offset:36720

; #define LAS __attribute__((address_space(3)))
; __device__ __forceinline__ void sgu_unit(const Params& p, int l, int un, LAS unsigned char* lds) {
;     ...
;     __syncthreads();
;     { const int fr = lane & 15, fq = lane >> 4; f32x4 acc[8];
; #pragma unroll
;       for (int nb = 0; nb < 8; ++nb) acc[nb] = (f32x4){0.f, 0.f, 0.f, 0.f};
; #pragma unroll
;       for (int ks = 0; ks < 4; ++ks) { const bf16x8 af = *(const LAS bf16x8*)(Wl + (wave * 16 + fr) * 136 + ks * 32 + fq * 8);
; #pragma unroll
;           for (int nb = 0; nb < 8; ++nb) { const bf16x8 bfr = *(const LAS bf16x8*)(Vl + (nb * 16 + fr) * 136 + ks * 32 + fq * 8);
;               acc[nb] = __builtin_amdgcn_mfma_f32_16x16x32_bf16(bfr, af, acc[nb], 0, 0, 0); } }
.LBB0_1428:
	s_or_b64 exec, exec, s[0:1]
	v_and_b32_e32 v7, 15, v64
	v_or_b32_e32 v36, v65, v7
	v_lshl_add_u32 v6, v66, 4, 0
	v_mad_u64_u32 v[34:35], s[2:3], v36, s13, v[6:7]
	v_mad_u32_u24 v35, v7, s13, v6
	v_bfe_u32 v170, v0, 4, 2
	v_bfe_u32 v171, v0, 3, 1
	v_xor_b32_e32 v172, v170, v171
	v_sub_u32_e32 v172, v172, v170
	v_lshl_add_u32 v172, v172, 4, v35
	v_xor_b32_e32 v173, 2, v170
	v_xor_b32_e32 v173, v173, v171
	v_sub_u32_e32 v173, v173, v170
	v_lshl_add_u32 v173, v173, 4, v35
	s_waitcnt lgkmcnt(0)
	s_barrier
	ds_read_b128 v[2:5], v34
	ds_read_b128 v[6:9], v172 offset:34816
	ds_read_b128 v[10:13], v173 offset:39168
	ds_read_b128 v[14:17], v172 offset:43584
	ds_read_b128 v[18:21], v173 offset:47936
	ds_read_b128 v[22:25], v172 offset:52352
	ds_read_b128 v[26:29], v173 offset:56704
	ds_read_b128 v[30:33], v172 offset:61120
	ds_read_b128 v[38:41], v173 offset:65472
	s_waitcnt lgkmcnt(7)
	v_mfma_f32_16x16x32_bf16 v[6:9], v[6:9], v[2:5], 0
	s_lshl_b64 s[0:1], s[40:41], 2
	v_readlane_b32 s40, v251, 16
	v_readlane_b32 s44, v251, 20
	s_waitcnt lgkmcnt(6)
	v_mfma_f32_16x16x32_bf16 v[10:13], v[10:13], v[2:5], 0
	v_readlane_b32 s45, v251, 21
	v_readlane_b32 s46, v251, 22
	v_readlane_b32 s47, v251, 23
	s_waitcnt lgkmcnt(5)
	v_mfma_f32_16x16x32_bf16 v[14:17], v[14:17], v[2:5], 0
	v_readlane_b32 s48, v251, 24
	v_readlane_b32 s49, v251, 25
	v_readlane_b32 s50, v251, 26
	s_waitcnt lgkmcnt(4)
	v_mfma_f32_16x16x32_bf16 v[18:21], v[18:21], v[2:5], 0
	v_readlane_b32 s51, v251, 27
	s_mov_b64 s[16:17], s[44:45]
	s_mov_b64 s[20:21], s[48:49]
	s_waitcnt lgkmcnt(3)
	v_mfma_f32_16x16x32_bf16 v[22:25], v[22:25], v[2:5], 0
	s_add_u32 s0, s20, s0
	s_addc_u32 s1, s21, s1
	v_ashrrev_i32_e32 v37, 31, v36
	s_waitcnt lgkmcnt(2)
	v_mfma_f32_16x16x32_bf16 v[26:29], v[26:29], v[2:5], 0
	v_lshlrev_b32_e32 v206, 3, v66
	v_readlane_b32 s41, v251, 17
	v_readlane_b32 s42, v251, 18
	s_waitcnt lgkmcnt(1)
	v_mfma_f32_16x16x32_bf16 v[30:33], v[30:33], v[2:5], 0
	v_readlane_b32 s43, v251, 19
	v_readlane_b32 s52, v251, 28
	v_readlane_b32 s53, v251, 29
	s_waitcnt lgkmcnt(0)
	v_mfma_f32_16x16x32_bf16 v[2:5], v[38:41], v[2:5], 0
	ds_read_b128 v[38:41], v34 offset:64
	ds_read_b128 v[42:45], v172 offset:34880
	v_readlane_b32 s54, v251, 30
	v_readlane_b32 s55, v251, 31
	s_waitcnt lgkmcnt(0)
	v_mfma_f32_16x16x32_bf16 v[6:9], v[42:45], v[38:41], v[6:9]
	ds_read_b128 v[42:45], v173 offset:39232
	s_mov_b64 s[18:19], s[46:47]
	s_mov_b64 s[22:23], s[50:51]
	s_waitcnt lgkmcnt(0)
	v_mfma_f32_16x16x32_bf16 v[10:13], v[42:45], v[38:41], v[10:13]
	ds_read_b128 v[42:45], v172 offset:43520
	s_waitcnt lgkmcnt(0)
	v_mfma_f32_16x16x32_bf16 v[14:17], v[42:45], v[38:41], v[14:17]
	ds_read_b128 v[42:45], v173 offset:47872
	s_waitcnt lgkmcnt(0)
	v_mfma_f32_16x16x32_bf16 v[18:21], v[42:45], v[38:41], v[18:21]
	ds_read_b128 v[42:45], v172 offset:52416
	s_waitcnt lgkmcnt(0)
	v_mfma_f32_16x16x32_bf16 v[22:25], v[42:45], v[38:41], v[22:25]
	ds_read_b128 v[42:45], v173 offset:56768
	s_waitcnt lgkmcnt(0)
	v_mfma_f32_16x16x32_bf16 v[26:29], v[42:45], v[38:41], v[26:29]
	ds_read_b128 v[42:45], v172 offset:61056
	s_waitcnt lgkmcnt(0)
	v_mfma_f32_16x16x32_bf16 v[30:33], v[42:45], v[38:41], v[30:33]
	ds_read_b128 v[42:45], v173 offset:65408
	s_waitcnt lgkmcnt(0)
	v_mfma_f32_16x16x32_bf16 v[2:5], v[42:45], v[38:41], v[2:5]
	ds_read_b128 v[38:41], v34 offset:128
	ds_read_b128 v[42:45], v172 offset:34944
	s_waitcnt lgkmcnt(0)
	v_mfma_f32_16x16x32_bf16 v[6:9], v[42:45], v[38:41], v[6:9]
	ds_read_b128 v[42:45], v173 offset:39296
	s_waitcnt lgkmcnt(0)
	v_mfma_f32_16x16x32_bf16 v[10:13], v[42:45], v[38:41], v[10:13]
	ds_read_b128 v[42:45], v172 offset:43712
	s_waitcnt lgkmcnt(0)
	v_mfma_f32_16x16x32_bf16 v[14:17], v[42:45], v[38:41], v[14:17]
	ds_read_b128 v[42:45], v173 offset:48064
	s_waitcnt lgkmcnt(0)
	v_mfma_f32_16x16x32_bf16 v[18:21], v[42:45], v[38:41], v[18:21]
	ds_read_b128 v[42:45], v172 offset:52224
	s_waitcnt lgkmcnt(0)
	v_mfma_f32_16x16x32_bf16 v[42:45], v[42:45], v[38:41], v[22:25]
	s_nop 2
	ds_read_b128 v[22:25], v173 offset:56576
	s_waitcnt lgkmcnt(0)
	v_mfma_f32_16x16x32_bf16 v[46:49], v[22:25], v[38:41], v[26:29]
	ds_read_b128 v[22:25], v172 offset:60992
	s_waitcnt lgkmcnt(0)
	v_mfma_f32_16x16x32_bf16 v[50:53], v[22:25], v[38:41], v[30:33]
	ds_read_b128 v[22:25], v173 offset:65344
	s_waitcnt lgkmcnt(0)
	v_mfma_f32_16x16x32_bf16 v[2:5], v[22:25], v[38:41], v[2:5]
	ds_read_b128 v[38:41], v34 offset:192
	ds_read_b128 v[22:25], v172 offset:35008
	s_waitcnt lgkmcnt(0)
	v_mfma_f32_16x16x32_bf16 v[30:33], v[22:25], v[38:41], v[6:9]
	s_nop 2
	ds_read_b128 v[6:9], v173 offset:39360
	s_waitcnt lgkmcnt(0)
	v_mfma_f32_16x16x32_bf16 v[26:29], v[6:9], v[38:41], v[10:13]
	ds_read_b128 v[6:9], v172 offset:43648
	s_waitcnt lgkmcnt(0)
	v_mfma_f32_16x16x32_bf16 v[22:25], v[6:9], v[38:41], v[14:17]
	ds_read_b128 v[6:9], v173 offset:48000
	s_waitcnt lgkmcnt(0)
	v_mfma_f32_16x16x32_bf16 v[18:21], v[6:9], v[38:41], v[18:21]
	ds_read_b128 v[6:9], v172 offset:52288
	s_waitcnt lgkmcnt(0)
	v_mfma_f32_16x16x32_bf16 v[14:17], v[6:9], v[38:41], v[42:45]
	ds_read_b128 v[6:9], v173 offset:56640
	s_nop 1
	ds_read_b128 v[42:45], v173 offset:65280
	s_waitcnt lgkmcnt(1)
	v_mfma_f32_16x16x32_bf16 v[10:13], v[6:9], v[38:41], v[46:49]
	ds_read_b128 v[6:9], v172 offset:60928
	v_lshl_add_u64 v[34:35], v[36:37], 2, s[0:1]
	s_movk_i32 s0, 0x1e00
	s_waitcnt lgkmcnt(0)
; __device__ __forceinline__ unsigned cvt_pk_bf16(float lo, float hi) { const f32x2 v = {lo, hi}; const bf16x2_t b = __builtin_convertvector(v, bf16x2_t); return __builtin_bit_cast(unsigned, b); }
; __device__ __forceinline__ float bflo(unsigned w) { return __uint_as_float(w << 16); }
; __device__ __forceinline__ float bfhi(unsigned w) { return __uint_as_float(w & 0xffff0000u); }
; __device__ __forceinline__ void sgu_unit(const Params& p, int l, int un, LAS unsigned char* lds) {
;     ...
;       const int pp = wave * 16 + fr; const float bias = p.in[I_SGUB][((size_t)l * 4 + h) * 128 + pp]; const bf16_t* pr = P + (size_t)(row0 + pp) * INP + C_SGU_U + h * 128;
;       u32x2 uq[8];
; #pragma unroll
;       for (int nb = 0; nb < 8; ++nb) uq[nb] = *(const u32x2*)(pr + nb * 16 + 4 * fq);
; #pragma unroll
;       for (int nb = 0; nb < 8; ++nb) { const int c = nb * 16 + 4 * fq; const u32x2 uv = uq[nb];
;           u32x2 w; w.x = cvt_pk_bf16(gelu_tanh(bflo(uv.x)) * (acc[nb][0] + bias), gelu_tanh(bfhi(uv.x)) * (acc[nb][1] + bias));
;           w.y = cvt_pk_bf16(gelu_tanh(bflo(uv.y)) * (acc[nb][2] + bias), gelu_tanh(bfhi(uv.y)) * (acc[nb][3] + bias));
;           *(u32x2*)(CAT + (size_t)(row0 + pp) * DM + h * 128 + c) = w; } }
	v_mfma_f32_16x16x32_bf16 v[6:9], v[6:9], v[38:41], v[50:53]
	s_nop 2
	v_add_u32_e32 v50, s12, v36
	v_mov_b64_e32 v[36:37], s[38:39]
	v_mad_i64_i32 v[36:37], s[0:1], v50, s0, v[36:37]
	v_readlane_b32 s0, v253, 39
	s_lshl_b32 s0, s0, 1
	s_mov_b32 s1, s5
	v_lshl_add_u64 v[36:37], v[36:37], 0, s[0:1]
	v_lshl_add_u64 v[36:37], v[36:37], 0, v[206:207]
	v_mfma_f32_16x16x32_bf16 v[2:5], v[42:45], v[38:41], v[2:5]
	global_load_dword v34, v[34:35], off
	s_nop 0
	global_load_dwordx2 v[52:53], v[36:37], off
	global_load_dwordx2 v[48:49], v[36:37], off offset:32
	global_load_dwordx2 v[46:47], v[36:37], off offset:64
	global_load_dwordx2 v[44:45], v[36:37], off offset:96
	global_load_dwordx2 v[42:43], v[36:37], off offset:128
	global_load_dwordx2 v[40:41], v[36:37], off offset:160
	global_load_dwordx2 v[38:39], v[36:37], off offset:192
	s_nop 0
	global_load_dwordx2 v[36:37], v[36:37], off offset:224
	v_ashrrev_i32_e32 v51, 31, v50
	v_lshlrev_b64 v[50:51], 12, v[50:51]
	v_lshl_add_u64 v[50:51], s[36:37], 0, v[50:51]
	v_lshl_add_u64 v[50:51], v[50:51], 0, s[0:1]
	s_mov_b64 s[0:1], 0x2d1b8000
	s_waitcnt vmcnt(7)
	v_lshlrev_b32_e32 v54, 16, v52
	v_mul_f32_e32 v35, 0x3dd2d3e8, v54
	v_fma_f32 v35, -v35, v54, s33
	v_mul_f32_e32 v35, v35, v54
	v_exp_f32_e32 v35, v35
	v_and_b32_e32 v55, 0xffff0000, v52
	v_add_f32_e32 v35, 1.0, v35
	v_rcp_f32_e32 v56, v35
	v_mul_f32_e32 v35, 0x3dd2d3e8, v55
	v_fma_f32 v35, -v35, v55, s33
	v_mul_f32_e32 v35, v35, v55
	v_exp_f32_e32 v35, v35
	s_nop 0
	v_add_f32_e32 v35, 1.0, v35
	v_rcp_f32_e32 v57, v35
	v_pk_add_f32 v[30:31], v[30:31], v[34:35] op_sel_hi:[1,0]
	v_pk_mul_f32 v[54:55], v[56:57], v[54:55]
	s_nop 0
	v_pk_mul_f32 v[30:31], v[30:31], v[54:55]
	s_nop 0
	v_cvt_pk_bf16_f32 v52, v30, v31
	v_lshlrev_b32_e32 v30, 16, v53
	v_mul_f32_e32 v35, 0x3dd2d3e8, v30
	v_fma_f32 v35, -v35, v30, s33
	v_mul_f32_e32 v35, v35, v30
	v_exp_f32_e32 v35, v35
	v_and_b32_e32 v31, 0xffff0000, v53
	v_add_f32_e32 v35, 1.0, v35
	v_rcp_f32_e32 v54, v35
	v_mul_f32_e32 v35, 0x3dd2d3e8, v31
	v_fma_f32 v35, -v35, v31, s33
	v_mul_f32_e32 v35, v35, v31
	v_exp_f32_e32 v35, v35
	s_nop 0
	v_add_f32_e32 v35, 1.0, v35
	v_rcp_f32_e32 v55, v35
	v_pk_add_f32 v[32:33], v[32:33], v[34:35] op_sel_hi:[1,0]
	v_pk_mul_f32 v[30:31], v[54:55], v[30:31]
	s_nop 0
	v_pk_mul_f32 v[30:31], v[32:33], v[30:31]
	v_lshl_add_u64 v[32:33], v[50:51], 0, v[206:207]
	v_cvt_pk_bf16_f32 v53, v30, v31
	v_lshl_add_u64 v[30:31], v[32:33], 0, s[0:1]
	s_mov_b32 s0, 0x2d1b8000
	v_add_co_u32_e32 v32, vcc, s0, v32
	s_nop 1
	v_addc_co_u32_e32 v33, vcc, 0, v33, vcc
	global_store_dwordx2 v[32:33], v[52:53], off
	s_waitcnt vmcnt(7)
	v_lshlrev_b32_e32 v32, 16, v48
	v_mul_f32_e32 v35, 0x3dd2d3e8, v32
	v_fma_f32 v35, -v35, v32, s33
	v_mul_f32_e32 v35, v35, v32
	v_exp_f32_e32 v35, v35
	v_and_b32_e32 v33, 0xffff0000, v48
	v_add_f32_e32 v35, 1.0, v35
	v_rcp_f32_e32 v50, v35
	v_mul_f32_e32 v35, 0x3dd2d3e8, v33
	v_fma_f32 v35, -v35, v33, s33
	v_mul_f32_e32 v35, v35, v33
	v_exp_f32_e32 v35, v35
	s_nop 0
	v_add_f32_e32 v35, 1.0, v35
	v_rcp_f32_e32 v51, v35
	v_pk_add_f32 v[26:27], v[26:27], v[34:35] op_sel_hi:[1,0]
	v_pk_add_f32 v[28:29], v[28:29], v[34:35] op_sel_hi:[1,0]
	v_pk_add_f32 v[22:23], v[22:23], v[34:35] op_sel_hi:[1,0]
	v_pk_mul_f32 v[32:33], v[50:51], v[32:33]
	v_pk_add_f32 v[24:25], v[24:25], v[34:35] op_sel_hi:[1,0]
	v_pk_mul_f32 v[26:27], v[26:27], v[32:33]
	v_lshlrev_b32_e32 v32, 16, v49
	v_cvt_pk_bf16_f32 v26, v26, v27
	v_mul_f32_e32 v27, 0x3dd2d3e8, v32
	v_fma_f32 v27, -v27, v32, s33
	v_mul_f32_e32 v27, v27, v32
	v_exp_f32_e32 v27, v27
	v_and_b32_e32 v33, 0xffff0000, v49
	v_pk_add_f32 v[18:19], v[18:19], v[34:35] op_sel_hi:[1,0]
	v_pk_add_f32 v[20:21], v[20:21], v[34:35] op_sel_hi:[1,0]
	v_add_f32_e32 v27, 1.0, v27
	v_rcp_f32_e32 v48, v27
	v_mul_f32_e32 v27, 0x3dd2d3e8, v33
	v_fma_f32 v27, -v27, v33, s33
	v_mul_f32_e32 v27, v27, v33
	v_exp_f32_e32 v27, v27
	v_pk_add_f32 v[14:15], v[14:15], v[34:35] op_sel_hi:[1,0]
	v_pk_add_f32 v[16:17], v[16:17], v[34:35] op_sel_hi:[1,0]
	v_pk_add_f32 v[10:11], v[10:11], v[34:35] op_sel_hi:[1,0]
	v_add_f32_e32 v27, 1.0, v27
	v_rcp_f32_e32 v49, v27
	v_pk_add_f32 v[12:13], v[12:13], v[34:35] op_sel_hi:[1,0]
	v_pk_add_f32 v[6:7], v[6:7], v[34:35] op_sel_hi:[1,0]
	v_pk_add_f32 v[8:9], v[8:9], v[34:35] op_sel_hi:[1,0]
	v_pk_mul_f32 v[32:33], v[48:49], v[32:33]
	v_pk_add_f32 v[2:3], v[34:35], v[2:3] op_sel_hi:[0,1]
	v_pk_mul_f32 v[28:29], v[28:29], v[32:33]
	v_pk_add_f32 v[4:5], v[34:35], v[4:5] op_sel_hi:[0,1]
	v_cvt_pk_bf16_f32 v27, v28, v29
	global_store_dwordx2 v[30:31], v[26:27], off offset:32
	s_waitcnt vmcnt(7)
	v_lshlrev_b32_e32 v26, 16, v46
	v_and_b32_e32 v27, 0xffff0000, v46
	v_mul_f32_e32 v28, 0x3dd2d3e8, v26
	v_mul_f32_e32 v29, 0x3dd2d3e8, v27
	v_fma_f32 v28, -v28, v26, s33
	v_fma_f32 v29, -v29, v27, s33
	v_mul_f32_e32 v28, v28, v26
	v_mul_f32_e32 v29, v29, v27
	v_exp_f32_e32 v28, v28
	v_exp_f32_e32 v29, v29
	v_add_f32_e32 v28, 1.0, v28
	v_add_f32_e32 v29, 1.0, v29
	v_rcp_f32_e32 v28, v28
	v_rcp_f32_e32 v29, v29
	s_nop 0
	v_pk_mul_f32 v[26:27], v[28:29], v[26:27]
	s_nop 0
	v_pk_mul_f32 v[22:23], v[22:23], v[26:27]
	v_lshlrev_b32_e32 v26, 16, v47
	v_cvt_pk_bf16_f32 v22, v22, v23
	v_mul_f32_e32 v23, 0x3dd2d3e8, v26
	v_fma_f32 v23, -v23, v26, s33
	v_mul_f32_e32 v23, v23, v26
	v_exp_f32_e32 v23, v23
	v_and_b32_e32 v27, 0xffff0000, v47
	v_add_f32_e32 v23, 1.0, v23
	v_rcp_f32_e32 v28, v23
	v_mul_f32_e32 v23, 0x3dd2d3e8, v27
	v_fma_f32 v23, -v23, v27, s33
	v_mul_f32_e32 v23, v23, v27
	v_exp_f32_e32 v23, v23
	s_nop 0
	v_add_f32_e32 v23, 1.0, v23
	v_rcp_f32_e32 v29, v23
	s_nop 0
	v_pk_mul_f32 v[26:27], v[28:29], v[26:27]
	s_nop 0
	v_pk_mul_f32 v[24:25], v[24:25], v[26:27]
	s_nop 0
	v_cvt_pk_bf16_f32 v23, v24, v25
	global_store_dwordx2 v[30:31], v[22:23], off offset:64
	s_waitcnt vmcnt(7)
; __device__ __forceinline__ unsigned cvt_pk_bf16(float lo, float hi) { const f32x2 v = {lo, hi}; const bf16x2_t b = __builtin_convertvector(v, bf16x2_t); return __builtin_bit_cast(unsigned, b); }
; __device__ __forceinline__ float bflo(unsigned w) { return __uint_as_float(w << 16); }
; __device__ __forceinline__ float bfhi(unsigned w) { return __uint_as_float(w & 0xffff0000u); }
; __device__ __forceinline__ void sgu_unit(const Params& p, int l, int un, LAS unsigned char* lds) {
;     ...
;       for (int nb = 0; nb < 8; ++nb) { const int c = nb * 16 + 4 * fq; const u32x2 uv = uq[nb];
;           u32x2 w; w.x = cvt_pk_bf16(gelu_tanh(bflo(uv.x)) * (acc[nb][0] + bias), gelu_tanh(bfhi(uv.x)) * (acc[nb][1] + bias));
;           w.y = cvt_pk_bf16(gelu_tanh(bflo(uv.y)) * (acc[nb][2] + bias), gelu_tanh(bfhi(uv.y)) * (acc[nb][3] + bias));
;           *(u32x2*)(CAT + (size_t)(row0 + pp) * DM + h * 128 + c) = w; } }
;     __syncthreads();
	v_lshlrev_b32_e32 v22, 16, v44
	v_and_b32_e32 v23, 0xffff0000, v44
	v_mul_f32_e32 v24, 0x3dd2d3e8, v22
	v_mul_f32_e32 v25, 0x3dd2d3e8, v23
	v_fma_f32 v24, -v24, v22, s33
	v_fma_f32 v25, -v25, v23, s33
	v_mul_f32_e32 v24, v24, v22
	v_mul_f32_e32 v25, v25, v23
	v_exp_f32_e32 v24, v24
	v_exp_f32_e32 v25, v25
	v_add_f32_e32 v24, 1.0, v24
	v_add_f32_e32 v25, 1.0, v25
	v_rcp_f32_e32 v24, v24
	v_rcp_f32_e32 v25, v25
	s_nop 0
	v_pk_mul_f32 v[22:23], v[24:25], v[22:23]
	s_nop 0
	v_pk_mul_f32 v[18:19], v[18:19], v[22:23]
	v_lshlrev_b32_e32 v22, 16, v45
	v_cvt_pk_bf16_f32 v18, v18, v19
	v_mul_f32_e32 v19, 0x3dd2d3e8, v22
	v_fma_f32 v19, -v19, v22, s33
	v_mul_f32_e32 v19, v19, v22
	v_exp_f32_e32 v19, v19
	v_and_b32_e32 v23, 0xffff0000, v45
	v_add_f32_e32 v19, 1.0, v19
	v_rcp_f32_e32 v24, v19
	v_mul_f32_e32 v19, 0x3dd2d3e8, v23
	v_fma_f32 v19, -v19, v23, s33
	v_mul_f32_e32 v19, v19, v23
	v_exp_f32_e32 v19, v19
	s_nop 0
	v_add_f32_e32 v19, 1.0, v19
	v_rcp_f32_e32 v25, v19
	s_nop 0
	v_pk_mul_f32 v[22:23], v[24:25], v[22:23]
	s_nop 0
	v_pk_mul_f32 v[20:21], v[20:21], v[22:23]
	s_nop 0
	v_cvt_pk_bf16_f32 v19, v20, v21
	global_store_dwordx2 v[30:31], v[18:19], off offset:96
	s_waitcnt vmcnt(7)
	v_lshlrev_b32_e32 v18, 16, v42
	v_and_b32_e32 v19, 0xffff0000, v42
	v_mul_f32_e32 v20, 0x3dd2d3e8, v18
	v_mul_f32_e32 v21, 0x3dd2d3e8, v19
	v_fma_f32 v20, -v20, v18, s33
	v_fma_f32 v21, -v21, v19, s33
	v_mul_f32_e32 v20, v20, v18
	v_mul_f32_e32 v21, v21, v19
	v_exp_f32_e32 v20, v20
	v_exp_f32_e32 v21, v21
	v_add_f32_e32 v20, 1.0, v20
	v_add_f32_e32 v21, 1.0, v21
	v_rcp_f32_e32 v20, v20
	v_rcp_f32_e32 v21, v21
	s_nop 0
	v_pk_mul_f32 v[18:19], v[20:21], v[18:19]
	s_nop 0
	v_pk_mul_f32 v[14:15], v[14:15], v[18:19]
	v_lshlrev_b32_e32 v18, 16, v43
	v_cvt_pk_bf16_f32 v14, v14, v15
	v_mul_f32_e32 v15, 0x3dd2d3e8, v18
	v_fma_f32 v15, -v15, v18, s33
	v_mul_f32_e32 v15, v15, v18
	v_exp_f32_e32 v15, v15
	v_and_b32_e32 v19, 0xffff0000, v43
	v_add_f32_e32 v15, 1.0, v15
	v_rcp_f32_e32 v20, v15
	v_mul_f32_e32 v15, 0x3dd2d3e8, v19
	v_fma_f32 v15, -v15, v19, s33
	v_mul_f32_e32 v15, v15, v19
	v_exp_f32_e32 v15, v15
	s_nop 0
	v_add_f32_e32 v15, 1.0, v15
	v_rcp_f32_e32 v21, v15
	s_nop 0
	v_pk_mul_f32 v[18:19], v[20:21], v[18:19]
	s_nop 0
	v_pk_mul_f32 v[16:17], v[16:17], v[18:19]
	s_nop 0
	v_cvt_pk_bf16_f32 v15, v16, v17
	global_store_dwordx2 v[30:31], v[14:15], off offset:128
	s_waitcnt vmcnt(7)
	v_lshlrev_b32_e32 v14, 16, v40
	v_and_b32_e32 v15, 0xffff0000, v40
	v_mul_f32_e32 v16, 0x3dd2d3e8, v14
	v_mul_f32_e32 v17, 0x3dd2d3e8, v15
	v_fma_f32 v16, -v16, v14, s33
	v_fma_f32 v17, -v17, v15, s33
	v_mul_f32_e32 v16, v16, v14
	v_mul_f32_e32 v17, v17, v15
	v_exp_f32_e32 v16, v16
	v_exp_f32_e32 v17, v17
	v_add_f32_e32 v16, 1.0, v16
	v_add_f32_e32 v17, 1.0, v17
	v_rcp_f32_e32 v16, v16
	v_rcp_f32_e32 v17, v17
	s_nop 0
	v_pk_mul_f32 v[14:15], v[16:17], v[14:15]
	s_nop 0
	v_pk_mul_f32 v[10:11], v[10:11], v[14:15]
	v_lshlrev_b32_e32 v14, 16, v41
	v_cvt_pk_bf16_f32 v10, v10, v11
	v_mul_f32_e32 v11, 0x3dd2d3e8, v14
	v_fma_f32 v11, -v11, v14, s33
	v_mul_f32_e32 v11, v11, v14
	v_exp_f32_e32 v11, v11
	v_and_b32_e32 v15, 0xffff0000, v41
	v_add_f32_e32 v11, 1.0, v11
	v_rcp_f32_e32 v16, v11
	v_mul_f32_e32 v11, 0x3dd2d3e8, v15
	v_fma_f32 v11, -v11, v15, s33
	v_mul_f32_e32 v11, v11, v15
	v_exp_f32_e32 v11, v11
	s_nop 0
	v_add_f32_e32 v11, 1.0, v11
	v_rcp_f32_e32 v17, v11
	s_nop 0
	v_pk_mul_f32 v[14:15], v[16:17], v[14:15]
	s_nop 0
	v_pk_mul_f32 v[12:13], v[12:13], v[14:15]
	s_nop 0
	v_cvt_pk_bf16_f32 v11, v12, v13
	global_store_dwordx2 v[30:31], v[10:11], off offset:160
	s_waitcnt vmcnt(7)
	v_lshlrev_b32_e32 v10, 16, v38
	v_and_b32_e32 v11, 0xffff0000, v38
	v_mul_f32_e32 v12, 0x3dd2d3e8, v10
	v_mul_f32_e32 v13, 0x3dd2d3e8, v11
	v_fma_f32 v12, -v12, v10, s33
	v_fma_f32 v13, -v13, v11, s33
	v_mul_f32_e32 v12, v12, v10
	v_mul_f32_e32 v13, v13, v11
	v_exp_f32_e32 v12, v12
	v_exp_f32_e32 v13, v13
	v_add_f32_e32 v12, 1.0, v12
	v_add_f32_e32 v13, 1.0, v13
	v_rcp_f32_e32 v12, v12
	v_rcp_f32_e32 v13, v13
	s_nop 0
	v_pk_mul_f32 v[10:11], v[12:13], v[10:11]
	s_nop 0
	v_pk_mul_f32 v[6:7], v[6:7], v[10:11]
	v_lshlrev_b32_e32 v10, 16, v39
	v_cvt_pk_bf16_f32 v6, v6, v7
	v_mul_f32_e32 v7, 0x3dd2d3e8, v10
	v_fma_f32 v7, -v7, v10, s33
	v_mul_f32_e32 v7, v7, v10
	v_exp_f32_e32 v7, v7
	v_and_b32_e32 v11, 0xffff0000, v39
	v_add_f32_e32 v7, 1.0, v7
	v_rcp_f32_e32 v12, v7
	v_mul_f32_e32 v7, 0x3dd2d3e8, v11
	v_fma_f32 v7, -v7, v11, s33
	v_mul_f32_e32 v7, v7, v11
	v_exp_f32_e32 v7, v7
	s_nop 0
	v_add_f32_e32 v7, 1.0, v7
	v_rcp_f32_e32 v13, v7
	s_nop 0
	v_pk_mul_f32 v[10:11], v[12:13], v[10:11]
	s_nop 0
	v_pk_mul_f32 v[8:9], v[8:9], v[10:11]
	s_nop 0
	v_cvt_pk_bf16_f32 v7, v8, v9
	global_store_dwordx2 v[30:31], v[6:7], off offset:192
	s_waitcnt vmcnt(7)
	v_lshlrev_b32_e32 v6, 16, v36
	v_and_b32_e32 v7, 0xffff0000, v36
	v_mul_f32_e32 v8, 0x3dd2d3e8, v6
	v_mul_f32_e32 v9, 0x3dd2d3e8, v7
	v_fma_f32 v8, -v8, v6, s33
	v_fma_f32 v9, -v9, v7, s33
	v_mul_f32_e32 v8, v8, v6
	v_mul_f32_e32 v9, v9, v7
	v_exp_f32_e32 v8, v8
	v_exp_f32_e32 v9, v9
	v_add_f32_e32 v8, 1.0, v8
	v_add_f32_e32 v9, 1.0, v9
	v_rcp_f32_e32 v8, v8
	v_rcp_f32_e32 v9, v9
	s_nop 0
	v_pk_mul_f32 v[6:7], v[8:9], v[6:7]
	s_nop 0
	v_pk_mul_f32 v[2:3], v[2:3], v[6:7]
	v_lshlrev_b32_e32 v6, 16, v37
	v_cvt_pk_bf16_f32 v2, v2, v3
	v_mul_f32_e32 v3, 0x3dd2d3e8, v6
	v_fma_f32 v3, -v3, v6, s33
	v_mul_f32_e32 v3, v3, v6
	v_exp_f32_e32 v3, v3
	v_and_b32_e32 v7, 0xffff0000, v37
	v_add_f32_e32 v3, 1.0, v3
	v_rcp_f32_e32 v8, v3
	v_mul_f32_e32 v3, 0x3dd2d3e8, v7
	v_fma_f32 v3, -v3, v7, s33
	v_mul_f32_e32 v3, v3, v7
	v_exp_f32_e32 v3, v3
	s_nop 0
	v_add_f32_e32 v3, 1.0, v3
	v_rcp_f32_e32 v9, v3
	s_nop 0
	v_pk_mul_f32 v[6:7], v[8:9], v[6:7]
	s_nop 0
	v_pk_mul_f32 v[4:5], v[4:5], v[6:7]
	s_nop 0
	v_cvt_pk_bf16_f32 v3, v4, v5
	global_store_dwordx2 v[30:31], v[2:3], off offset:224
	s_barrier
